# v37 + peeled first K-tile pair per unit with SrcC=0 first-touch MFMAs (no accumulator zeroing pass)
# speedup vs baseline: 1.0391x; 1.0018x over previous
; #define G_ENDTILE(VM) do { asm volatile("s_waitcnt vmcnt(" #VM ")" ::: "memory"); \
;         asm volatile("s_waitcnt lgkmcnt(0)" ::: "memory"); __builtin_amdgcn_s_barrier(); asm volatile("" ::: "memory"); } while (0)
;     ...
;     for (int ui = 0;; ++ui) {
; #pragma unroll
;         for (int m = 0; m < MF; ++m)
; #pragma unroll
;             for (int n = 0; n < 4; ++n) acc[m][n] = (f32x4){0.f, 0.f, 0.f, 0.f};
;         for (int t = 0; t < nt - 2; t += 2) {
;             G_TILE(G_A0, G_B0, true, G_B1, G_A1, t + 1, true, t + 2, (void)0);
;             G_ENDTILE(8);
;             G_TILE(G_A1, G_B1, true, G_B0, G_A0, t + 2, true, t + 3, (void)0);
;             G_ENDTILE(8);
.LBB0_69:
	s_andn2_b64 vcc, exec, s[30:31]
	v_mov_b32_e32 v159, 0
	s_cbranch_vccnz .LBB0_72
	s_mov_b32 s8, 0
	s_mov_b32 s9, 0x5a0000
	s_movk_i32 s24, 0x100
	s_mov_b32 m0, s68
	s_add_i32 s25, s24, 0xffffff80
	ds_read_b64_tr_b16 v[170:171], v166
	ds_read_b64_tr_b16 v[172:173], v167
	ds_read_b64_tr_b16 v[176:177], v167 offset:32
	ds_read_b128 v[178:181], v162
	ds_read_b64_tr_b16 v[174:175], v166 offset:32
	ds_read_b64_tr_b16 v[182:183], v166 offset:64
	ds_read_b64_tr_b16 v[186:187], v166 offset:96
	ds_read_b64_tr_b16 v[184:185], v167 offset:64
	ds_read_b64_tr_b16 v[188:189], v167 offset:96
	ds_read_b128 v[190:193], v162 offset:2048
	ds_read_b128 v[194:197], v162 offset:4096
	buffer_load_dwordx4 v163, s[20:23], s25 offen lds
	s_mov_b32 m0, s67
	s_waitcnt lgkmcnt(7)
	v_mfma_f32_16x16x32_bf16 v[156:159], v[170:173], v[178:181], 0
	buffer_load_dwordx4 v165, s[20:23], s25 offen lds
	s_waitcnt lgkmcnt(6)
	v_mfma_f32_16x16x32_bf16 v[152:155], v[174:177], v[178:181], 0
	s_waitcnt lgkmcnt(3)
	v_mfma_f32_16x16x32_bf16 v[148:151], v[182:185], v[178:181], 0
	s_waitcnt lgkmcnt(2)
	v_mfma_f32_16x16x32_bf16 v[144:147], v[186:189], v[178:181], 0
	s_waitcnt lgkmcnt(1)
	v_mfma_f32_16x16x32_bf16 v[140:143], v[170:173], v[190:193], 0
	s_mov_b32 m0, s66
	s_nop 0
	buffer_load_dwordx4 v164, s[20:23], s25 offen lds
	ds_read_b128 v[178:181], v162 offset:6144
	s_waitcnt vmcnt(10)
	v_cvt_pk_bf16_f32 v15, v14, v15
	v_cvt_pk_bf16_f32 v14, v12, v13
	v_mfma_f32_16x16x32_bf16 v[136:139], v[174:177], v[190:193], 0
	ds_write_b64 v161, v[14:15] offset:34816
	v_mfma_f32_16x16x32_bf16 v[132:135], v[182:185], v[190:193], 0
	s_mov_b32 m0, s65
	s_nop 0
	buffer_load_dwordx4 v168, s[20:23], s25 offen lds
	s_add_i32 s25, s9, 0xffd60000
	v_mfma_f32_16x16x32_bf16 v[128:131], v[186:189], v[190:193], 0
	s_waitcnt lgkmcnt(2)
	v_mfma_f32_16x16x32_bf16 v[124:127], v[170:173], v[194:197], 0
	ds_read_b128 v[190:193], v162 offset:8192
	v_mfma_f32_16x16x32_bf16 v[120:123], v[174:177], v[194:197], 0
	v_mfma_f32_16x16x32_bf16 v[116:119], v[182:185], v[194:197], 0
	v_mfma_f32_16x16x32_bf16 v[112:115], v[186:189], v[194:197], 0
	s_waitcnt lgkmcnt(2)
	v_mfma_f32_16x16x32_bf16 v[108:111], v[170:173], v[178:181], 0
	ds_read_b128 v[194:197], v162 offset:10240
	buffer_load_dwordx4 v[12:15], v160, s[12:15], s25 offen
	s_waitcnt vmcnt(11)
	v_cvt_pk_bf16_f32 v3, v2, v3
	v_cvt_pk_bf16_f32 v2, v0, v1
	v_mfma_f32_16x16x32_bf16 v[104:107], v[174:177], v[178:181], 0
	ds_write_b64 v161, v[2:3] offset:43520
	v_mfma_f32_16x16x32_bf16 v[100:103], v[182:185], v[178:181], 0
	v_mfma_f32_16x16x32_bf16 v[96:99], v[186:189], v[178:181], 0
	s_add_i32 s26, s9, 0xffdc0000
	s_waitcnt lgkmcnt(2)
	v_mfma_f32_16x16x32_bf16 v[92:95], v[170:173], v[190:193], 0
	ds_read_b128 v[178:181], v162 offset:12288
	v_mfma_f32_16x16x32_bf16 v[88:91], v[174:177], v[190:193], 0
	v_mfma_f32_16x16x32_bf16 v[84:87], v[182:185], v[190:193], 0
	v_mfma_f32_16x16x32_bf16 v[80:83], v[186:189], v[190:193], 0
	s_waitcnt lgkmcnt(2)
	v_mfma_f32_16x16x32_bf16 v[76:79], v[170:173], v[194:197], 0
	ds_read_b128 v[190:193], v162 offset:14336
	buffer_load_dwordx4 v[0:3], v160, s[12:15], s26 offen
	s_waitcnt vmcnt(11)
	v_cvt_pk_bf16_f32 v31, v30, v31
	v_cvt_pk_bf16_f32 v30, v28, v29
	v_mfma_f32_16x16x32_bf16 v[72:75], v[174:177], v[194:197], 0
	ds_write_b64 v161, v[30:31] offset:52224
	v_mfma_f32_16x16x32_bf16 v[68:71], v[182:185], v[194:197], 0
	v_mfma_f32_16x16x32_bf16 v[64:67], v[186:189], v[194:197], 0
	s_add_i32 s27, s9, 0xffe20000
	s_waitcnt lgkmcnt(2)
	v_mfma_f32_16x16x32_bf16 v[60:63], v[170:173], v[178:181], 0
	ds_read_b128 v[194:197], v162 offset:1024
	v_mfma_f32_16x16x32_bf16 v[56:59], v[174:177], v[178:181], 0
	v_mfma_f32_16x16x32_bf16 v[52:55], v[182:185], v[178:181], 0
	v_mfma_f32_16x16x32_bf16 v[48:51], v[186:189], v[178:181], 0
	s_waitcnt lgkmcnt(2)
	v_mfma_f32_16x16x32_bf16 v[44:47], v[170:173], v[190:193], 0
	ds_read_b128 v[170:173], v162 offset:3072
	buffer_load_dwordx4 v[28:31], v160, s[12:15], s27 offen
	s_waitcnt vmcnt(11)
	v_cvt_pk_bf16_f32 v27, v26, v27
	v_cvt_pk_bf16_f32 v26, v24, v25
	v_mfma_f32_16x16x32_bf16 v[40:43], v[174:177], v[190:193], 0
	ds_read_b64_tr_b16 v[244:245], v166 offset:17408
	ds_read_b64_tr_b16 v[248:249], v166 offset:17440
	ds_read_b64_tr_b16 v[198:199], v166 offset:17472
	ds_read_b64_tr_b16 v[202:203], v166 offset:17504
	ds_read_b64_tr_b16 v[246:247], v167 offset:17408
	ds_read_b64_tr_b16 v[250:251], v167 offset:17440
	ds_read_b64_tr_b16 v[200:201], v167 offset:17472
	ds_read_b64_tr_b16 v[204:205], v167 offset:17504
	ds_write_b64 v161, v[26:27] offset:60928
	v_mfma_f32_16x16x32_bf16 v[36:39], v[182:185], v[190:193], 0
	v_mfma_f32_16x16x32_bf16 v[32:35], v[186:189], v[190:193], 0
	s_add_i32 s42, s9, 0xffe80000
	s_waitcnt lgkmcnt(4)
	v_mfma_f32_16x16x32_bf16 v[156:159], v[244:247], v[194:197], v[156:159]
	ds_read_b128 v[182:185], v162 offset:5120
	s_waitcnt lgkmcnt(4)
	v_mfma_f32_16x16x32_bf16 v[152:155], v[248:251], v[194:197], v[152:155]
	s_waitcnt lgkmcnt(3)
	v_mfma_f32_16x16x32_bf16 v[148:151], v[198:201], v[194:197], v[148:151]
	s_waitcnt lgkmcnt(2)
	v_mfma_f32_16x16x32_bf16 v[144:147], v[202:205], v[194:197], v[144:147]
	v_mfma_f32_16x16x32_bf16 v[140:143], v[244:247], v[170:173], v[140:143]
	ds_read_b128 v[186:189], v162 offset:7168
	buffer_load_dwordx4 v[24:27], v160, s[12:15], s42 offen
	s_waitcnt vmcnt(11)
	v_cvt_pk_bf16_f32 v23, v22, v23
	v_cvt_pk_bf16_f32 v22, v20, v21
	v_mfma_f32_16x16x32_bf16 v[136:139], v[248:251], v[170:173], v[136:139]
	ds_write_b64 v161, v[22:23] offset:35072
	v_mfma_f32_16x16x32_bf16 v[132:135], v[198:201], v[170:173], v[132:135]
	v_mfma_f32_16x16x32_bf16 v[128:131], v[202:205], v[170:173], v[128:131]
	s_waitcnt lgkmcnt(2)
; #define G_DMA_A(kt, AO) do { G_DMA1(kt, AO, 0); G_DMA1(kt, AO, 1); G_DMA1(kt, AO, 2); G_DMA1(kt, AO, 3); if (MF == 9) G_DMA5(kt, AO); } while (0)
; #define G_ISSUE_B(kt) do { const unsigned _sb = (unsigned)(kt) * 4u * kstepB; \
;         _Pragma("unroll") for (int _i = 0; _i < 8; ++_i) sb[_i] = bload16(_i < 4 ? rsB0 : rsB1, vob, _sb + (_i & 3) * kstepB); } while (0)
; #define G_WRITE_B(BO) do { \
;         _Pragma("unroll") for (int _i = 0; _i < 8; ++_i) *(LAS u32x2*)(b_wr + (BO) + (_i & 3) * (16 * G_BSTRIDE) + (_i >> 2) * SLAB1) = pack4(__builtin_bit_cast(f32x4, sb[_i])); } while (0)
; #define G_ENDTILE(VM) do { asm volatile("s_waitcnt vmcnt(" #VM ")" ::: "memory"); \
;         asm volatile("s_waitcnt lgkmcnt(0)" ::: "memory"); __builtin_amdgcn_s_barrier(); asm volatile("" ::: "memory"); } while (0)
;     ...
;     __builtin_amdgcn_s_barrier();
;     G_DMA_A(0, G_A0); G_ISSUE_B(0); G_WRITE_B(G_B0);
;     __builtin_amdgcn_sched_barrier(0);
;     G_ISSUE_B(1);
;     __builtin_amdgcn_sched_barrier(0);
;     G_ENDTILE(8);
;     for (int ui = 0;; ++ui) {
; #pragma unroll
;         for (int m = 0; m < MF; ++m)
; #pragma unroll
;             for (int n = 0; n < 4; ++n) acc[m][n] = (f32x4){0.f, 0.f, 0.f, 0.f};
;         for (int t = 0; t < nt - 2; t += 2) {
;             G_TILE(G_A0, G_B0, true, G_B1, G_A1, t + 1, true, t + 2, (void)0);
;             G_ENDTILE(8);
;             G_TILE(G_A1, G_B1, true, G_B0, G_A0, t + 2, true, t + 3, (void)0);
;             G_ENDTILE(8);
	v_mfma_f32_16x16x32_bf16 v[124:127], v[244:247], v[182:185], v[124:127]
	ds_read_b128 v[170:173], v162 offset:9216
	v_mfma_f32_16x16x32_bf16 v[120:123], v[248:251], v[182:185], v[120:123]
	v_mfma_f32_16x16x32_bf16 v[116:119], v[198:201], v[182:185], v[116:119]
	v_mfma_f32_16x16x32_bf16 v[112:115], v[202:205], v[182:185], v[112:115]
	s_waitcnt lgkmcnt(2)
	v_mfma_f32_16x16x32_bf16 v[108:111], v[244:247], v[186:189], v[108:111]
	ds_read_b128 v[182:185], v162 offset:11264
	buffer_load_dwordx4 v[20:23], v160, s[16:19], s25 offen
	s_waitcnt vmcnt(11)
	v_cvt_pk_bf16_f32 v7, v6, v7
	v_cvt_pk_bf16_f32 v6, v4, v5
	v_mfma_f32_16x16x32_bf16 v[104:107], v[248:251], v[186:189], v[104:107]
	ds_write_b64 v161, v[6:7] offset:43776
	v_mfma_f32_16x16x32_bf16 v[100:103], v[198:201], v[186:189], v[100:103]
	v_mfma_f32_16x16x32_bf16 v[96:99], v[202:205], v[186:189], v[96:99]
	s_waitcnt lgkmcnt(2)
	v_mfma_f32_16x16x32_bf16 v[92:95], v[244:247], v[170:173], v[92:95]
	ds_read_b128 v[186:189], v162 offset:13312
	v_mfma_f32_16x16x32_bf16 v[88:91], v[248:251], v[170:173], v[88:91]
	v_mfma_f32_16x16x32_bf16 v[84:87], v[198:201], v[170:173], v[84:87]
	v_mfma_f32_16x16x32_bf16 v[80:83], v[202:205], v[170:173], v[80:83]
	s_waitcnt lgkmcnt(2)
	v_mfma_f32_16x16x32_bf16 v[76:79], v[244:247], v[182:185], v[76:79]
	ds_read_b128 v[252:255], v162 offset:15360
	buffer_load_dwordx4 v[4:7], v160, s[16:19], s26 offen
	s_waitcnt vmcnt(11)
	v_cvt_pk_bf16_f32 v11, v10, v11
	v_cvt_pk_bf16_f32 v10, v8, v9
	v_mfma_f32_16x16x32_bf16 v[72:75], v[248:251], v[182:185], v[72:75]
	ds_write_b64 v161, v[10:11] offset:52480
	v_mfma_f32_16x16x32_bf16 v[68:71], v[198:201], v[182:185], v[68:71]
	v_mfma_f32_16x16x32_bf16 v[64:67], v[202:205], v[182:185], v[64:67]
	s_waitcnt lgkmcnt(2)
	v_mfma_f32_16x16x32_bf16 v[60:63], v[244:247], v[186:189], v[60:63]
	buffer_load_dwordx4 v[8:11], v160, s[16:19], s27 offen
	s_waitcnt vmcnt(11)
	v_cvt_pk_bf16_f32 v19, v18, v19
	v_cvt_pk_bf16_f32 v18, v16, v17
	v_mfma_f32_16x16x32_bf16 v[56:59], v[248:251], v[186:189], v[56:59]
	ds_write_b64 v161, v[18:19] offset:61184
	v_mfma_f32_16x16x32_bf16 v[52:55], v[198:201], v[186:189], v[52:55]
	buffer_load_dwordx4 v[16:19], v160, s[16:19], s42 offen
	v_mfma_f32_16x16x32_bf16 v[48:51], v[202:205], v[186:189], v[48:51]
	s_waitcnt vmcnt(8)
	s_mov_b32 m0, s55
	s_waitcnt lgkmcnt(0)
	s_barrier
	ds_read_b64_tr_b16 v[170:171], v166 offset:34816
	ds_read_b64_tr_b16 v[172:173], v167 offset:34816
	ds_read_b64_tr_b16 v[176:177], v167 offset:34848
	ds_read_b128 v[178:181], v162 offset:32768
	ds_read_b64_tr_b16 v[174:175], v166 offset:34848
	ds_read_b64_tr_b16 v[182:183], v166 offset:34880
	ds_read_b64_tr_b16 v[186:187], v166 offset:34912
	ds_read_b64_tr_b16 v[184:185], v167 offset:34880
	ds_read_b64_tr_b16 v[188:189], v167 offset:34912
	ds_read_b128 v[190:193], v162 offset:34816
	ds_read_b128 v[194:197], v162 offset:36864
	buffer_load_dwordx4 v163, s[20:23], s24 offen lds
	s_mov_b32 m0, s56
	v_mfma_f32_16x16x32_bf16 v[44:47], v[244:247], v[252:255], v[44:47]
	v_mfma_f32_16x16x32_bf16 v[40:43], v[248:251], v[252:255], v[40:43]
	v_mfma_f32_16x16x32_bf16 v[36:39], v[198:201], v[252:255], v[36:39]
	v_mfma_f32_16x16x32_bf16 v[32:35], v[202:205], v[252:255], v[32:35]
	s_waitcnt lgkmcnt(7)
	v_mfma_f32_16x16x32_bf16 v[156:159], v[170:173], v[178:181], v[156:159]
	buffer_load_dwordx4 v165, s[20:23], s24 offen lds
	s_add_i32 s25, s9, 0xffee0000
	s_waitcnt lgkmcnt(6)
	v_mfma_f32_16x16x32_bf16 v[152:155], v[174:177], v[178:181], v[152:155]
	s_waitcnt lgkmcnt(3)
	v_mfma_f32_16x16x32_bf16 v[148:151], v[182:185], v[178:181], v[148:151]
	s_waitcnt lgkmcnt(2)
	v_mfma_f32_16x16x32_bf16 v[144:147], v[186:189], v[178:181], v[144:147]
	s_waitcnt lgkmcnt(1)
	v_mfma_f32_16x16x32_bf16 v[140:143], v[170:173], v[190:193], v[140:143]
	s_mov_b32 m0, s57
	s_nop 0
	buffer_load_dwordx4 v164, s[20:23], s24 offen lds
	ds_read_b128 v[178:181], v162 offset:38912
	s_waitcnt vmcnt(10)
	v_cvt_pk_bf16_f32 v15, v14, v15
	v_cvt_pk_bf16_f32 v14, v12, v13
	v_mfma_f32_16x16x32_bf16 v[136:139], v[174:177], v[190:193], v[136:139]
	ds_write_b64 v161, v[14:15]
	v_mfma_f32_16x16x32_bf16 v[132:135], v[182:185], v[190:193], v[132:135]
	s_mov_b32 m0, s59
	s_nop 0
	buffer_load_dwordx4 v168, s[20:23], s24 offen lds
	v_mfma_f32_16x16x32_bf16 v[128:131], v[186:189], v[190:193], v[128:131]
	s_waitcnt lgkmcnt(2)
	v_mfma_f32_16x16x32_bf16 v[124:127], v[170:173], v[194:197], v[124:127]
	ds_read_b128 v[190:193], v162 offset:40960
	v_mfma_f32_16x16x32_bf16 v[120:123], v[174:177], v[194:197], v[120:123]
	v_mfma_f32_16x16x32_bf16 v[116:119], v[182:185], v[194:197], v[116:119]
	v_mfma_f32_16x16x32_bf16 v[112:115], v[186:189], v[194:197], v[112:115]
	s_waitcnt lgkmcnt(2)
	v_mfma_f32_16x16x32_bf16 v[108:111], v[170:173], v[178:181], v[108:111]
	ds_read_b128 v[194:197], v162 offset:43008
	buffer_load_dwordx4 v[12:15], v160, s[12:15], s25 offen
	s_waitcnt vmcnt(11)
	v_cvt_pk_bf16_f32 v3, v2, v3
	v_cvt_pk_bf16_f32 v2, v0, v1
	v_mfma_f32_16x16x32_bf16 v[104:107], v[174:177], v[178:181], v[104:107]
	ds_write_b64 v161, v[2:3] offset:8704
	v_mfma_f32_16x16x32_bf16 v[100:103], v[182:185], v[178:181], v[100:103]
	v_mfma_f32_16x16x32_bf16 v[96:99], v[186:189], v[178:181], v[96:99]
	s_add_i32 s26, s9, 0xfff40000
	s_waitcnt lgkmcnt(2)
; #define G_DMA_A(kt, AO) do { G_DMA1(kt, AO, 0); G_DMA1(kt, AO, 1); G_DMA1(kt, AO, 2); G_DMA1(kt, AO, 3); if (MF == 9) G_DMA5(kt, AO); } while (0)
; #define G_ISSUE_B(kt) do { const unsigned _sb = (unsigned)(kt) * 4u * kstepB; \
;         _Pragma("unroll") for (int _i = 0; _i < 8; ++_i) sb[_i] = bload16(_i < 4 ? rsB0 : rsB1, vob, _sb + (_i & 3) * kstepB); } while (0)
; #define G_WRITE_B(BO) do { \
;         _Pragma("unroll") for (int _i = 0; _i < 8; ++_i) *(LAS u32x2*)(b_wr + (BO) + (_i & 3) * (16 * G_BSTRIDE) + (_i >> 2) * SLAB1) = pack4(__builtin_bit_cast(f32x4, sb[_i])); } while (0)
; #define G_ENDTILE(VM) do { asm volatile("s_waitcnt vmcnt(" #VM ")" ::: "memory"); \
;         asm volatile("s_waitcnt lgkmcnt(0)" ::: "memory"); __builtin_amdgcn_s_barrier(); asm volatile("" ::: "memory"); } while (0)
;     ...
;     __builtin_amdgcn_s_barrier();
;     G_DMA_A(0, G_A0); G_ISSUE_B(0); G_WRITE_B(G_B0);
;     __builtin_amdgcn_sched_barrier(0);
;     G_ISSUE_B(1);
;     __builtin_amdgcn_sched_barrier(0);
;     G_ENDTILE(8);
;     for (int ui = 0;; ++ui) {
; #pragma unroll
;         for (int m = 0; m < MF; ++m)
; #pragma unroll
;             for (int n = 0; n < 4; ++n) acc[m][n] = (f32x4){0.f, 0.f, 0.f, 0.f};
;         for (int t = 0; t < nt - 2; t += 2) {
;             G_TILE(G_A0, G_B0, true, G_B1, G_A1, t + 1, true, t + 2, (void)0);
;             G_ENDTILE(8);
;             G_TILE(G_A1, G_B1, true, G_B0, G_A0, t + 2, true, t + 3, (void)0);
;             G_ENDTILE(8);
;         }
	v_mfma_f32_16x16x32_bf16 v[92:95], v[170:173], v[190:193], v[92:95]
	ds_read_b128 v[178:181], v162 offset:45056
	v_mfma_f32_16x16x32_bf16 v[88:91], v[174:177], v[190:193], v[88:91]
	v_mfma_f32_16x16x32_bf16 v[84:87], v[182:185], v[190:193], v[84:87]
	v_mfma_f32_16x16x32_bf16 v[80:83], v[186:189], v[190:193], v[80:83]
	s_waitcnt lgkmcnt(2)
	v_mfma_f32_16x16x32_bf16 v[76:79], v[170:173], v[194:197], v[76:79]
	ds_read_b128 v[190:193], v162 offset:47104
	buffer_load_dwordx4 v[0:3], v160, s[12:15], s26 offen
	s_waitcnt vmcnt(11)
	v_cvt_pk_bf16_f32 v31, v30, v31
	v_cvt_pk_bf16_f32 v30, v28, v29
	v_mfma_f32_16x16x32_bf16 v[72:75], v[174:177], v[194:197], v[72:75]
	ds_write_b64 v161, v[30:31] offset:17408
	v_mfma_f32_16x16x32_bf16 v[68:71], v[182:185], v[194:197], v[68:71]
	v_mfma_f32_16x16x32_bf16 v[64:67], v[186:189], v[194:197], v[64:67]
	s_add_i32 s27, s9, 0xfffa0000
	s_waitcnt lgkmcnt(2)
	v_mfma_f32_16x16x32_bf16 v[60:63], v[170:173], v[178:181], v[60:63]
	ds_read_b128 v[194:197], v162 offset:33792
	v_mfma_f32_16x16x32_bf16 v[56:59], v[174:177], v[178:181], v[56:59]
	v_mfma_f32_16x16x32_bf16 v[52:55], v[182:185], v[178:181], v[52:55]
	v_mfma_f32_16x16x32_bf16 v[48:51], v[186:189], v[178:181], v[48:51]
	s_waitcnt lgkmcnt(2)
	v_mfma_f32_16x16x32_bf16 v[44:47], v[170:173], v[190:193], v[44:47]
	ds_read_b128 v[170:173], v162 offset:35840
	buffer_load_dwordx4 v[28:31], v160, s[12:15], s27 offen
	s_waitcnt vmcnt(11)
	v_cvt_pk_bf16_f32 v27, v26, v27
	v_cvt_pk_bf16_f32 v26, v24, v25
	v_mfma_f32_16x16x32_bf16 v[40:43], v[174:177], v[190:193], v[40:43]
	ds_read_b64_tr_b16 v[244:245], v166 offset:52224
	ds_read_b64_tr_b16 v[248:249], v166 offset:52256
	ds_read_b64_tr_b16 v[198:199], v166 offset:52288
	ds_read_b64_tr_b16 v[202:203], v166 offset:52320
	ds_read_b64_tr_b16 v[246:247], v167 offset:52224
	ds_read_b64_tr_b16 v[250:251], v167 offset:52256
	ds_read_b64_tr_b16 v[200:201], v167 offset:52288
	ds_read_b64_tr_b16 v[204:205], v167 offset:52320
	ds_write_b64 v161, v[26:27] offset:26112
	v_mfma_f32_16x16x32_bf16 v[36:39], v[182:185], v[190:193], v[36:39]
	v_mfma_f32_16x16x32_bf16 v[32:35], v[186:189], v[190:193], v[32:35]
	s_waitcnt lgkmcnt(4)
	v_mfma_f32_16x16x32_bf16 v[156:159], v[244:247], v[194:197], v[156:159]
	ds_read_b128 v[182:185], v162 offset:37888
	s_waitcnt lgkmcnt(4)
	v_mfma_f32_16x16x32_bf16 v[152:155], v[248:251], v[194:197], v[152:155]
	s_waitcnt lgkmcnt(3)
	v_mfma_f32_16x16x32_bf16 v[148:151], v[198:201], v[194:197], v[148:151]
	s_waitcnt lgkmcnt(2)
	v_mfma_f32_16x16x32_bf16 v[144:147], v[202:205], v[194:197], v[144:147]
	v_mfma_f32_16x16x32_bf16 v[140:143], v[244:247], v[170:173], v[140:143]
	ds_read_b128 v[186:189], v162 offset:39936
	buffer_load_dwordx4 v[24:27], v160, s[12:15], s9 offen
	s_waitcnt vmcnt(11)
	v_cvt_pk_bf16_f32 v23, v22, v23
	v_cvt_pk_bf16_f32 v22, v20, v21
	v_mfma_f32_16x16x32_bf16 v[136:139], v[248:251], v[170:173], v[136:139]
	ds_write_b64 v161, v[22:23] offset:256
	v_mfma_f32_16x16x32_bf16 v[132:135], v[198:201], v[170:173], v[132:135]
	v_mfma_f32_16x16x32_bf16 v[128:131], v[202:205], v[170:173], v[128:131]
	s_waitcnt lgkmcnt(2)
	v_mfma_f32_16x16x32_bf16 v[124:127], v[244:247], v[182:185], v[124:127]
	ds_read_b128 v[170:173], v162 offset:41984
	v_mfma_f32_16x16x32_bf16 v[120:123], v[248:251], v[182:185], v[120:123]
	v_mfma_f32_16x16x32_bf16 v[116:119], v[198:201], v[182:185], v[116:119]
	v_mfma_f32_16x16x32_bf16 v[112:115], v[202:205], v[182:185], v[112:115]
	s_waitcnt lgkmcnt(2)
	v_mfma_f32_16x16x32_bf16 v[108:111], v[244:247], v[186:189], v[108:111]
	ds_read_b128 v[182:185], v162 offset:44032
	buffer_load_dwordx4 v[20:23], v160, s[16:19], s25 offen
	s_waitcnt vmcnt(11)
	v_cvt_pk_bf16_f32 v7, v6, v7
	v_cvt_pk_bf16_f32 v6, v4, v5
	v_mfma_f32_16x16x32_bf16 v[104:107], v[248:251], v[186:189], v[104:107]
	ds_write_b64 v161, v[6:7] offset:8960
	v_mfma_f32_16x16x32_bf16 v[100:103], v[198:201], v[186:189], v[100:103]
	v_mfma_f32_16x16x32_bf16 v[96:99], v[202:205], v[186:189], v[96:99]
	s_waitcnt lgkmcnt(2)
	v_mfma_f32_16x16x32_bf16 v[92:95], v[244:247], v[170:173], v[92:95]
	ds_read_b128 v[186:189], v162 offset:46080
	v_mfma_f32_16x16x32_bf16 v[88:91], v[248:251], v[170:173], v[88:91]
	v_mfma_f32_16x16x32_bf16 v[84:87], v[198:201], v[170:173], v[84:87]
	v_mfma_f32_16x16x32_bf16 v[80:83], v[202:205], v[170:173], v[80:83]
	s_waitcnt lgkmcnt(2)
	v_mfma_f32_16x16x32_bf16 v[76:79], v[244:247], v[182:185], v[76:79]
	ds_read_b128 v[252:255], v162 offset:48128
	buffer_load_dwordx4 v[4:7], v160, s[16:19], s26 offen
	s_waitcnt vmcnt(11)
	v_cvt_pk_bf16_f32 v11, v10, v11
	v_cvt_pk_bf16_f32 v10, v8, v9
	v_mfma_f32_16x16x32_bf16 v[72:75], v[248:251], v[182:185], v[72:75]
	ds_write_b64 v161, v[10:11] offset:17664
	v_mfma_f32_16x16x32_bf16 v[68:71], v[198:201], v[182:185], v[68:71]
	v_mfma_f32_16x16x32_bf16 v[64:67], v[202:205], v[182:185], v[64:67]
	s_waitcnt lgkmcnt(2)
	v_mfma_f32_16x16x32_bf16 v[60:63], v[244:247], v[186:189], v[60:63]
	buffer_load_dwordx4 v[8:11], v160, s[16:19], s27 offen
	s_waitcnt vmcnt(11)
	v_cvt_pk_bf16_f32 v19, v18, v19
	v_cvt_pk_bf16_f32 v18, v16, v17
	v_mfma_f32_16x16x32_bf16 v[56:59], v[248:251], v[186:189], v[56:59]
	ds_write_b64 v161, v[18:19] offset:26368
	v_mfma_f32_16x16x32_bf16 v[52:55], v[198:201], v[186:189], v[52:55]
	buffer_load_dwordx4 v[16:19], v160, s[16:19], s9 offen
	v_mfma_f32_16x16x32_bf16 v[48:51], v[202:205], v[186:189], v[48:51]
	s_waitcnt vmcnt(8)
	s_waitcnt lgkmcnt(0)
	s_barrier
	s_add_i32 s8, s8, 2
	s_add_i32 s9, s9, 0x300000
	s_addk_i32 s24, 0x100
	s_cmp_ge_i32 s8, s64
	s_cbranch_scc1 .Lflush_P1

.Lflush_P1:
	v_mfma_f32_16x16x32_bf16 v[44:47], v[244:247], v[252:255], v[44:47]
	v_mfma_f32_16x16x32_bf16 v[40:43], v[248:251], v[252:255], v[40:43]
	v_mfma_f32_16x16x32_bf16 v[36:39], v[198:201], v[252:255], v[36:39]
	v_mfma_f32_16x16x32_bf16 v[32:35], v[202:205], v[252:255], v[32:35]
	s_branch .LBB0_73

; #define G_ENDTILE(VM) do { asm volatile("s_waitcnt vmcnt(" #VM ")" ::: "memory"); \
;         asm volatile("s_waitcnt lgkmcnt(0)" ::: "memory"); __builtin_amdgcn_s_barrier(); asm volatile("" ::: "memory"); } while (0)
;     ...
;     for (int ui = 0;; ++ui) {
; #pragma unroll
;         for (int m = 0; m < MF; ++m)
; #pragma unroll
;             for (int n = 0; n < 4; ++n) acc[m][n] = (f32x4){0.f, 0.f, 0.f, 0.f};
;         for (int t = 0; t < nt - 2; t += 2) {
;             G_TILE(G_A0, G_B0, true, G_B1, G_A1, t + 1, true, t + 2, (void)0);
;             G_ENDTILE(8);
;             G_TILE(G_A1, G_B1, true, G_B0, G_A0, t + 2, true, t + 3, (void)0);
;             G_ENDTILE(8);
.LBB0_376:
	s_andn2_b64 vcc, exec, s[30:31]
	v_mov_b32_e32 v159, 0
	s_cbranch_vccnz .LBB0_379
	s_mov_b32 s8, 0
	s_mov_b32 s9, 0x1e0000
	s_movk_i32 s24, 0x100
	s_mov_b32 m0, s72
	s_add_i32 s25, s24, 0xffffff80
	ds_read_b64_tr_b16 v[170:171], v165
	ds_read_b64_tr_b16 v[172:173], v166
	ds_read_b64_tr_b16 v[176:177], v166 offset:32
	ds_read_b128 v[178:181], v162
	ds_read_b64_tr_b16 v[174:175], v165 offset:32
	ds_read_b64_tr_b16 v[182:183], v165 offset:64
	ds_read_b64_tr_b16 v[186:187], v165 offset:96
	ds_read_b64_tr_b16 v[184:185], v166 offset:64
	ds_read_b64_tr_b16 v[188:189], v166 offset:96
	ds_read_b128 v[190:193], v162 offset:2048
	ds_read_b128 v[198:201], v162 offset:4096
	buffer_load_dwordx4 v163, s[20:23], s25 offen lds
	s_mov_b32 m0, s71
	s_waitcnt lgkmcnt(7)
	v_mfma_f32_16x16x32_bf16 v[156:159], v[170:173], v[178:181], 0
	buffer_load_dwordx4 v164, s[20:23], s25 offen lds
	s_waitcnt lgkmcnt(6)
	v_mfma_f32_16x16x32_bf16 v[152:155], v[174:177], v[178:181], 0
	s_waitcnt lgkmcnt(3)
	v_mfma_f32_16x16x32_bf16 v[148:151], v[182:185], v[178:181], 0
	s_waitcnt lgkmcnt(2)
	v_mfma_f32_16x16x32_bf16 v[144:147], v[186:189], v[178:181], 0
	s_waitcnt lgkmcnt(1)
	v_mfma_f32_16x16x32_bf16 v[140:143], v[170:173], v[190:193], 0
	s_mov_b32 m0, s70
	s_nop 0
	buffer_load_dwordx4 v167, s[20:23], s25 offen lds
	ds_read_b128 v[178:181], v162 offset:6144
	s_waitcnt vmcnt(10)
	v_cvt_pk_bf16_f32 v15, v14, v15
	v_cvt_pk_bf16_f32 v14, v12, v13
	v_mfma_f32_16x16x32_bf16 v[136:139], v[174:177], v[190:193], 0
	ds_write_b64 v161, v[14:15] offset:34816
	v_mfma_f32_16x16x32_bf16 v[132:135], v[182:185], v[190:193], 0
	s_mov_b32 m0, s68
	s_nop 0
	buffer_load_dwordx4 v168, s[20:23], s25 offen lds
	s_add_i32 s25, s9, 0xfff20000
	v_mfma_f32_16x16x32_bf16 v[128:131], v[186:189], v[190:193], 0
	s_waitcnt lgkmcnt(2)
	v_mfma_f32_16x16x32_bf16 v[124:127], v[170:173], v[198:201], 0
	ds_read_b128 v[190:193], v162 offset:8192
	v_mfma_f32_16x16x32_bf16 v[120:123], v[174:177], v[198:201], 0
	v_mfma_f32_16x16x32_bf16 v[116:119], v[182:185], v[198:201], 0
	v_mfma_f32_16x16x32_bf16 v[112:115], v[186:189], v[198:201], 0
	s_waitcnt lgkmcnt(2)
	v_mfma_f32_16x16x32_bf16 v[108:111], v[170:173], v[178:181], 0
	ds_read_b128 v[198:201], v162 offset:10240
	buffer_load_dwordx4 v[12:15], v160, s[12:15], s25 offen
	s_waitcnt vmcnt(10)
	v_cvt_pk_bf16_f32 v31, v30, v31
	v_cvt_pk_bf16_f32 v30, v28, v29
	v_mfma_f32_16x16x32_bf16 v[104:107], v[174:177], v[178:181], 0
	ds_write_b64 v161, v[30:31] offset:43520
	v_mfma_f32_16x16x32_bf16 v[100:103], v[182:185], v[178:181], 0
	v_mfma_f32_16x16x32_bf16 v[96:99], v[186:189], v[178:181], 0
	s_add_i32 s26, s9, 0xfff40000
	s_waitcnt lgkmcnt(2)
	v_mfma_f32_16x16x32_bf16 v[92:95], v[170:173], v[190:193], 0
	ds_read_b128 v[178:181], v162 offset:12288
	v_mfma_f32_16x16x32_bf16 v[88:91], v[174:177], v[190:193], 0
	v_mfma_f32_16x16x32_bf16 v[84:87], v[182:185], v[190:193], 0
	v_mfma_f32_16x16x32_bf16 v[80:83], v[186:189], v[190:193], 0
	s_waitcnt lgkmcnt(2)
	v_mfma_f32_16x16x32_bf16 v[76:79], v[170:173], v[198:201], 0
	ds_read_b128 v[190:193], v162 offset:14336
	v_cvt_pk_bf16_f32 v7, v6, v7
	v_cvt_pk_bf16_f32 v6, v4, v5
	v_mfma_f32_16x16x32_bf16 v[72:75], v[174:177], v[198:201], 0
	ds_write_b64 v161, v[6:7] offset:52224
	v_mfma_f32_16x16x32_bf16 v[68:71], v[182:185], v[198:201], 0
	v_mfma_f32_16x16x32_bf16 v[64:67], v[186:189], v[198:201], 0
	s_add_i32 s27, s9, 0xfff60000
	buffer_load_dwordx4 v[28:31], v160, s[12:15], s26 offen
	s_waitcnt lgkmcnt(2)
	v_mfma_f32_16x16x32_bf16 v[60:63], v[170:173], v[178:181], 0
	ds_read_b128 v[198:201], v162 offset:1024
	v_mfma_f32_16x16x32_bf16 v[56:59], v[174:177], v[178:181], 0
	v_mfma_f32_16x16x32_bf16 v[52:55], v[182:185], v[178:181], 0
	v_mfma_f32_16x16x32_bf16 v[48:51], v[186:189], v[178:181], 0
	s_waitcnt lgkmcnt(2)
	v_mfma_f32_16x16x32_bf16 v[44:47], v[170:173], v[190:193], 0
	ds_read_b128 v[170:173], v162 offset:3072
	buffer_load_dwordx4 v[4:7], v160, s[12:15], s27 offen
	s_waitcnt vmcnt(11)
	v_cvt_pk_bf16_f32 v27, v26, v27
	v_cvt_pk_bf16_f32 v26, v24, v25
	v_mfma_f32_16x16x32_bf16 v[40:43], v[174:177], v[190:193], 0
	ds_read_b64_tr_b16 v[244:245], v165 offset:17408
	ds_read_b64_tr_b16 v[248:249], v165 offset:17440
	ds_read_b64_tr_b16 v[202:203], v165 offset:17472
	ds_read_b64_tr_b16 v[206:207], v165 offset:17504
	ds_read_b64_tr_b16 v[246:247], v166 offset:17408
	ds_read_b64_tr_b16 v[250:251], v166 offset:17440
	ds_read_b64_tr_b16 v[204:205], v166 offset:17472
	ds_read_b64_tr_b16 v[208:209], v166 offset:17504
	ds_write_b64 v161, v[26:27] offset:60928
	v_mfma_f32_16x16x32_bf16 v[36:39], v[182:185], v[190:193], 0
	v_mfma_f32_16x16x32_bf16 v[32:35], v[186:189], v[190:193], 0
	s_add_i32 s45, s9, 0xfff80000
	s_waitcnt lgkmcnt(4)
	v_mfma_f32_16x16x32_bf16 v[156:159], v[244:247], v[198:201], v[156:159]
	ds_read_b128 v[182:185], v162 offset:5120
	s_waitcnt lgkmcnt(4)
	v_mfma_f32_16x16x32_bf16 v[152:155], v[248:251], v[198:201], v[152:155]
	s_waitcnt lgkmcnt(3)
	v_mfma_f32_16x16x32_bf16 v[148:151], v[202:205], v[198:201], v[148:151]
	s_waitcnt lgkmcnt(2)
	v_mfma_f32_16x16x32_bf16 v[144:147], v[206:209], v[198:201], v[144:147]
	v_mfma_f32_16x16x32_bf16 v[140:143], v[244:247], v[170:173], v[140:143]
	ds_read_b128 v[186:189], v162 offset:7168
	buffer_load_dwordx4 v[24:27], v160, s[12:15], s45 offen
	s_waitcnt vmcnt(11)
	v_cvt_pk_bf16_f32 v23, v22, v23
	v_cvt_pk_bf16_f32 v22, v20, v21
	v_mfma_f32_16x16x32_bf16 v[136:139], v[248:251], v[170:173], v[136:139]
	ds_write_b64 v161, v[22:23] offset:35072
	v_mfma_f32_16x16x32_bf16 v[132:135], v[202:205], v[170:173], v[132:135]
	v_mfma_f32_16x16x32_bf16 v[128:131], v[206:209], v[170:173], v[128:131]
	s_waitcnt lgkmcnt(2)
; #define G_DMA_A(kt, AO) do { G_DMA1(kt, AO, 0); G_DMA1(kt, AO, 1); G_DMA1(kt, AO, 2); G_DMA1(kt, AO, 3); if (MF == 9) G_DMA5(kt, AO); } while (0)
; #define G_ISSUE_B(kt) do { const unsigned _sb = (unsigned)(kt) * 4u * kstepB; \
;         _Pragma("unroll") for (int _i = 0; _i < 8; ++_i) sb[_i] = bload16(_i < 4 ? rsB0 : rsB1, vob, _sb + (_i & 3) * kstepB); } while (0)
; #define G_WRITE_B(BO) do { \
;         _Pragma("unroll") for (int _i = 0; _i < 8; ++_i) *(LAS u32x2*)(b_wr + (BO) + (_i & 3) * (16 * G_BSTRIDE) + (_i >> 2) * SLAB1) = pack4(__builtin_bit_cast(f32x4, sb[_i])); } while (0)
; #define G_ENDTILE(VM) do { asm volatile("s_waitcnt vmcnt(" #VM ")" ::: "memory"); \
;         asm volatile("s_waitcnt lgkmcnt(0)" ::: "memory"); __builtin_amdgcn_s_barrier(); asm volatile("" ::: "memory"); } while (0)
;     ...
;     __builtin_amdgcn_s_barrier();
;     G_DMA_A(0, G_A0); G_ISSUE_B(0); G_WRITE_B(G_B0);
;     __builtin_amdgcn_sched_barrier(0);
;     G_ISSUE_B(1);
;     __builtin_amdgcn_sched_barrier(0);
;     G_ENDTILE(8);
;     for (int ui = 0;; ++ui) {
; #pragma unroll
;         for (int m = 0; m < MF; ++m)
; #pragma unroll
;             for (int n = 0; n < 4; ++n) acc[m][n] = (f32x4){0.f, 0.f, 0.f, 0.f};
;         for (int t = 0; t < nt - 2; t += 2) {
;             G_TILE(G_A0, G_B0, true, G_B1, G_A1, t + 1, true, t + 2, (void)0);
;             G_ENDTILE(8);
;             G_TILE(G_A1, G_B1, true, G_B0, G_A0, t + 2, true, t + 3, (void)0);
;             G_ENDTILE(8);
	v_mfma_f32_16x16x32_bf16 v[124:127], v[244:247], v[182:185], v[124:127]
	ds_read_b128 v[170:173], v162 offset:9216
	v_mfma_f32_16x16x32_bf16 v[120:123], v[248:251], v[182:185], v[120:123]
	v_mfma_f32_16x16x32_bf16 v[116:119], v[202:205], v[182:185], v[116:119]
	v_mfma_f32_16x16x32_bf16 v[112:115], v[206:209], v[182:185], v[112:115]
	s_waitcnt lgkmcnt(2)
	v_mfma_f32_16x16x32_bf16 v[108:111], v[244:247], v[186:189], v[108:111]
	ds_read_b128 v[182:185], v162 offset:11264
	buffer_load_dwordx4 v[20:23], v160, s[16:19], s25 offen
	s_waitcnt vmcnt(10)
	v_cvt_pk_bf16_f32 v11, v10, v11
	v_cvt_pk_bf16_f32 v10, v8, v9
	v_mfma_f32_16x16x32_bf16 v[104:107], v[248:251], v[186:189], v[104:107]
	ds_write_b64 v161, v[10:11] offset:43776
	v_mfma_f32_16x16x32_bf16 v[100:103], v[202:205], v[186:189], v[100:103]
	v_mfma_f32_16x16x32_bf16 v[96:99], v[206:209], v[186:189], v[96:99]
	s_waitcnt lgkmcnt(2)
	v_mfma_f32_16x16x32_bf16 v[92:95], v[244:247], v[170:173], v[92:95]
	ds_read_b128 v[186:189], v162 offset:13312
	v_mfma_f32_16x16x32_bf16 v[88:91], v[248:251], v[170:173], v[88:91]
	v_mfma_f32_16x16x32_bf16 v[84:87], v[202:205], v[170:173], v[84:87]
	v_mfma_f32_16x16x32_bf16 v[80:83], v[206:209], v[170:173], v[80:83]
	s_waitcnt lgkmcnt(2)
	v_mfma_f32_16x16x32_bf16 v[76:79], v[244:247], v[182:185], v[76:79]
	ds_read_b128 v[252:255], v162 offset:15360
	v_cvt_pk_bf16_f32 v3, v2, v3
	v_cvt_pk_bf16_f32 v2, v0, v1
	v_mfma_f32_16x16x32_bf16 v[72:75], v[248:251], v[182:185], v[72:75]
	ds_write_b64 v161, v[2:3] offset:52480
	v_mfma_f32_16x16x32_bf16 v[68:71], v[202:205], v[182:185], v[68:71]
	v_mfma_f32_16x16x32_bf16 v[64:67], v[206:209], v[182:185], v[64:67]
	buffer_load_dwordx4 v[8:11], v160, s[16:19], s26 offen
	s_waitcnt lgkmcnt(2)
	v_mfma_f32_16x16x32_bf16 v[60:63], v[244:247], v[186:189], v[60:63]
	buffer_load_dwordx4 v[0:3], v160, s[16:19], s27 offen
	s_waitcnt vmcnt(11)
	v_cvt_pk_bf16_f32 v19, v18, v19
	v_cvt_pk_bf16_f32 v18, v16, v17
	v_mfma_f32_16x16x32_bf16 v[56:59], v[248:251], v[186:189], v[56:59]
	ds_write_b64 v161, v[18:19] offset:61184
	v_mfma_f32_16x16x32_bf16 v[52:55], v[202:205], v[186:189], v[52:55]
	buffer_load_dwordx4 v[16:19], v160, s[16:19], s45 offen
	v_mfma_f32_16x16x32_bf16 v[48:51], v[206:209], v[186:189], v[48:51]
	s_waitcnt vmcnt(8)
	s_mov_b32 m0, s59
	s_waitcnt lgkmcnt(0)
	s_barrier
	ds_read_b64_tr_b16 v[170:171], v165 offset:34816
	ds_read_b64_tr_b16 v[172:173], v166 offset:34816
	ds_read_b64_tr_b16 v[176:177], v166 offset:34848
	ds_read_b128 v[178:181], v162 offset:32768
	ds_read_b64_tr_b16 v[174:175], v165 offset:34848
	ds_read_b64_tr_b16 v[182:183], v165 offset:34880
	ds_read_b64_tr_b16 v[186:187], v165 offset:34912
	ds_read_b64_tr_b16 v[184:185], v166 offset:34880
	ds_read_b64_tr_b16 v[188:189], v166 offset:34912
	ds_read_b128 v[190:193], v162 offset:34816
	ds_read_b128 v[198:201], v162 offset:36864
	buffer_load_dwordx4 v163, s[20:23], s24 offen lds
	s_mov_b32 m0, s60
	v_mfma_f32_16x16x32_bf16 v[44:47], v[244:247], v[252:255], v[44:47]
	v_mfma_f32_16x16x32_bf16 v[40:43], v[248:251], v[252:255], v[40:43]
	v_mfma_f32_16x16x32_bf16 v[36:39], v[202:205], v[252:255], v[36:39]
	v_mfma_f32_16x16x32_bf16 v[32:35], v[206:209], v[252:255], v[32:35]
	s_waitcnt lgkmcnt(7)
	v_mfma_f32_16x16x32_bf16 v[156:159], v[170:173], v[178:181], v[156:159]
	buffer_load_dwordx4 v164, s[20:23], s24 offen lds
	s_add_i32 s25, s9, 0xfffa0000
	s_waitcnt lgkmcnt(6)
	v_mfma_f32_16x16x32_bf16 v[152:155], v[174:177], v[178:181], v[152:155]
	s_waitcnt lgkmcnt(3)
	v_mfma_f32_16x16x32_bf16 v[148:151], v[182:185], v[178:181], v[148:151]
	s_waitcnt lgkmcnt(2)
	v_mfma_f32_16x16x32_bf16 v[144:147], v[186:189], v[178:181], v[144:147]
	s_waitcnt lgkmcnt(1)
	v_mfma_f32_16x16x32_bf16 v[140:143], v[170:173], v[190:193], v[140:143]
	s_mov_b32 m0, s61
	s_nop 0
	buffer_load_dwordx4 v167, s[20:23], s24 offen lds
	ds_read_b128 v[178:181], v162 offset:38912
	s_waitcnt vmcnt(10)
	v_cvt_pk_bf16_f32 v15, v14, v15
	v_cvt_pk_bf16_f32 v14, v12, v13
	v_mfma_f32_16x16x32_bf16 v[136:139], v[174:177], v[190:193], v[136:139]
	ds_write_b64 v161, v[14:15]
	v_mfma_f32_16x16x32_bf16 v[132:135], v[182:185], v[190:193], v[132:135]
	s_mov_b32 m0, s62
	s_nop 0
	buffer_load_dwordx4 v168, s[20:23], s24 offen lds
	v_mfma_f32_16x16x32_bf16 v[128:131], v[186:189], v[190:193], v[128:131]
	s_waitcnt lgkmcnt(2)
	v_mfma_f32_16x16x32_bf16 v[124:127], v[170:173], v[198:201], v[124:127]
	ds_read_b128 v[190:193], v162 offset:40960
	v_mfma_f32_16x16x32_bf16 v[120:123], v[174:177], v[198:201], v[120:123]
	v_mfma_f32_16x16x32_bf16 v[116:119], v[182:185], v[198:201], v[116:119]
	v_mfma_f32_16x16x32_bf16 v[112:115], v[186:189], v[198:201], v[112:115]
	s_waitcnt lgkmcnt(2)
	v_mfma_f32_16x16x32_bf16 v[108:111], v[170:173], v[178:181], v[108:111]
	ds_read_b128 v[198:201], v162 offset:43008
	buffer_load_dwordx4 v[12:15], v160, s[12:15], s25 offen
	s_waitcnt vmcnt(11)
	v_cvt_pk_bf16_f32 v31, v30, v31
	v_cvt_pk_bf16_f32 v30, v28, v29
	v_mfma_f32_16x16x32_bf16 v[104:107], v[174:177], v[178:181], v[104:107]
	ds_write_b64 v161, v[30:31] offset:8704
	v_mfma_f32_16x16x32_bf16 v[100:103], v[182:185], v[178:181], v[100:103]
	v_mfma_f32_16x16x32_bf16 v[96:99], v[186:189], v[178:181], v[96:99]
	s_add_i32 s26, s9, 0xfffc0000
	s_waitcnt lgkmcnt(2)
; #define G_DMA_A(kt, AO) do { G_DMA1(kt, AO, 0); G_DMA1(kt, AO, 1); G_DMA1(kt, AO, 2); G_DMA1(kt, AO, 3); if (MF == 9) G_DMA5(kt, AO); } while (0)
; #define G_ISSUE_B(kt) do { const unsigned _sb = (unsigned)(kt) * 4u * kstepB; \
;         _Pragma("unroll") for (int _i = 0; _i < 8; ++_i) sb[_i] = bload16(_i < 4 ? rsB0 : rsB1, vob, _sb + (_i & 3) * kstepB); } while (0)
; #define G_WRITE_B(BO) do { \
;         _Pragma("unroll") for (int _i = 0; _i < 8; ++_i) *(LAS u32x2*)(b_wr + (BO) + (_i & 3) * (16 * G_BSTRIDE) + (_i >> 2) * SLAB1) = pack4(__builtin_bit_cast(f32x4, sb[_i])); } while (0)
; #define G_ENDTILE(VM) do { asm volatile("s_waitcnt vmcnt(" #VM ")" ::: "memory"); \
;         asm volatile("s_waitcnt lgkmcnt(0)" ::: "memory"); __builtin_amdgcn_s_barrier(); asm volatile("" ::: "memory"); } while (0)
;     ...
;     __builtin_amdgcn_s_barrier();
;     G_DMA_A(0, G_A0); G_ISSUE_B(0); G_WRITE_B(G_B0);
;     __builtin_amdgcn_sched_barrier(0);
;     G_ISSUE_B(1);
;     __builtin_amdgcn_sched_barrier(0);
;     G_ENDTILE(8);
;     for (int ui = 0;; ++ui) {
; #pragma unroll
;         for (int m = 0; m < MF; ++m)
; #pragma unroll
;             for (int n = 0; n < 4; ++n) acc[m][n] = (f32x4){0.f, 0.f, 0.f, 0.f};
;         for (int t = 0; t < nt - 2; t += 2) {
;             G_TILE(G_A0, G_B0, true, G_B1, G_A1, t + 1, true, t + 2, (void)0);
;             G_ENDTILE(8);
;             G_TILE(G_A1, G_B1, true, G_B0, G_A0, t + 2, true, t + 3, (void)0);
;             G_ENDTILE(8);
;         }
	v_mfma_f32_16x16x32_bf16 v[92:95], v[170:173], v[190:193], v[92:95]
	ds_read_b128 v[178:181], v162 offset:45056
	v_mfma_f32_16x16x32_bf16 v[88:91], v[174:177], v[190:193], v[88:91]
	v_mfma_f32_16x16x32_bf16 v[84:87], v[182:185], v[190:193], v[84:87]
	v_mfma_f32_16x16x32_bf16 v[80:83], v[186:189], v[190:193], v[80:83]
	s_waitcnt lgkmcnt(2)
	v_mfma_f32_16x16x32_bf16 v[76:79], v[170:173], v[198:201], v[76:79]
	ds_read_b128 v[190:193], v162 offset:47104
	buffer_load_dwordx4 v[28:31], v160, s[12:15], s26 offen
	s_waitcnt vmcnt(11)
	v_cvt_pk_bf16_f32 v7, v6, v7
	v_cvt_pk_bf16_f32 v6, v4, v5
	v_mfma_f32_16x16x32_bf16 v[72:75], v[174:177], v[198:201], v[72:75]
	ds_write_b64 v161, v[6:7] offset:17408
	v_mfma_f32_16x16x32_bf16 v[68:71], v[182:185], v[198:201], v[68:71]
	v_mfma_f32_16x16x32_bf16 v[64:67], v[186:189], v[198:201], v[64:67]
	s_add_i32 s27, s9, 0xfffe0000
	s_waitcnt lgkmcnt(2)
	v_mfma_f32_16x16x32_bf16 v[60:63], v[170:173], v[178:181], v[60:63]
	ds_read_b128 v[198:201], v162 offset:33792
	v_mfma_f32_16x16x32_bf16 v[56:59], v[174:177], v[178:181], v[56:59]
	v_mfma_f32_16x16x32_bf16 v[52:55], v[182:185], v[178:181], v[52:55]
	v_mfma_f32_16x16x32_bf16 v[48:51], v[186:189], v[178:181], v[48:51]
	s_waitcnt lgkmcnt(2)
	v_mfma_f32_16x16x32_bf16 v[44:47], v[170:173], v[190:193], v[44:47]
	ds_read_b128 v[170:173], v162 offset:35840
	buffer_load_dwordx4 v[4:7], v160, s[12:15], s27 offen
	s_waitcnt vmcnt(11)
	v_cvt_pk_bf16_f32 v27, v26, v27
	v_cvt_pk_bf16_f32 v26, v24, v25
	v_mfma_f32_16x16x32_bf16 v[40:43], v[174:177], v[190:193], v[40:43]
	ds_read_b64_tr_b16 v[244:245], v165 offset:52224
	ds_read_b64_tr_b16 v[248:249], v165 offset:52256
	ds_read_b64_tr_b16 v[202:203], v165 offset:52288
	ds_read_b64_tr_b16 v[206:207], v165 offset:52320
	ds_read_b64_tr_b16 v[246:247], v166 offset:52224
	ds_read_b64_tr_b16 v[250:251], v166 offset:52256
	ds_read_b64_tr_b16 v[204:205], v166 offset:52288
	ds_read_b64_tr_b16 v[208:209], v166 offset:52320
	ds_write_b64 v161, v[26:27] offset:26112
	v_mfma_f32_16x16x32_bf16 v[36:39], v[182:185], v[190:193], v[36:39]
	v_mfma_f32_16x16x32_bf16 v[32:35], v[186:189], v[190:193], v[32:35]
	s_waitcnt lgkmcnt(4)
	v_mfma_f32_16x16x32_bf16 v[156:159], v[244:247], v[198:201], v[156:159]
	ds_read_b128 v[182:185], v162 offset:37888
	s_waitcnt lgkmcnt(4)
	v_mfma_f32_16x16x32_bf16 v[152:155], v[248:251], v[198:201], v[152:155]
	s_waitcnt lgkmcnt(3)
	v_mfma_f32_16x16x32_bf16 v[148:151], v[202:205], v[198:201], v[148:151]
	s_waitcnt lgkmcnt(2)
	v_mfma_f32_16x16x32_bf16 v[144:147], v[206:209], v[198:201], v[144:147]
	v_mfma_f32_16x16x32_bf16 v[140:143], v[244:247], v[170:173], v[140:143]
	ds_read_b128 v[186:189], v162 offset:39936
	buffer_load_dwordx4 v[24:27], v160, s[12:15], s9 offen
	s_waitcnt vmcnt(11)
	v_cvt_pk_bf16_f32 v23, v22, v23
	v_cvt_pk_bf16_f32 v22, v20, v21
	v_mfma_f32_16x16x32_bf16 v[136:139], v[248:251], v[170:173], v[136:139]
	ds_write_b64 v161, v[22:23] offset:256
	v_mfma_f32_16x16x32_bf16 v[132:135], v[202:205], v[170:173], v[132:135]
	v_mfma_f32_16x16x32_bf16 v[128:131], v[206:209], v[170:173], v[128:131]
	s_waitcnt lgkmcnt(2)
	v_mfma_f32_16x16x32_bf16 v[124:127], v[244:247], v[182:185], v[124:127]
	ds_read_b128 v[170:173], v162 offset:41984
	v_mfma_f32_16x16x32_bf16 v[120:123], v[248:251], v[182:185], v[120:123]
	v_mfma_f32_16x16x32_bf16 v[116:119], v[202:205], v[182:185], v[116:119]
	v_mfma_f32_16x16x32_bf16 v[112:115], v[206:209], v[182:185], v[112:115]
	s_waitcnt lgkmcnt(2)
	v_mfma_f32_16x16x32_bf16 v[108:111], v[244:247], v[186:189], v[108:111]
	ds_read_b128 v[182:185], v162 offset:44032
	buffer_load_dwordx4 v[20:23], v160, s[16:19], s25 offen
	s_waitcnt vmcnt(11)
	v_cvt_pk_bf16_f32 v11, v10, v11
	v_cvt_pk_bf16_f32 v10, v8, v9
	v_mfma_f32_16x16x32_bf16 v[104:107], v[248:251], v[186:189], v[104:107]
	ds_write_b64 v161, v[10:11] offset:8960
	v_mfma_f32_16x16x32_bf16 v[100:103], v[202:205], v[186:189], v[100:103]
	v_mfma_f32_16x16x32_bf16 v[96:99], v[206:209], v[186:189], v[96:99]
	s_waitcnt lgkmcnt(2)
	v_mfma_f32_16x16x32_bf16 v[92:95], v[244:247], v[170:173], v[92:95]
	ds_read_b128 v[186:189], v162 offset:46080
	v_mfma_f32_16x16x32_bf16 v[88:91], v[248:251], v[170:173], v[88:91]
	v_mfma_f32_16x16x32_bf16 v[84:87], v[202:205], v[170:173], v[84:87]
	v_mfma_f32_16x16x32_bf16 v[80:83], v[206:209], v[170:173], v[80:83]
	s_waitcnt lgkmcnt(2)
	v_mfma_f32_16x16x32_bf16 v[76:79], v[244:247], v[182:185], v[76:79]
	ds_read_b128 v[252:255], v162 offset:48128
	buffer_load_dwordx4 v[8:11], v160, s[16:19], s26 offen
	s_waitcnt vmcnt(11)
	v_cvt_pk_bf16_f32 v3, v2, v3
	v_cvt_pk_bf16_f32 v2, v0, v1
	v_mfma_f32_16x16x32_bf16 v[72:75], v[248:251], v[182:185], v[72:75]
	ds_write_b64 v161, v[2:3] offset:17664
	v_mfma_f32_16x16x32_bf16 v[68:71], v[202:205], v[182:185], v[68:71]
	v_mfma_f32_16x16x32_bf16 v[64:67], v[206:209], v[182:185], v[64:67]
	s_waitcnt lgkmcnt(2)
	v_mfma_f32_16x16x32_bf16 v[60:63], v[244:247], v[186:189], v[60:63]
	buffer_load_dwordx4 v[0:3], v160, s[16:19], s27 offen
	s_waitcnt vmcnt(11)
	v_cvt_pk_bf16_f32 v19, v18, v19
	v_cvt_pk_bf16_f32 v18, v16, v17
	v_mfma_f32_16x16x32_bf16 v[56:59], v[248:251], v[186:189], v[56:59]
	ds_write_b64 v161, v[18:19] offset:26368
	v_mfma_f32_16x16x32_bf16 v[52:55], v[202:205], v[186:189], v[52:55]
	buffer_load_dwordx4 v[16:19], v160, s[16:19], s9 offen
	v_mfma_f32_16x16x32_bf16 v[48:51], v[206:209], v[186:189], v[48:51]
	s_waitcnt vmcnt(8)
	s_waitcnt lgkmcnt(0)
	s_barrier
	s_add_i32 s8, s8, 2
	s_add_i32 s9, s9, 0x100000
	s_addk_i32 s24, 0x100
	s_cmp_ge_i32 s8, s67
	s_cbranch_scc1 .Lflush_P3

.Lflush_P3:
	v_mfma_f32_16x16x32_bf16 v[44:47], v[244:247], v[252:255], v[44:47]
	v_mfma_f32_16x16x32_bf16 v[40:43], v[248:251], v[252:255], v[40:43]
	v_mfma_f32_16x16x32_bf16 v[36:39], v[202:205], v[252:255], v[36:39]
	v_mfma_f32_16x16x32_bf16 v[32:35], v[206:209], v[252:255], v[32:35]
	s_branch .LBB0_380

; #define G_ENDTILE(VM) do { asm volatile("s_waitcnt vmcnt(" #VM ")" ::: "memory"); \
;         asm volatile("s_waitcnt lgkmcnt(0)" ::: "memory"); __builtin_amdgcn_s_barrier(); asm volatile("" ::: "memory"); } while (0)
;     ...
;     for (int ui = 0;; ++ui) {
; #pragma unroll
;         for (int m = 0; m < MF; ++m)
; #pragma unroll
;             for (int n = 0; n < 4; ++n) acc[m][n] = (f32x4){0.f, 0.f, 0.f, 0.f};
;         for (int t = 0; t < nt - 2; t += 2) {
;             G_TILE(G_A0, G_B0, true, G_B1, G_A1, t + 1, true, t + 2, (void)0);
;             G_ENDTILE(8);
;             G_TILE(G_A1, G_B1, true, G_B0, G_A0, t + 2, true, t + 3, (void)0);
;             G_ENDTILE(8);
.LBB0_649:
	s_andn2_b64 vcc, exec, s[40:41]
	v_mov_b32_e32 v175, 0
	s_cbranch_vccnz .LBB0_652
	s_mov_b32 s16, 0
	s_mov_b32 s17, 0x1e0000
	s_movk_i32 s36, 0x100
	s_cmp_lt_u32 s99, 9
	s_cbranch_scc1 .Lslow_P5
	s_mov_b32 m0, s85
	s_add_i32 s37, s36, 0xffffff80
	ds_read_b64_tr_b16 v[178:179], v188
	ds_read_b64_tr_b16 v[176:177], v187
	ds_read_b64_tr_b16 v[180:181], v187 offset:32
	ds_read_b64_tr_b16 v[198:199], v187 offset:64
	ds_read_b64_tr_b16 v[202:203], v187 offset:96
	ds_read_b128 v[206:209], v186
	ds_read_b64_tr_b16 v[182:183], v188 offset:32
	ds_read_b64_tr_b16 v[200:201], v188 offset:64
	ds_read_b64_tr_b16 v[204:205], v188 offset:96
	ds_read_b128 v[210:213], v186 offset:2048
	ds_read_b128 v[214:217], v186 offset:4096
	buffer_load_dwordx4 v189, s[20:23], s37 offen lds
	s_mov_b32 m0, s7
	s_waitcnt lgkmcnt(5)
	v_mfma_f32_16x16x32_bf16 v[172:175], v[176:179], v[206:209], 0
	buffer_load_dwordx4 v192, s[20:23], s37 offen lds
	s_waitcnt lgkmcnt(4)
	v_mfma_f32_16x16x32_bf16 v[168:171], v[180:183], v[206:209], 0
	s_waitcnt lgkmcnt(3)
	v_mfma_f32_16x16x32_bf16 v[164:167], v[198:201], v[206:209], 0
	s_waitcnt lgkmcnt(2)
	v_mfma_f32_16x16x32_bf16 v[160:163], v[202:205], v[206:209], 0
	s_waitcnt lgkmcnt(1)
	v_mfma_f32_16x16x32_bf16 v[156:159], v[176:179], v[210:213], 0
	s_mov_b32 m0, s6
	s_nop 0
	buffer_load_dwordx4 v191, s[20:23], s37 offen lds
	ds_read_b128 v[206:209], v186 offset:6144
	s_waitcnt vmcnt(10)
	v_cvt_pk_bf16_f32 v15, v14, v15
	v_cvt_pk_bf16_f32 v14, v12, v13
	v_mfma_f32_16x16x32_bf16 v[152:155], v[180:183], v[210:213], 0
	ds_write_b64 v185, v[14:15] offset:34816
	v_mfma_f32_16x16x32_bf16 v[148:151], v[198:201], v[210:213], 0
	s_mov_b32 m0, s47
	s_nop 0
	buffer_load_dwordx4 v190, s[20:23], s37 offen lds
	v_mfma_f32_16x16x32_bf16 v[144:147], v[202:205], v[210:213], 0
	s_waitcnt lgkmcnt(2)
	v_mfma_f32_16x16x32_bf16 v[132:135], v[176:179], v[214:217], 0
	s_mov_b32 m0, s48
	s_nop 0
	buffer_load_dwordx4 v193, s[20:23], s37 offen lds
	s_add_i32 s37, s17, 0xfff20000
	ds_read_b128 v[210:213], v186 offset:8192
	v_mfma_f32_16x16x32_bf16 v[124:127], v[180:183], v[214:217], 0
	v_mfma_f32_16x16x32_bf16 v[120:123], v[198:201], v[214:217], 0
	v_mfma_f32_16x16x32_bf16 v[140:143], v[202:205], v[214:217], 0
	s_waitcnt lgkmcnt(2)
	v_mfma_f32_16x16x32_bf16 v[136:139], v[176:179], v[206:209], 0
	ds_read_b128 v[214:217], v186 offset:10240
	buffer_load_dwordx4 v[12:15], v184, s[24:27], s37 offen
	s_waitcnt vmcnt(12)
	v_cvt_pk_bf16_f32 v3, v2, v3
	v_cvt_pk_bf16_f32 v2, v0, v1
	v_mfma_f32_16x16x32_bf16 v[128:131], v[180:183], v[206:209], 0
	ds_write_b64 v185, v[2:3] offset:43520
	v_mfma_f32_16x16x32_bf16 v[116:119], v[198:201], v[206:209], 0
	v_mfma_f32_16x16x32_bf16 v[112:115], v[202:205], v[206:209], 0
	s_add_i32 s38, s17, 0xfff40000
	s_waitcnt lgkmcnt(2)
	v_mfma_f32_16x16x32_bf16 v[100:103], v[176:179], v[210:213], 0
	ds_read_b128 v[206:209], v186 offset:12288
	v_mfma_f32_16x16x32_bf16 v[92:95], v[180:183], v[210:213], 0
	v_mfma_f32_16x16x32_bf16 v[88:91], v[198:201], v[210:213], 0
	v_mfma_f32_16x16x32_bf16 v[108:111], v[202:205], v[210:213], 0
	s_waitcnt lgkmcnt(2)
	v_mfma_f32_16x16x32_bf16 v[104:107], v[176:179], v[214:217], 0
	ds_read_b128 v[210:213], v186 offset:14336
	buffer_load_dwordx4 v[0:3], v184, s[24:27], s38 offen
	s_waitcnt vmcnt(12)
	v_cvt_pk_bf16_f32 v31, v30, v31
	v_cvt_pk_bf16_f32 v30, v28, v29
	v_mfma_f32_16x16x32_bf16 v[96:99], v[180:183], v[214:217], 0
	ds_write_b64 v185, v[30:31] offset:52224
	v_mfma_f32_16x16x32_bf16 v[84:87], v[198:201], v[214:217], 0
	v_mfma_f32_16x16x32_bf16 v[80:83], v[202:205], v[214:217], 0
	s_add_i32 s39, s17, 0xfff60000
	s_waitcnt lgkmcnt(2)
	v_mfma_f32_16x16x32_bf16 v[72:75], v[176:179], v[206:209], 0
	ds_read_b128 v[214:217], v186 offset:16384
	v_mfma_f32_16x16x32_bf16 v[64:67], v[180:183], v[206:209], 0
	v_mfma_f32_16x16x32_bf16 v[60:63], v[198:201], v[206:209], 0
	v_mfma_f32_16x16x32_bf16 v[76:79], v[202:205], v[206:209], 0
	s_waitcnt lgkmcnt(2)
	v_mfma_f32_16x16x32_bf16 v[68:71], v[176:179], v[210:213], 0
	ds_read_b128 v[206:209], v186 offset:1024
	buffer_load_dwordx4 v[28:31], v184, s[24:27], s39 offen
	s_waitcnt vmcnt(12)
	v_cvt_pk_bf16_f32 v27, v26, v27
	v_cvt_pk_bf16_f32 v26, v24, v25
	v_mfma_f32_16x16x32_bf16 v[56:59], v[180:183], v[210:213], 0
	ds_write_b64 v185, v[26:27] offset:60928
	v_mfma_f32_16x16x32_bf16 v[52:55], v[198:201], v[210:213], 0
	v_mfma_f32_16x16x32_bf16 v[48:51], v[202:205], v[210:213], 0
	s_add_i32 s42, s17, 0xfff80000
	ds_read_b128 v[210:213], v186 offset:3072
	s_waitcnt lgkmcnt(3)
	v_mfma_f32_16x16x32_bf16 v[44:47], v[176:179], v[214:217], 0
	ds_read_b64_tr_b16 v[246:247], v188 offset:17408
	ds_read_b64_tr_b16 v[220:221], v188 offset:17440
	ds_read_b64_tr_b16 v[244:245], v187 offset:17408
	ds_read_b64_tr_b16 v[218:219], v187 offset:17440
	v_mfma_f32_16x16x32_bf16 v[40:43], v[180:183], v[214:217], 0
	ds_read_b64_tr_b16 v[248:249], v187 offset:17472
	ds_read_b64_tr_b16 v[250:251], v188 offset:17472
	v_mfma_f32_16x16x32_bf16 v[36:39], v[198:201], v[214:217], 0
	ds_read_b64_tr_b16 v[252:253], v187 offset:17504
	ds_read_b64_tr_b16 v[254:255], v188 offset:17504
	v_mfma_f32_16x16x32_bf16 v[32:35], v[202:205], v[214:217], 0
	s_waitcnt lgkmcnt(5)
	v_mfma_f32_16x16x32_bf16 v[172:175], v[244:247], v[206:209], v[172:175]
	ds_read_b128 v[202:205], v186 offset:5120
	buffer_load_dwordx4 v[24:27], v184, s[24:27], s42 offen
	s_waitcnt vmcnt(12)
	v_cvt_pk_bf16_f32 v23, v22, v23
	v_cvt_pk_bf16_f32 v22, v20, v21
	s_waitcnt lgkmcnt(5)
	v_mfma_f32_16x16x32_bf16 v[168:171], v[218:221], v[206:209], v[168:171]
	ds_write_b64 v185, v[22:23] offset:34880
	s_waitcnt lgkmcnt(4)
; #define G_DMA_A(kt, AO) do { G_DMA1(kt, AO, 0); G_DMA1(kt, AO, 1); G_DMA1(kt, AO, 2); G_DMA1(kt, AO, 3); if (MF == 9) G_DMA5(kt, AO); } while (0)
; #define G_ISSUE_B(kt) do { const unsigned _sb = (unsigned)(kt) * 4u * kstepB; \
;         _Pragma("unroll") for (int _i = 0; _i < 8; ++_i) sb[_i] = bload16(_i < 4 ? rsB0 : rsB1, vob, _sb + (_i & 3) * kstepB); } while (0)
; #define G_WRITE_B(BO) do { \
;         _Pragma("unroll") for (int _i = 0; _i < 8; ++_i) *(LAS u32x2*)(b_wr + (BO) + (_i & 3) * (16 * G_BSTRIDE) + (_i >> 2) * SLAB1) = pack4(__builtin_bit_cast(f32x4, sb[_i])); } while (0)
; #define G_ENDTILE(VM) do { asm volatile("s_waitcnt vmcnt(" #VM ")" ::: "memory"); \
;         asm volatile("s_waitcnt lgkmcnt(0)" ::: "memory"); __builtin_amdgcn_s_barrier(); asm volatile("" ::: "memory"); } while (0)
;     ...
;     __builtin_amdgcn_s_barrier();
;     G_DMA_A(0, G_A0); G_ISSUE_B(0); G_WRITE_B(G_B0);
;     __builtin_amdgcn_sched_barrier(0);
;     G_ISSUE_B(1);
;     __builtin_amdgcn_sched_barrier(0);
;     G_ENDTILE(8);
;     for (int ui = 0;; ++ui) {
; #pragma unroll
;         for (int m = 0; m < MF; ++m)
; #pragma unroll
;             for (int n = 0; n < 4; ++n) acc[m][n] = (f32x4){0.f, 0.f, 0.f, 0.f};
;         for (int t = 0; t < nt - 2; t += 2) {
;             G_TILE(G_A0, G_B0, true, G_B1, G_A1, t + 1, true, t + 2, (void)0);
;             G_ENDTILE(8);
;             G_TILE(G_A1, G_B1, true, G_B0, G_A0, t + 2, true, t + 3, (void)0);
;             G_ENDTILE(8);
	v_mfma_f32_16x16x32_bf16 v[164:167], v[248:251], v[206:209], v[164:167]
	s_waitcnt lgkmcnt(2)
	v_mfma_f32_16x16x32_bf16 v[160:163], v[252:255], v[206:209], v[160:163]
	v_mfma_f32_16x16x32_bf16 v[156:159], v[244:247], v[210:213], v[156:159]
	ds_read_b128 v[206:209], v186 offset:7168
	v_mfma_f32_16x16x32_bf16 v[152:155], v[218:221], v[210:213], v[152:155]
	v_mfma_f32_16x16x32_bf16 v[148:151], v[248:251], v[210:213], v[148:151]
	v_mfma_f32_16x16x32_bf16 v[144:147], v[252:255], v[210:213], v[144:147]
	s_waitcnt lgkmcnt(2)
	v_mfma_f32_16x16x32_bf16 v[132:135], v[244:247], v[202:205], v[132:135]
	ds_read_b128 v[210:213], v186 offset:9216
	buffer_load_dwordx4 v[20:23], v184, s[28:31], s37 offen
	s_waitcnt vmcnt(12)
	v_cvt_pk_bf16_f32 v7, v6, v7
	v_cvt_pk_bf16_f32 v6, v4, v5
	v_mfma_f32_16x16x32_bf16 v[124:127], v[218:221], v[202:205], v[124:127]
	ds_write_b64 v185, v[6:7] offset:43584
	v_mfma_f32_16x16x32_bf16 v[120:123], v[248:251], v[202:205], v[120:123]
	v_mfma_f32_16x16x32_bf16 v[140:143], v[252:255], v[202:205], v[140:143]
	s_waitcnt lgkmcnt(2)
	v_mfma_f32_16x16x32_bf16 v[136:139], v[244:247], v[206:209], v[136:139]
	ds_read_b128 v[202:205], v186 offset:11264
	v_mfma_f32_16x16x32_bf16 v[128:131], v[218:221], v[206:209], v[128:131]
	v_mfma_f32_16x16x32_bf16 v[116:119], v[248:251], v[206:209], v[116:119]
	v_mfma_f32_16x16x32_bf16 v[112:115], v[252:255], v[206:209], v[112:115]
	s_waitcnt lgkmcnt(2)
	v_mfma_f32_16x16x32_bf16 v[100:103], v[244:247], v[210:213], v[100:103]
	ds_read_b128 v[206:209], v186 offset:13312
	buffer_load_dwordx4 v[4:7], v184, s[28:31], s38 offen
	s_waitcnt vmcnt(12)
	v_cvt_pk_bf16_f32 v11, v10, v11
	v_cvt_pk_bf16_f32 v10, v8, v9
	v_mfma_f32_16x16x32_bf16 v[92:95], v[218:221], v[210:213], v[92:95]
	ds_write_b64 v185, v[10:11] offset:52288
	v_mfma_f32_16x16x32_bf16 v[88:91], v[248:251], v[210:213], v[88:91]
	v_mfma_f32_16x16x32_bf16 v[108:111], v[252:255], v[210:213], v[108:111]
	s_waitcnt lgkmcnt(2)
	v_mfma_f32_16x16x32_bf16 v[104:107], v[244:247], v[202:205], v[104:107]
	ds_read_b128 v[210:213], v186 offset:15360
	v_mfma_f32_16x16x32_bf16 v[96:99], v[218:221], v[202:205], v[96:99]
	v_mfma_f32_16x16x32_bf16 v[84:87], v[248:251], v[202:205], v[84:87]
	v_mfma_f32_16x16x32_bf16 v[80:83], v[252:255], v[202:205], v[80:83]
	s_waitcnt lgkmcnt(2)
	v_mfma_f32_16x16x32_bf16 v[72:75], v[244:247], v[206:209], v[72:75]
	ds_read_b128 v[238:241], v186 offset:17408
	buffer_load_dwordx4 v[8:11], v184, s[28:31], s39 offen
	s_waitcnt vmcnt(12)
	v_cvt_pk_bf16_f32 v19, v18, v19
	v_cvt_pk_bf16_f32 v18, v16, v17
	v_mfma_f32_16x16x32_bf16 v[64:67], v[218:221], v[206:209], v[64:67]
	ds_write_b64 v185, v[18:19] offset:60992
	v_mfma_f32_16x16x32_bf16 v[60:63], v[248:251], v[206:209], v[60:63]
	v_mfma_f32_16x16x32_bf16 v[76:79], v[252:255], v[206:209], v[76:79]
	s_waitcnt lgkmcnt(2)
	v_mfma_f32_16x16x32_bf16 v[68:71], v[244:247], v[210:213], v[68:71]
	v_mfma_f32_16x16x32_bf16 v[56:59], v[218:221], v[210:213], v[56:59]
	v_mfma_f32_16x16x32_bf16 v[52:55], v[248:251], v[210:213], v[52:55]
	v_mfma_f32_16x16x32_bf16 v[48:51], v[252:255], v[210:213], v[48:51]
	s_waitcnt lgkmcnt(1)
	buffer_load_dwordx4 v[16:19], v184, s[28:31], s42 offen
	s_waitcnt vmcnt(8)
	s_mov_b32 m0, s46
	s_waitcnt lgkmcnt(0)
	s_barrier
	ds_read_b64_tr_b16 v[178:179], v188 offset:34816
	ds_read_b64_tr_b16 v[176:177], v187 offset:34816
	ds_read_b64_tr_b16 v[180:181], v187 offset:34848
	ds_read_b64_tr_b16 v[198:199], v187 offset:34880
	ds_read_b64_tr_b16 v[202:203], v187 offset:34912
	ds_read_b128 v[206:209], v186 offset:36864
	ds_read_b64_tr_b16 v[182:183], v188 offset:34848
	ds_read_b64_tr_b16 v[200:201], v188 offset:34880
	ds_read_b64_tr_b16 v[204:205], v188 offset:34912
	ds_read_b128 v[210:213], v186 offset:38912
	ds_read_b128 v[214:217], v186 offset:40960
	buffer_load_dwordx4 v189, s[20:23], s36 offen lds
	s_mov_b32 m0, s86
	v_mfma_f32_16x16x32_bf16 v[44:47], v[244:247], v[238:241], v[44:47]
	v_mfma_f32_16x16x32_bf16 v[40:43], v[218:221], v[238:241], v[40:43]
	v_mfma_f32_16x16x32_bf16 v[36:39], v[248:251], v[238:241], v[36:39]
	v_mfma_f32_16x16x32_bf16 v[32:35], v[252:255], v[238:241], v[32:35]
	s_waitcnt lgkmcnt(5)
	v_mfma_f32_16x16x32_bf16 v[172:175], v[176:179], v[206:209], v[172:175]
	buffer_load_dwordx4 v192, s[20:23], s36 offen lds
	s_add_i32 s37, s17, 0xfffa0000
	s_waitcnt lgkmcnt(4)
	v_mfma_f32_16x16x32_bf16 v[168:171], v[180:183], v[206:209], v[168:171]
	s_waitcnt lgkmcnt(3)
	v_mfma_f32_16x16x32_bf16 v[164:167], v[198:201], v[206:209], v[164:167]
	s_waitcnt lgkmcnt(2)
	v_mfma_f32_16x16x32_bf16 v[160:163], v[202:205], v[206:209], v[160:163]
	s_waitcnt lgkmcnt(1)
	v_mfma_f32_16x16x32_bf16 v[156:159], v[176:179], v[210:213], v[156:159]
	s_mov_b32 m0, s89
	s_nop 0
	buffer_load_dwordx4 v191, s[20:23], s36 offen lds
	ds_read_b128 v[206:209], v186 offset:43008
	s_waitcnt vmcnt(10)
	v_cvt_pk_bf16_f32 v15, v14, v15
	v_cvt_pk_bf16_f32 v14, v12, v13
	v_mfma_f32_16x16x32_bf16 v[152:155], v[180:183], v[210:213], v[152:155]
	ds_write_b64 v185, v[14:15]
	v_mfma_f32_16x16x32_bf16 v[148:151], v[198:201], v[210:213], v[148:151]
	s_mov_b32 m0, s90
	s_nop 0
	buffer_load_dwordx4 v190, s[20:23], s36 offen lds
	v_mfma_f32_16x16x32_bf16 v[144:147], v[202:205], v[210:213], v[144:147]
	s_waitcnt lgkmcnt(2)
	v_mfma_f32_16x16x32_bf16 v[132:135], v[176:179], v[214:217], v[132:135]
	s_mov_b32 m0, s91
	s_nop 0
	buffer_load_dwordx4 v193, s[20:23], s36 offen lds
	ds_read_b128 v[210:213], v186 offset:45056
	v_mfma_f32_16x16x32_bf16 v[124:127], v[180:183], v[214:217], v[124:127]
	v_mfma_f32_16x16x32_bf16 v[120:123], v[198:201], v[214:217], v[120:123]
	v_mfma_f32_16x16x32_bf16 v[140:143], v[202:205], v[214:217], v[140:143]
	s_waitcnt lgkmcnt(2)
; #define G_DMA_A(kt, AO) do { G_DMA1(kt, AO, 0); G_DMA1(kt, AO, 1); G_DMA1(kt, AO, 2); G_DMA1(kt, AO, 3); if (MF == 9) G_DMA5(kt, AO); } while (0)
; #define G_ISSUE_B(kt) do { const unsigned _sb = (unsigned)(kt) * 4u * kstepB; \
;         _Pragma("unroll") for (int _i = 0; _i < 8; ++_i) sb[_i] = bload16(_i < 4 ? rsB0 : rsB1, vob, _sb + (_i & 3) * kstepB); } while (0)
; #define G_WRITE_B(BO) do { \
;         _Pragma("unroll") for (int _i = 0; _i < 8; ++_i) *(LAS u32x2*)(b_wr + (BO) + (_i & 3) * (16 * G_BSTRIDE) + (_i >> 2) * SLAB1) = pack4(__builtin_bit_cast(f32x4, sb[_i])); } while (0)
; #define G_ENDTILE(VM) do { asm volatile("s_waitcnt vmcnt(" #VM ")" ::: "memory"); \
;         asm volatile("s_waitcnt lgkmcnt(0)" ::: "memory"); __builtin_amdgcn_s_barrier(); asm volatile("" ::: "memory"); } while (0)
;     ...
;     __builtin_amdgcn_s_barrier();
;     G_DMA_A(0, G_A0); G_ISSUE_B(0); G_WRITE_B(G_B0);
;     __builtin_amdgcn_sched_barrier(0);
;     G_ISSUE_B(1);
;     __builtin_amdgcn_sched_barrier(0);
;     G_ENDTILE(8);
;     for (int ui = 0;; ++ui) {
; #pragma unroll
;         for (int m = 0; m < MF; ++m)
; #pragma unroll
;             for (int n = 0; n < 4; ++n) acc[m][n] = (f32x4){0.f, 0.f, 0.f, 0.f};
;         for (int t = 0; t < nt - 2; t += 2) {
;             G_TILE(G_A0, G_B0, true, G_B1, G_A1, t + 1, true, t + 2, (void)0);
;             G_ENDTILE(8);
;             G_TILE(G_A1, G_B1, true, G_B0, G_A0, t + 2, true, t + 3, (void)0);
;             G_ENDTILE(8);
;         }
	v_mfma_f32_16x16x32_bf16 v[136:139], v[176:179], v[206:209], v[136:139]
	ds_read_b128 v[214:217], v186 offset:47104
	buffer_load_dwordx4 v[12:15], v184, s[24:27], s37 offen
	s_waitcnt vmcnt(12)
	v_cvt_pk_bf16_f32 v3, v2, v3
	v_cvt_pk_bf16_f32 v2, v0, v1
	v_mfma_f32_16x16x32_bf16 v[128:131], v[180:183], v[206:209], v[128:131]
	ds_write_b64 v185, v[2:3] offset:8704
	v_mfma_f32_16x16x32_bf16 v[116:119], v[198:201], v[206:209], v[116:119]
	v_mfma_f32_16x16x32_bf16 v[112:115], v[202:205], v[206:209], v[112:115]
	s_add_i32 s38, s17, 0xfffc0000
	s_waitcnt lgkmcnt(2)
	v_mfma_f32_16x16x32_bf16 v[100:103], v[176:179], v[210:213], v[100:103]
	ds_read_b128 v[206:209], v186 offset:49152
	v_mfma_f32_16x16x32_bf16 v[92:95], v[180:183], v[210:213], v[92:95]
	v_mfma_f32_16x16x32_bf16 v[88:91], v[198:201], v[210:213], v[88:91]
	v_mfma_f32_16x16x32_bf16 v[108:111], v[202:205], v[210:213], v[108:111]
	s_waitcnt lgkmcnt(2)
	v_mfma_f32_16x16x32_bf16 v[104:107], v[176:179], v[214:217], v[104:107]
	ds_read_b128 v[210:213], v186 offset:51200
	buffer_load_dwordx4 v[0:3], v184, s[24:27], s38 offen
	s_waitcnt vmcnt(12)
	v_cvt_pk_bf16_f32 v31, v30, v31
	v_cvt_pk_bf16_f32 v30, v28, v29
	v_mfma_f32_16x16x32_bf16 v[96:99], v[180:183], v[214:217], v[96:99]
	ds_write_b64 v185, v[30:31] offset:17408
	v_mfma_f32_16x16x32_bf16 v[84:87], v[198:201], v[214:217], v[84:87]
	v_mfma_f32_16x16x32_bf16 v[80:83], v[202:205], v[214:217], v[80:83]
	s_add_i32 s39, s17, 0xfffe0000
	s_waitcnt lgkmcnt(2)
	v_mfma_f32_16x16x32_bf16 v[72:75], v[176:179], v[206:209], v[72:75]
	ds_read_b128 v[214:217], v186 offset:53248
	v_mfma_f32_16x16x32_bf16 v[64:67], v[180:183], v[206:209], v[64:67]
	v_mfma_f32_16x16x32_bf16 v[60:63], v[198:201], v[206:209], v[60:63]
	v_mfma_f32_16x16x32_bf16 v[76:79], v[202:205], v[206:209], v[76:79]
	s_waitcnt lgkmcnt(2)
	v_mfma_f32_16x16x32_bf16 v[68:71], v[176:179], v[210:213], v[68:71]
	ds_read_b128 v[206:209], v186 offset:37888
	buffer_load_dwordx4 v[28:31], v184, s[24:27], s39 offen
	s_waitcnt vmcnt(12)
	v_cvt_pk_bf16_f32 v27, v26, v27
	v_cvt_pk_bf16_f32 v26, v24, v25
	v_mfma_f32_16x16x32_bf16 v[56:59], v[180:183], v[210:213], v[56:59]
	ds_write_b64 v185, v[26:27] offset:26112
	v_mfma_f32_16x16x32_bf16 v[52:55], v[198:201], v[210:213], v[52:55]
	v_mfma_f32_16x16x32_bf16 v[48:51], v[202:205], v[210:213], v[48:51]
	ds_read_b128 v[210:213], v186 offset:39936
	s_waitcnt lgkmcnt(3)
	v_mfma_f32_16x16x32_bf16 v[44:47], v[176:179], v[214:217], v[44:47]
	ds_read_b64_tr_b16 v[246:247], v188 offset:52224
	ds_read_b64_tr_b16 v[220:221], v188 offset:52256
	ds_read_b64_tr_b16 v[244:245], v187 offset:52224
	ds_read_b64_tr_b16 v[218:219], v187 offset:52256
	v_mfma_f32_16x16x32_bf16 v[40:43], v[180:183], v[214:217], v[40:43]
	ds_read_b64_tr_b16 v[248:249], v187 offset:52288
	ds_read_b64_tr_b16 v[250:251], v188 offset:52288
	v_mfma_f32_16x16x32_bf16 v[36:39], v[198:201], v[214:217], v[36:39]
	ds_read_b64_tr_b16 v[252:253], v187 offset:52320
	ds_read_b64_tr_b16 v[254:255], v188 offset:52320
	v_mfma_f32_16x16x32_bf16 v[32:35], v[202:205], v[214:217], v[32:35]
	s_waitcnt lgkmcnt(5)
	v_mfma_f32_16x16x32_bf16 v[172:175], v[244:247], v[206:209], v[172:175]
	ds_read_b128 v[202:205], v186 offset:41984
	buffer_load_dwordx4 v[24:27], v184, s[24:27], s17 offen
	s_waitcnt vmcnt(12)
	v_cvt_pk_bf16_f32 v23, v22, v23
	v_cvt_pk_bf16_f32 v22, v20, v21
	s_waitcnt lgkmcnt(5)
	v_mfma_f32_16x16x32_bf16 v[168:171], v[218:221], v[206:209], v[168:171]
	ds_write_b64 v185, v[22:23] offset:64
	s_waitcnt lgkmcnt(4)
	v_mfma_f32_16x16x32_bf16 v[164:167], v[248:251], v[206:209], v[164:167]
	s_waitcnt lgkmcnt(2)
	v_mfma_f32_16x16x32_bf16 v[160:163], v[252:255], v[206:209], v[160:163]
	v_mfma_f32_16x16x32_bf16 v[156:159], v[244:247], v[210:213], v[156:159]
	ds_read_b128 v[206:209], v186 offset:44032
	v_mfma_f32_16x16x32_bf16 v[152:155], v[218:221], v[210:213], v[152:155]
	v_mfma_f32_16x16x32_bf16 v[148:151], v[248:251], v[210:213], v[148:151]
	v_mfma_f32_16x16x32_bf16 v[144:147], v[252:255], v[210:213], v[144:147]
	s_waitcnt lgkmcnt(2)
	v_mfma_f32_16x16x32_bf16 v[132:135], v[244:247], v[202:205], v[132:135]
	ds_read_b128 v[210:213], v186 offset:46080
	buffer_load_dwordx4 v[20:23], v184, s[28:31], s37 offen
	s_waitcnt vmcnt(12)
	v_cvt_pk_bf16_f32 v7, v6, v7
	v_cvt_pk_bf16_f32 v6, v4, v5
	v_mfma_f32_16x16x32_bf16 v[124:127], v[218:221], v[202:205], v[124:127]
	ds_write_b64 v185, v[6:7] offset:8768
	v_mfma_f32_16x16x32_bf16 v[120:123], v[248:251], v[202:205], v[120:123]
	v_mfma_f32_16x16x32_bf16 v[140:143], v[252:255], v[202:205], v[140:143]
	s_waitcnt lgkmcnt(2)
	v_mfma_f32_16x16x32_bf16 v[136:139], v[244:247], v[206:209], v[136:139]
	ds_read_b128 v[202:205], v186 offset:48128
	v_mfma_f32_16x16x32_bf16 v[128:131], v[218:221], v[206:209], v[128:131]
	v_mfma_f32_16x16x32_bf16 v[116:119], v[248:251], v[206:209], v[116:119]
	v_mfma_f32_16x16x32_bf16 v[112:115], v[252:255], v[206:209], v[112:115]
	s_waitcnt lgkmcnt(2)
	v_mfma_f32_16x16x32_bf16 v[100:103], v[244:247], v[210:213], v[100:103]
	ds_read_b128 v[206:209], v186 offset:50176
	buffer_load_dwordx4 v[4:7], v184, s[28:31], s38 offen
	s_waitcnt vmcnt(12)
	v_cvt_pk_bf16_f32 v11, v10, v11
	v_cvt_pk_bf16_f32 v10, v8, v9
	v_mfma_f32_16x16x32_bf16 v[92:95], v[218:221], v[210:213], v[92:95]
	ds_write_b64 v185, v[10:11] offset:17472
	v_mfma_f32_16x16x32_bf16 v[88:91], v[248:251], v[210:213], v[88:91]
	v_mfma_f32_16x16x32_bf16 v[108:111], v[252:255], v[210:213], v[108:111]
	s_waitcnt lgkmcnt(2)
	v_mfma_f32_16x16x32_bf16 v[104:107], v[244:247], v[202:205], v[104:107]
	ds_read_b128 v[210:213], v186 offset:52224
	v_mfma_f32_16x16x32_bf16 v[96:99], v[218:221], v[202:205], v[96:99]
	v_mfma_f32_16x16x32_bf16 v[84:87], v[248:251], v[202:205], v[84:87]
	v_mfma_f32_16x16x32_bf16 v[80:83], v[252:255], v[202:205], v[80:83]
	s_waitcnt lgkmcnt(2)
	v_mfma_f32_16x16x32_bf16 v[72:75], v[244:247], v[206:209], v[72:75]
	ds_read_b128 v[238:241], v186 offset:54272
	buffer_load_dwordx4 v[8:11], v184, s[28:31], s39 offen
	s_waitcnt vmcnt(12)
	v_cvt_pk_bf16_f32 v19, v18, v19
	v_cvt_pk_bf16_f32 v18, v16, v17
	v_mfma_f32_16x16x32_bf16 v[64:67], v[218:221], v[206:209], v[64:67]
	ds_write_b64 v185, v[18:19] offset:26176
	v_mfma_f32_16x16x32_bf16 v[60:63], v[248:251], v[206:209], v[60:63]
	v_mfma_f32_16x16x32_bf16 v[76:79], v[252:255], v[206:209], v[76:79]
	s_waitcnt lgkmcnt(2)
	v_mfma_f32_16x16x32_bf16 v[68:71], v[244:247], v[210:213], v[68:71]
	v_mfma_f32_16x16x32_bf16 v[56:59], v[218:221], v[210:213], v[56:59]
	v_mfma_f32_16x16x32_bf16 v[52:55], v[248:251], v[210:213], v[52:55]
	v_mfma_f32_16x16x32_bf16 v[48:51], v[252:255], v[210:213], v[48:51]
	s_waitcnt lgkmcnt(1)
	buffer_load_dwordx4 v[16:19], v184, s[28:31], s17 offen
	s_waitcnt vmcnt(8)
	s_waitcnt lgkmcnt(0)
	s_barrier
	s_add_i32 s16, s16, 2
	s_add_i32 s17, s17, 0x100000
	s_addk_i32 s36, 0x100
	s_cmp_ge_i32 s16, s97
	s_cbranch_scc1 .Lflush_P5

.Lflush_P5:
	v_mfma_f32_16x16x32_bf16 v[44:47], v[244:247], v[238:241], v[44:47]
	v_mfma_f32_16x16x32_bf16 v[40:43], v[218:221], v[238:241], v[40:43]
	v_mfma_f32_16x16x32_bf16 v[36:39], v[248:251], v[238:241], v[36:39]
	v_mfma_f32_16x16x32_bf16 v[32:35], v[252:255], v[238:241], v[32:35]
	s_branch .LBB0_653

;     ...
;         for (int m = 0; m < MF; ++m)
; #pragma unroll
;             for (int n = 0; n < 4; ++n) acc[m][n] = (f32x4){0.f, 0.f, 0.f, 0.f};
.Lslow_P5:
	v_mov_b32_e32 v32, 0
	v_mov_b32_e32 v33, v32
	v_mov_b32_e32 v34, v32
	v_mov_b32_e32 v35, v32
	v_mov_b32_e32 v36, v32
	v_mov_b32_e32 v37, v32
	v_mov_b32_e32 v38, v32
	v_mov_b32_e32 v39, v32
	v_mov_b32_e32 v40, v32
	v_mov_b32_e32 v41, v32
	v_mov_b32_e32 v42, v32
	v_mov_b32_e32 v43, v32
	v_mov_b32_e32 v44, v32
	v_mov_b32_e32 v45, v32
	v_mov_b32_e32 v46, v32
	v_mov_b32_e32 v47, v32
	v_mov_b32_e32 v48, v32
	v_mov_b32_e32 v49, v32
	v_mov_b32_e32 v50, v32
	v_mov_b32_e32 v51, v32
	v_mov_b32_e32 v52, v32
	v_mov_b32_e32 v53, v32
	v_mov_b32_e32 v54, v32
	v_mov_b32_e32 v55, v32
	v_mov_b32_e32 v56, v32
	v_mov_b32_e32 v57, v32
	v_mov_b32_e32 v58, v32
	v_mov_b32_e32 v59, v32
	v_mov_b32_e32 v68, v32
	v_mov_b32_e32 v69, v32
	v_mov_b32_e32 v70, v32
	v_mov_b32_e32 v71, v32
	v_mov_b32_e32 v76, v32
	v_mov_b32_e32 v77, v32
	v_mov_b32_e32 v78, v32
	v_mov_b32_e32 v79, v32
	v_mov_b32_e32 v60, v32
	v_mov_b32_e32 v61, v32
	v_mov_b32_e32 v62, v32
	v_mov_b32_e32 v63, v32
	v_mov_b32_e32 v64, v32
	v_mov_b32_e32 v65, v32
	v_mov_b32_e32 v66, v32
	v_mov_b32_e32 v67, v32
	v_mov_b32_e32 v72, v32
	v_mov_b32_e32 v73, v32
	v_mov_b32_e32 v74, v32
	v_mov_b32_e32 v75, v32
	v_mov_b32_e32 v80, v32
	v_mov_b32_e32 v81, v32
	v_mov_b32_e32 v82, v32
	v_mov_b32_e32 v83, v32
	v_mov_b32_e32 v84, v32
	v_mov_b32_e32 v85, v32
	v_mov_b32_e32 v86, v32
	v_mov_b32_e32 v87, v32
	v_mov_b32_e32 v96, v32
	v_mov_b32_e32 v97, v32
	v_mov_b32_e32 v98, v32
	v_mov_b32_e32 v99, v32
	v_mov_b32_e32 v104, v32
	v_mov_b32_e32 v105, v32
	v_mov_b32_e32 v106, v32
	v_mov_b32_e32 v107, v32
	v_mov_b32_e32 v108, v32
	v_mov_b32_e32 v109, v32
	v_mov_b32_e32 v110, v32
	v_mov_b32_e32 v111, v32
	v_mov_b32_e32 v88, v32
	v_mov_b32_e32 v89, v32
	v_mov_b32_e32 v90, v32
	v_mov_b32_e32 v91, v32
	v_mov_b32_e32 v92, v32
	v_mov_b32_e32 v93, v32
	v_mov_b32_e32 v94, v32
	v_mov_b32_e32 v95, v32
	v_mov_b32_e32 v100, v32
	v_mov_b32_e32 v101, v32
	v_mov_b32_e32 v102, v32
	v_mov_b32_e32 v103, v32
	v_mov_b32_e32 v112, v32
	v_mov_b32_e32 v113, v32
	v_mov_b32_e32 v114, v32
	v_mov_b32_e32 v115, v32
	v_mov_b32_e32 v116, v32
	v_mov_b32_e32 v117, v32
	v_mov_b32_e32 v118, v32
	v_mov_b32_e32 v119, v32
	v_mov_b32_e32 v128, v32
	v_mov_b32_e32 v129, v32
	v_mov_b32_e32 v130, v32
	v_mov_b32_e32 v131, v32
	v_mov_b32_e32 v136, v32
	v_mov_b32_e32 v137, v32
	v_mov_b32_e32 v138, v32
	v_mov_b32_e32 v139, v32
	v_mov_b32_e32 v140, v32
	v_mov_b32_e32 v141, v32
	v_mov_b32_e32 v142, v32
	v_mov_b32_e32 v143, v32
	v_mov_b32_e32 v120, v32
	v_mov_b32_e32 v121, v32
	v_mov_b32_e32 v122, v32
	v_mov_b32_e32 v123, v32
	v_mov_b32_e32 v124, v32
	v_mov_b32_e32 v125, v32
	v_mov_b32_e32 v126, v32
	v_mov_b32_e32 v127, v32
	v_mov_b32_e32 v132, v32
	v_mov_b32_e32 v133, v32
	v_mov_b32_e32 v134, v32
	v_mov_b32_e32 v135, v32
	v_mov_b32_e32 v144, v32
	v_mov_b32_e32 v145, v32
	v_mov_b32_e32 v146, v32
	v_mov_b32_e32 v147, v32
	v_mov_b32_e32 v148, v32
	v_mov_b32_e32 v149, v32
	v_mov_b32_e32 v150, v32
	v_mov_b32_e32 v151, v32
	v_mov_b32_e32 v152, v32
	v_mov_b32_e32 v153, v32
	v_mov_b32_e32 v154, v32
	v_mov_b32_e32 v155, v32
	v_mov_b32_e32 v156, v32
	v_mov_b32_e32 v157, v32
	v_mov_b32_e32 v158, v32
	v_mov_b32_e32 v159, v32
	v_mov_b32_e32 v160, v32
	v_mov_b32_e32 v161, v32
	v_mov_b32_e32 v162, v32
	v_mov_b32_e32 v163, v32
	v_mov_b32_e32 v164, v32
	v_mov_b32_e32 v165, v32
	v_mov_b32_e32 v166, v32
	v_mov_b32_e32 v167, v32
	v_mov_b32_e32 v168, v32
	v_mov_b32_e32 v169, v32
	v_mov_b32_e32 v170, v32
	v_mov_b32_e32 v171, v32
	v_mov_b32_e32 v172, v32
	v_mov_b32_e32 v173, v32
	v_mov_b32_e32 v174, v32
	v_mov_b32_e32 v175, v32
	v_mov_b32_e32 v218, 0
	v_mov_b32_e32 v219, 0
	v_mov_b32_e32 v220, 0
	v_mov_b32_e32 v221, 0
	v_mov_b32_e32 v238, 0
	v_mov_b32_e32 v239, 0
	v_mov_b32_e32 v240, 0
	v_mov_b32_e32 v241, 0
	v_mov_b32_e32 v244, 0
	v_mov_b32_e32 v245, 0
	v_mov_b32_e32 v246, 0
	v_mov_b32_e32 v247, 0
	v_mov_b32_e32 v248, 0
	v_mov_b32_e32 v249, 0
	v_mov_b32_e32 v250, 0
	v_mov_b32_e32 v251, 0
	v_mov_b32_e32 v252, 0
	v_mov_b32_e32 v253, 0
	v_mov_b32_e32 v254, 0
	v_mov_b32_e32 v255, 0
	s_branch .Lchk5_loop

; #define G_DMA_A(kt, AO) do { G_DMA1(kt, AO, 0); G_DMA1(kt, AO, 1); G_DMA1(kt, AO, 2); G_DMA1(kt, AO, 3); if (MF == 9) G_DMA5(kt, AO); } while (0)
; #define G_ISSUE_B(kt) do { const unsigned _sb = (unsigned)(kt) * 4u * kstepB; \
;         _Pragma("unroll") for (int _i = 0; _i < 8; ++_i) sb[_i] = bload16(_i < 4 ? rsB0 : rsB1, vob, _sb + (_i & 3) * kstepB); } while (0)
; #define G_WRITE_B(BO) do { \
;         _Pragma("unroll") for (int _i = 0; _i < 8; ++_i) *(LAS u32x2*)(b_wr + (BO) + (_i & 3) * (16 * G_BSTRIDE) + (_i >> 2) * SLAB1) = pack4(__builtin_bit_cast(f32x4, sb[_i])); } while (0)
; #define G_ENDTILE(VM) do { asm volatile("s_waitcnt vmcnt(" #VM ")" ::: "memory"); \
;         asm volatile("s_waitcnt lgkmcnt(0)" ::: "memory"); __builtin_amdgcn_s_barrier(); asm volatile("" ::: "memory"); } while (0)
;     ...
;     __builtin_amdgcn_s_barrier();
;     G_DMA_A(0, G_A0); G_ISSUE_B(0); G_WRITE_B(G_B0);
;     __builtin_amdgcn_sched_barrier(0);
;     G_ISSUE_B(1);
;     __builtin_amdgcn_sched_barrier(0);
;     G_ENDTILE(8);
;     for (int ui = 0;; ++ui) {
; #pragma unroll
;         for (int m = 0; m < MF; ++m)
; #pragma unroll
;             for (int n = 0; n < 4; ++n) acc[m][n] = (f32x4){0.f, 0.f, 0.f, 0.f};
;         for (int t = 0; t < nt - 2; t += 2) {
;             G_TILE(G_A0, G_B0, true, G_B1, G_A1, t + 1, true, t + 2, (void)0);
.LBB0_861:
	s_andn2_b64 vcc, exec, s[28:29]
	v_mov_b32_e32 v175, 0
	s_cbranch_vccnz .LBB0_864
	s_mov_b32 s8, 0
	s_mov_b32 s9, 0x1e0000
	s_movk_i32 s36, 0x100
	s_waitcnt vmcnt(1)
	s_waitcnt vmcnt(0)
	s_cmp_lt_u32 s99, 9
	s_cbranch_scc1 .Lslow_P6
	s_mov_b32 m0, s85
	s_add_i32 s38, s36, 0xffffff80
	ds_read_b64_tr_b16 v[178:179], v206
	ds_read_b64_tr_b16 v[176:177], v205
	ds_read_b64_tr_b16 v[180:181], v205 offset:32
	ds_read_b64_tr_b16 v[184:185], v205 offset:64
	ds_read_b64_tr_b16 v[188:189], v205 offset:96
	ds_read_b128 v[192:195], v199
	ds_read_b64_tr_b16 v[182:183], v206 offset:32
	ds_read_b64_tr_b16 v[186:187], v206 offset:64
	ds_read_b64_tr_b16 v[190:191], v206 offset:96
	ds_read_b128 v[208:211], v199 offset:2048
	ds_read_b128 v[212:215], v199 offset:4096
	buffer_load_dwordx4 v200, s[20:23], s38 offen lds
	s_mov_b32 m0, s86
	s_waitcnt lgkmcnt(0)
	v_mfma_f32_16x16x32_bf16 v[172:175], v[176:179], v[192:195], 0
	buffer_load_dwordx4 v201, s[20:23], s38 offen lds
	v_mfma_f32_16x16x32_bf16 v[168:171], v[180:183], v[192:195], 0
	v_mfma_f32_16x16x32_bf16 v[164:167], v[184:187], v[192:195], 0
	v_mfma_f32_16x16x32_bf16 v[160:163], v[188:191], v[192:195], 0
	v_mfma_f32_16x16x32_bf16 v[156:159], v[176:179], v[208:211], 0
	s_mov_b32 m0, s87
	s_nop 0
	buffer_load_dwordx4 v202, s[20:23], s38 offen lds
	ds_read_b128 v[192:195], v199 offset:6144
	s_waitcnt vmcnt(10)
	v_cvt_pk_bf16_f32 v23, v22, v23
	v_cvt_pk_bf16_f32 v22, v20, v21
	v_mfma_f32_16x16x32_bf16 v[152:155], v[180:183], v[208:211], 0
	ds_write_b64 v198, v[22:23] offset:34816
	v_mfma_f32_16x16x32_bf16 v[148:151], v[184:187], v[208:211], 0
	s_mov_b32 m0, s88
	s_nop 0
	buffer_load_dwordx4 v203, s[20:23], s38 offen lds
	v_mfma_f32_16x16x32_bf16 v[144:147], v[188:191], v[208:211], 0
	v_mfma_f32_16x16x32_bf16 v[132:135], v[176:179], v[212:215], 0
	s_mov_b32 m0, s89
	s_nop 0
	buffer_load_dwordx4 v204, s[20:23], s38 offen lds
	s_add_i32 s38, s9, 0xfff20000
	ds_read_b128 v[208:211], v199 offset:8192
	v_mfma_f32_16x16x32_bf16 v[124:127], v[180:183], v[212:215], 0
	v_mfma_f32_16x16x32_bf16 v[120:123], v[184:187], v[212:215], 0
	v_mfma_f32_16x16x32_bf16 v[140:143], v[188:191], v[212:215], 0
	s_waitcnt lgkmcnt(2)
	v_mfma_f32_16x16x32_bf16 v[136:139], v[176:179], v[192:195], 0
	ds_read_b128 v[212:215], v199 offset:10240
	buffer_load_dwordx4 v[20:23], v197, s[24:27], s38 offen
	s_waitcnt vmcnt(11)
	v_cvt_pk_bf16_f32 v31, v30, v31
	v_cvt_pk_bf16_f32 v30, v28, v29
	v_mfma_f32_16x16x32_bf16 v[128:131], v[180:183], v[192:195], 0
	ds_write_b64 v198, v[30:31] offset:43520
	v_mfma_f32_16x16x32_bf16 v[116:119], v[184:187], v[192:195], 0
	v_mfma_f32_16x16x32_bf16 v[112:115], v[188:191], v[192:195], 0
	s_add_i32 s39, s9, 0xfff40000
	s_waitcnt lgkmcnt(2)
	v_mfma_f32_16x16x32_bf16 v[100:103], v[176:179], v[208:211], 0
	ds_read_b128 v[192:195], v199 offset:12288
	v_mfma_f32_16x16x32_bf16 v[92:95], v[180:183], v[208:211], 0
	v_mfma_f32_16x16x32_bf16 v[88:91], v[184:187], v[208:211], 0
	v_mfma_f32_16x16x32_bf16 v[108:111], v[188:191], v[208:211], 0
	s_waitcnt lgkmcnt(2)
	v_mfma_f32_16x16x32_bf16 v[104:107], v[176:179], v[212:215], 0
	ds_read_b128 v[208:211], v199 offset:14336
	v_cvt_pk_bf16_f32 v19, v18, v19
	v_cvt_pk_bf16_f32 v18, v16, v17
	v_mfma_f32_16x16x32_bf16 v[96:99], v[180:183], v[212:215], 0
	ds_write_b64 v198, v[18:19] offset:52224
	v_mfma_f32_16x16x32_bf16 v[84:87], v[184:187], v[212:215], 0
	v_mfma_f32_16x16x32_bf16 v[80:83], v[188:191], v[212:215], 0
	s_add_i32 s43, s9, 0xfff60000
	buffer_load_dwordx4 v[28:31], v197, s[24:27], s39 offen
	s_waitcnt lgkmcnt(2)
	v_mfma_f32_16x16x32_bf16 v[72:75], v[176:179], v[192:195], 0
	ds_read_b128 v[212:215], v199 offset:16384
	v_mfma_f32_16x16x32_bf16 v[64:67], v[180:183], v[192:195], 0
	v_mfma_f32_16x16x32_bf16 v[60:63], v[184:187], v[192:195], 0
	v_mfma_f32_16x16x32_bf16 v[76:79], v[188:191], v[192:195], 0
	s_waitcnt lgkmcnt(2)
	v_mfma_f32_16x16x32_bf16 v[68:71], v[176:179], v[208:211], 0
	ds_read_b128 v[192:195], v199 offset:1024
	buffer_load_dwordx4 v[16:19], v197, s[24:27], s43 offen
	s_waitcnt vmcnt(12)
	v_cvt_pk_bf16_f32 v27, v26, v27
	v_cvt_pk_bf16_f32 v26, v24, v25
	v_mfma_f32_16x16x32_bf16 v[56:59], v[180:183], v[208:211], 0
	ds_write_b64 v198, v[26:27] offset:60928
	v_mfma_f32_16x16x32_bf16 v[52:55], v[184:187], v[208:211], 0
	v_mfma_f32_16x16x32_bf16 v[48:51], v[188:191], v[208:211], 0
	s_add_i32 s45, s9, 0xfff80000
	ds_read_b128 v[208:211], v199 offset:3072
	s_waitcnt lgkmcnt(3)
	v_mfma_f32_16x16x32_bf16 v[44:47], v[176:179], v[212:215], 0
	ds_read_b64_tr_b16 v[246:247], v206 offset:17408
	ds_read_b64_tr_b16 v[218:219], v206 offset:17440
	ds_read_b64_tr_b16 v[244:245], v205 offset:17408
	ds_read_b64_tr_b16 v[216:217], v205 offset:17440
	v_mfma_f32_16x16x32_bf16 v[40:43], v[180:183], v[212:215], 0
	ds_read_b64_tr_b16 v[248:249], v205 offset:17472
	ds_read_b64_tr_b16 v[250:251], v206 offset:17472
	v_mfma_f32_16x16x32_bf16 v[36:39], v[184:187], v[212:215], 0
	ds_read_b64_tr_b16 v[252:253], v205 offset:17504
	ds_read_b64_tr_b16 v[254:255], v206 offset:17504
	v_mfma_f32_16x16x32_bf16 v[32:35], v[188:191], v[212:215], 0
	s_waitcnt lgkmcnt(5)
	v_mfma_f32_16x16x32_bf16 v[172:175], v[244:247], v[192:195], v[172:175]
	ds_read_b128 v[188:191], v199 offset:5120
	buffer_load_dwordx4 v[24:27], v197, s[24:27], s45 offen
	s_waitcnt vmcnt(12)
	v_cvt_pk_bf16_f32 v15, v14, v15
	v_cvt_pk_bf16_f32 v14, v12, v13
	s_waitcnt lgkmcnt(5)
	v_mfma_f32_16x16x32_bf16 v[168:171], v[216:219], v[192:195], v[168:171]
	ds_write_b64 v198, v[14:15] offset:35072
	s_waitcnt lgkmcnt(4)
	v_mfma_f32_16x16x32_bf16 v[164:167], v[248:251], v[192:195], v[164:167]
	s_waitcnt lgkmcnt(2)
; #define G_DMA_A(kt, AO) do { G_DMA1(kt, AO, 0); G_DMA1(kt, AO, 1); G_DMA1(kt, AO, 2); G_DMA1(kt, AO, 3); if (MF == 9) G_DMA5(kt, AO); } while (0)
; #define G_ISSUE_B(kt) do { const unsigned _sb = (unsigned)(kt) * 4u * kstepB; \
;         _Pragma("unroll") for (int _i = 0; _i < 8; ++_i) sb[_i] = bload16(_i < 4 ? rsB0 : rsB1, vob, _sb + (_i & 3) * kstepB); } while (0)
; #define G_WRITE_B(BO) do { \
;         _Pragma("unroll") for (int _i = 0; _i < 8; ++_i) *(LAS u32x2*)(b_wr + (BO) + (_i & 3) * (16 * G_BSTRIDE) + (_i >> 2) * SLAB1) = pack4(__builtin_bit_cast(f32x4, sb[_i])); } while (0)
; #define G_ENDTILE(VM) do { asm volatile("s_waitcnt vmcnt(" #VM ")" ::: "memory"); \
;         asm volatile("s_waitcnt lgkmcnt(0)" ::: "memory"); __builtin_amdgcn_s_barrier(); asm volatile("" ::: "memory"); } while (0)
;     ...
;     __builtin_amdgcn_s_barrier();
;     G_DMA_A(0, G_A0); G_ISSUE_B(0); G_WRITE_B(G_B0);
;     __builtin_amdgcn_sched_barrier(0);
;     G_ISSUE_B(1);
;     __builtin_amdgcn_sched_barrier(0);
;     G_ENDTILE(8);
;     for (int ui = 0;; ++ui) {
; #pragma unroll
;         for (int m = 0; m < MF; ++m)
; #pragma unroll
;             for (int n = 0; n < 4; ++n) acc[m][n] = (f32x4){0.f, 0.f, 0.f, 0.f};
;         for (int t = 0; t < nt - 2; t += 2) {
;             G_TILE(G_A0, G_B0, true, G_B1, G_A1, t + 1, true, t + 2, (void)0);
;             G_ENDTILE(8);
;             G_TILE(G_A1, G_B1, true, G_B0, G_A0, t + 2, true, t + 3, (void)0);
	v_mfma_f32_16x16x32_bf16 v[160:163], v[252:255], v[192:195], v[160:163]
	v_mfma_f32_16x16x32_bf16 v[156:159], v[244:247], v[208:211], v[156:159]
	ds_read_b128 v[192:195], v199 offset:7168
	v_mfma_f32_16x16x32_bf16 v[152:155], v[216:219], v[208:211], v[152:155]
	v_mfma_f32_16x16x32_bf16 v[148:151], v[248:251], v[208:211], v[148:151]
	v_mfma_f32_16x16x32_bf16 v[144:147], v[252:255], v[208:211], v[144:147]
	s_waitcnt lgkmcnt(2)
	v_mfma_f32_16x16x32_bf16 v[132:135], v[244:247], v[188:191], v[132:135]
	ds_read_b128 v[208:211], v199 offset:9216
	buffer_load_dwordx4 v[12:15], v197, s[16:19], s38 offen
	s_waitcnt vmcnt(11)
	v_cvt_pk_bf16_f32 v7, v6, v7
	v_cvt_pk_bf16_f32 v6, v4, v5
	v_mfma_f32_16x16x32_bf16 v[124:127], v[216:219], v[188:191], v[124:127]
	ds_write_b64 v198, v[6:7] offset:43776
	v_mfma_f32_16x16x32_bf16 v[120:123], v[248:251], v[188:191], v[120:123]
	v_mfma_f32_16x16x32_bf16 v[140:143], v[252:255], v[188:191], v[140:143]
	s_waitcnt lgkmcnt(2)
	v_mfma_f32_16x16x32_bf16 v[136:139], v[244:247], v[192:195], v[136:139]
	ds_read_b128 v[188:191], v199 offset:11264
	v_mfma_f32_16x16x32_bf16 v[128:131], v[216:219], v[192:195], v[128:131]
	v_mfma_f32_16x16x32_bf16 v[116:119], v[248:251], v[192:195], v[116:119]
	v_mfma_f32_16x16x32_bf16 v[112:115], v[252:255], v[192:195], v[112:115]
	s_waitcnt lgkmcnt(2)
	v_mfma_f32_16x16x32_bf16 v[100:103], v[244:247], v[208:211], v[100:103]
	ds_read_b128 v[192:195], v199 offset:13312
	v_cvt_pk_bf16_f32 v3, v2, v3
	v_cvt_pk_bf16_f32 v2, v0, v1
	v_mfma_f32_16x16x32_bf16 v[92:95], v[216:219], v[208:211], v[92:95]
	ds_write_b64 v198, v[2:3] offset:52480
	v_mfma_f32_16x16x32_bf16 v[88:91], v[248:251], v[208:211], v[88:91]
	v_mfma_f32_16x16x32_bf16 v[108:111], v[252:255], v[208:211], v[108:111]
	buffer_load_dwordx4 v[4:7], v197, s[16:19], s39 offen
	s_waitcnt lgkmcnt(2)
	v_mfma_f32_16x16x32_bf16 v[104:107], v[244:247], v[188:191], v[104:107]
	ds_read_b128 v[208:211], v199 offset:15360
	v_mfma_f32_16x16x32_bf16 v[96:99], v[216:219], v[188:191], v[96:99]
	v_mfma_f32_16x16x32_bf16 v[84:87], v[248:251], v[188:191], v[84:87]
	v_mfma_f32_16x16x32_bf16 v[80:83], v[252:255], v[188:191], v[80:83]
	s_waitcnt lgkmcnt(2)
	v_mfma_f32_16x16x32_bf16 v[72:75], v[244:247], v[192:195], v[72:75]
	ds_read_b128 v[236:239], v199 offset:17408
	buffer_load_dwordx4 v[0:3], v197, s[16:19], s43 offen
	s_waitcnt vmcnt(12)
	v_cvt_pk_bf16_f32 v11, v10, v11
	v_cvt_pk_bf16_f32 v10, v8, v9
	v_mfma_f32_16x16x32_bf16 v[64:67], v[216:219], v[192:195], v[64:67]
	ds_write_b64 v198, v[10:11] offset:61184
	v_mfma_f32_16x16x32_bf16 v[60:63], v[248:251], v[192:195], v[60:63]
	v_mfma_f32_16x16x32_bf16 v[76:79], v[252:255], v[192:195], v[76:79]
	s_waitcnt lgkmcnt(2)
	v_mfma_f32_16x16x32_bf16 v[68:71], v[244:247], v[208:211], v[68:71]
	v_mfma_f32_16x16x32_bf16 v[56:59], v[216:219], v[208:211], v[56:59]
	v_mfma_f32_16x16x32_bf16 v[52:55], v[248:251], v[208:211], v[52:55]
	v_mfma_f32_16x16x32_bf16 v[48:51], v[252:255], v[208:211], v[48:51]
	s_waitcnt lgkmcnt(1)
	buffer_load_dwordx4 v[8:11], v197, s[16:19], s45 offen
	s_waitcnt vmcnt(8)
	s_mov_b32 m0, s49
	s_waitcnt lgkmcnt(0)
	s_barrier
	ds_read_b64_tr_b16 v[178:179], v206 offset:34816
	ds_read_b64_tr_b16 v[176:177], v205 offset:34816
	ds_read_b64_tr_b16 v[180:181], v205 offset:34848
	ds_read_b64_tr_b16 v[184:185], v205 offset:34880
	ds_read_b64_tr_b16 v[188:189], v205 offset:34912
	ds_read_b128 v[192:195], v199 offset:36864
	ds_read_b64_tr_b16 v[182:183], v206 offset:34848
	ds_read_b64_tr_b16 v[186:187], v206 offset:34880
	ds_read_b64_tr_b16 v[190:191], v206 offset:34912
	ds_read_b128 v[208:211], v199 offset:38912
	ds_read_b128 v[212:215], v199 offset:40960
	buffer_load_dwordx4 v200, s[20:23], s36 offen lds
	s_mov_b32 m0, s68
	v_mfma_f32_16x16x32_bf16 v[44:47], v[244:247], v[236:239], v[44:47]
	v_mfma_f32_16x16x32_bf16 v[40:43], v[216:219], v[236:239], v[40:43]
	v_mfma_f32_16x16x32_bf16 v[36:39], v[248:251], v[236:239], v[36:39]
	v_mfma_f32_16x16x32_bf16 v[32:35], v[252:255], v[236:239], v[32:35]
	s_waitcnt lgkmcnt(5)
	v_mfma_f32_16x16x32_bf16 v[172:175], v[176:179], v[192:195], v[172:175]
	buffer_load_dwordx4 v201, s[20:23], s36 offen lds
	s_add_i32 s38, s9, 0xfffa0000
	s_waitcnt lgkmcnt(4)
	v_mfma_f32_16x16x32_bf16 v[168:171], v[180:183], v[192:195], v[168:171]
	s_waitcnt lgkmcnt(3)
	v_mfma_f32_16x16x32_bf16 v[164:167], v[184:187], v[192:195], v[164:167]
	s_waitcnt lgkmcnt(2)
	v_mfma_f32_16x16x32_bf16 v[160:163], v[188:191], v[192:195], v[160:163]
	s_waitcnt lgkmcnt(1)
	v_mfma_f32_16x16x32_bf16 v[156:159], v[176:179], v[208:211], v[156:159]
	s_mov_b32 m0, s77
	s_nop 0
	buffer_load_dwordx4 v202, s[20:23], s36 offen lds
	ds_read_b128 v[192:195], v199 offset:43008
	s_waitcnt vmcnt(10)
	v_cvt_pk_bf16_f32 v23, v22, v23
	v_cvt_pk_bf16_f32 v22, v20, v21
	v_mfma_f32_16x16x32_bf16 v[152:155], v[180:183], v[208:211], v[152:155]
	ds_write_b64 v198, v[22:23]
	v_mfma_f32_16x16x32_bf16 v[148:151], v[184:187], v[208:211], v[148:151]
	s_mov_b32 m0, s78
	s_nop 0
	buffer_load_dwordx4 v203, s[20:23], s36 offen lds
	v_mfma_f32_16x16x32_bf16 v[144:147], v[188:191], v[208:211], v[144:147]
	s_waitcnt lgkmcnt(2)
	v_mfma_f32_16x16x32_bf16 v[132:135], v[176:179], v[212:215], v[132:135]
	s_mov_b32 m0, s79
	s_nop 0
	buffer_load_dwordx4 v204, s[20:23], s36 offen lds
	ds_read_b128 v[208:211], v199 offset:45056
	v_mfma_f32_16x16x32_bf16 v[124:127], v[180:183], v[212:215], v[124:127]
	v_mfma_f32_16x16x32_bf16 v[120:123], v[184:187], v[212:215], v[120:123]
	v_mfma_f32_16x16x32_bf16 v[140:143], v[188:191], v[212:215], v[140:143]
	s_waitcnt lgkmcnt(2)
; #define G_DMA_A(kt, AO) do { G_DMA1(kt, AO, 0); G_DMA1(kt, AO, 1); G_DMA1(kt, AO, 2); G_DMA1(kt, AO, 3); if (MF == 9) G_DMA5(kt, AO); } while (0)
; #define G_ISSUE_B(kt) do { const unsigned _sb = (unsigned)(kt) * 4u * kstepB; \
;         _Pragma("unroll") for (int _i = 0; _i < 8; ++_i) sb[_i] = bload16(_i < 4 ? rsB0 : rsB1, vob, _sb + (_i & 3) * kstepB); } while (0)
; #define G_WRITE_B(BO) do { \
;         _Pragma("unroll") for (int _i = 0; _i < 8; ++_i) *(LAS u32x2*)(b_wr + (BO) + (_i & 3) * (16 * G_BSTRIDE) + (_i >> 2) * SLAB1) = pack4(__builtin_bit_cast(f32x4, sb[_i])); } while (0)
; #define G_ENDTILE(VM) do { asm volatile("s_waitcnt vmcnt(" #VM ")" ::: "memory"); \
;         asm volatile("s_waitcnt lgkmcnt(0)" ::: "memory"); __builtin_amdgcn_s_barrier(); asm volatile("" ::: "memory"); } while (0)
;     ...
;     __builtin_amdgcn_s_barrier();
;     G_DMA_A(0, G_A0); G_ISSUE_B(0); G_WRITE_B(G_B0);
;     __builtin_amdgcn_sched_barrier(0);
;     G_ISSUE_B(1);
;     __builtin_amdgcn_sched_barrier(0);
;     G_ENDTILE(8);
;     for (int ui = 0;; ++ui) {
; #pragma unroll
;         for (int m = 0; m < MF; ++m)
; #pragma unroll
;             for (int n = 0; n < 4; ++n) acc[m][n] = (f32x4){0.f, 0.f, 0.f, 0.f};
;         for (int t = 0; t < nt - 2; t += 2) {
;             G_TILE(G_A0, G_B0, true, G_B1, G_A1, t + 1, true, t + 2, (void)0);
;             G_ENDTILE(8);
;             G_TILE(G_A1, G_B1, true, G_B0, G_A0, t + 2, true, t + 3, (void)0);
;             G_ENDTILE(8);
;         }
	v_mfma_f32_16x16x32_bf16 v[136:139], v[176:179], v[192:195], v[136:139]
	ds_read_b128 v[212:215], v199 offset:47104
	buffer_load_dwordx4 v[20:23], v197, s[24:27], s38 offen
	s_waitcnt vmcnt(12)
	v_cvt_pk_bf16_f32 v31, v30, v31
	v_cvt_pk_bf16_f32 v30, v28, v29
	v_mfma_f32_16x16x32_bf16 v[128:131], v[180:183], v[192:195], v[128:131]
	ds_write_b64 v198, v[30:31] offset:8704
	v_mfma_f32_16x16x32_bf16 v[116:119], v[184:187], v[192:195], v[116:119]
	v_mfma_f32_16x16x32_bf16 v[112:115], v[188:191], v[192:195], v[112:115]
	s_add_i32 s39, s9, 0xfffc0000
	s_waitcnt lgkmcnt(2)
	v_mfma_f32_16x16x32_bf16 v[100:103], v[176:179], v[208:211], v[100:103]
	ds_read_b128 v[192:195], v199 offset:49152
	v_mfma_f32_16x16x32_bf16 v[92:95], v[180:183], v[208:211], v[92:95]
	v_mfma_f32_16x16x32_bf16 v[88:91], v[184:187], v[208:211], v[88:91]
	v_mfma_f32_16x16x32_bf16 v[108:111], v[188:191], v[208:211], v[108:111]
	s_waitcnt lgkmcnt(2)
	v_mfma_f32_16x16x32_bf16 v[104:107], v[176:179], v[212:215], v[104:107]
	ds_read_b128 v[208:211], v199 offset:51200
	buffer_load_dwordx4 v[28:31], v197, s[24:27], s39 offen
	s_waitcnt vmcnt(12)
	v_cvt_pk_bf16_f32 v19, v18, v19
	v_cvt_pk_bf16_f32 v18, v16, v17
	v_mfma_f32_16x16x32_bf16 v[96:99], v[180:183], v[212:215], v[96:99]
	ds_write_b64 v198, v[18:19] offset:17408
	v_mfma_f32_16x16x32_bf16 v[84:87], v[184:187], v[212:215], v[84:87]
	v_mfma_f32_16x16x32_bf16 v[80:83], v[188:191], v[212:215], v[80:83]
	s_add_i32 s43, s9, 0xfffe0000
	s_waitcnt lgkmcnt(2)
	v_mfma_f32_16x16x32_bf16 v[72:75], v[176:179], v[192:195], v[72:75]
	ds_read_b128 v[212:215], v199 offset:53248
	v_mfma_f32_16x16x32_bf16 v[64:67], v[180:183], v[192:195], v[64:67]
	v_mfma_f32_16x16x32_bf16 v[60:63], v[184:187], v[192:195], v[60:63]
	v_mfma_f32_16x16x32_bf16 v[76:79], v[188:191], v[192:195], v[76:79]
	s_waitcnt lgkmcnt(2)
	v_mfma_f32_16x16x32_bf16 v[68:71], v[176:179], v[208:211], v[68:71]
	ds_read_b128 v[192:195], v199 offset:37888
	buffer_load_dwordx4 v[16:19], v197, s[24:27], s43 offen
	s_waitcnt vmcnt(12)
	v_cvt_pk_bf16_f32 v27, v26, v27
	v_cvt_pk_bf16_f32 v26, v24, v25
	v_mfma_f32_16x16x32_bf16 v[56:59], v[180:183], v[208:211], v[56:59]
	ds_write_b64 v198, v[26:27] offset:26112
	v_mfma_f32_16x16x32_bf16 v[52:55], v[184:187], v[208:211], v[52:55]
	v_mfma_f32_16x16x32_bf16 v[48:51], v[188:191], v[208:211], v[48:51]
	s_waitcnt lgkmcnt(2)
	v_mfma_f32_16x16x32_bf16 v[44:47], v[176:179], v[212:215], v[44:47]
	ds_read_b128 v[176:179], v199 offset:39936
	v_mfma_f32_16x16x32_bf16 v[40:43], v[180:183], v[212:215], v[40:43]
	ds_read_b64_tr_b16 v[244:245], v205 offset:52224
	ds_read_b64_tr_b16 v[248:249], v205 offset:52256
	ds_read_b64_tr_b16 v[216:217], v205 offset:52288
	ds_read_b64_tr_b16 v[220:221], v205 offset:52320
	ds_read_b64_tr_b16 v[246:247], v206 offset:52224
	ds_read_b64_tr_b16 v[250:251], v206 offset:52256
	ds_read_b64_tr_b16 v[218:219], v206 offset:52288
	ds_read_b64_tr_b16 v[222:223], v206 offset:52320
	v_mfma_f32_16x16x32_bf16 v[36:39], v[184:187], v[212:215], v[36:39]
	v_mfma_f32_16x16x32_bf16 v[32:35], v[188:191], v[212:215], v[32:35]
	s_waitcnt lgkmcnt(3)
	v_mfma_f32_16x16x32_bf16 v[172:175], v[244:247], v[192:195], v[172:175]
	ds_read_b128 v[184:187], v199 offset:41984
	buffer_load_dwordx4 v[24:27], v197, s[24:27], s9 offen
	s_waitcnt vmcnt(12)
	v_cvt_pk_bf16_f32 v15, v14, v15
	v_cvt_pk_bf16_f32 v14, v12, v13
	s_waitcnt lgkmcnt(3)
	v_mfma_f32_16x16x32_bf16 v[168:171], v[248:251], v[192:195], v[168:171]
	ds_write_b64 v198, v[14:15] offset:256
	s_waitcnt lgkmcnt(3)
	v_mfma_f32_16x16x32_bf16 v[164:167], v[216:219], v[192:195], v[164:167]
	s_waitcnt lgkmcnt(2)
	v_mfma_f32_16x16x32_bf16 v[160:163], v[220:223], v[192:195], v[160:163]
	v_mfma_f32_16x16x32_bf16 v[156:159], v[244:247], v[176:179], v[156:159]
	ds_read_b128 v[188:191], v199 offset:44032
	v_mfma_f32_16x16x32_bf16 v[152:155], v[248:251], v[176:179], v[152:155]
	v_mfma_f32_16x16x32_bf16 v[148:151], v[216:219], v[176:179], v[148:151]
	v_mfma_f32_16x16x32_bf16 v[144:147], v[220:223], v[176:179], v[144:147]
	s_waitcnt lgkmcnt(2)
	v_mfma_f32_16x16x32_bf16 v[132:135], v[244:247], v[184:187], v[132:135]
	ds_read_b128 v[176:179], v199 offset:46080
	buffer_load_dwordx4 v[12:15], v197, s[16:19], s38 offen
	s_waitcnt vmcnt(12)
	v_cvt_pk_bf16_f32 v7, v6, v7
	v_cvt_pk_bf16_f32 v6, v4, v5
	v_mfma_f32_16x16x32_bf16 v[124:127], v[248:251], v[184:187], v[124:127]
	ds_write_b64 v198, v[6:7] offset:8960
	v_mfma_f32_16x16x32_bf16 v[120:123], v[216:219], v[184:187], v[120:123]
	v_mfma_f32_16x16x32_bf16 v[140:143], v[220:223], v[184:187], v[140:143]
	s_waitcnt lgkmcnt(2)
	v_mfma_f32_16x16x32_bf16 v[136:139], v[244:247], v[188:191], v[136:139]
	ds_read_b128 v[184:187], v199 offset:48128
	v_mfma_f32_16x16x32_bf16 v[128:131], v[248:251], v[188:191], v[128:131]
	v_mfma_f32_16x16x32_bf16 v[116:119], v[216:219], v[188:191], v[116:119]
	v_mfma_f32_16x16x32_bf16 v[112:115], v[220:223], v[188:191], v[112:115]
	s_waitcnt lgkmcnt(2)
	v_mfma_f32_16x16x32_bf16 v[100:103], v[244:247], v[176:179], v[100:103]
	ds_read_b128 v[188:191], v199 offset:50176
	buffer_load_dwordx4 v[4:7], v197, s[16:19], s39 offen
	s_waitcnt vmcnt(12)
	v_cvt_pk_bf16_f32 v3, v2, v3
	v_cvt_pk_bf16_f32 v2, v0, v1
	v_mfma_f32_16x16x32_bf16 v[92:95], v[248:251], v[176:179], v[92:95]
	ds_write_b64 v198, v[2:3] offset:17664
	v_mfma_f32_16x16x32_bf16 v[88:91], v[216:219], v[176:179], v[88:91]
	v_mfma_f32_16x16x32_bf16 v[108:111], v[220:223], v[176:179], v[108:111]
	s_waitcnt lgkmcnt(2)
	v_mfma_f32_16x16x32_bf16 v[104:107], v[244:247], v[184:187], v[104:107]
	ds_read_b128 v[176:179], v199 offset:52224
	v_mfma_f32_16x16x32_bf16 v[96:99], v[248:251], v[184:187], v[96:99]
	v_mfma_f32_16x16x32_bf16 v[84:87], v[216:219], v[184:187], v[84:87]
	v_mfma_f32_16x16x32_bf16 v[80:83], v[220:223], v[184:187], v[80:83]
	s_waitcnt lgkmcnt(2)
	v_mfma_f32_16x16x32_bf16 v[72:75], v[244:247], v[188:191], v[72:75]
	ds_read_b128 v[252:255], v199 offset:54272
	buffer_load_dwordx4 v[0:3], v197, s[16:19], s43 offen
	s_waitcnt vmcnt(12)
	v_cvt_pk_bf16_f32 v11, v10, v11
	v_cvt_pk_bf16_f32 v10, v8, v9
	v_mfma_f32_16x16x32_bf16 v[64:67], v[248:251], v[188:191], v[64:67]
	ds_write_b64 v198, v[10:11] offset:26368
	v_mfma_f32_16x16x32_bf16 v[60:63], v[216:219], v[188:191], v[60:63]
	v_mfma_f32_16x16x32_bf16 v[76:79], v[220:223], v[188:191], v[76:79]
	s_waitcnt lgkmcnt(2)
	v_mfma_f32_16x16x32_bf16 v[68:71], v[244:247], v[176:179], v[68:71]
	v_mfma_f32_16x16x32_bf16 v[56:59], v[248:251], v[176:179], v[56:59]
	v_mfma_f32_16x16x32_bf16 v[52:55], v[216:219], v[176:179], v[52:55]
	v_mfma_f32_16x16x32_bf16 v[48:51], v[220:223], v[176:179], v[48:51]
	s_waitcnt lgkmcnt(1)
	buffer_load_dwordx4 v[8:11], v197, s[16:19], s9 offen
	s_waitcnt vmcnt(8)
	s_waitcnt lgkmcnt(0)
	s_barrier
	s_add_i32 s8, s8, 2
	s_add_i32 s9, s9, 0x100000
	s_addk_i32 s36, 0x100
	s_cmp_ge_i32 s8, s84
	s_cbranch_scc1 .Lflush_P6

.Lflush_P6:
	v_mfma_f32_16x16x32_bf16 v[44:47], v[244:247], v[252:255], v[44:47]
	v_mfma_f32_16x16x32_bf16 v[40:43], v[248:251], v[252:255], v[40:43]
	v_mfma_f32_16x16x32_bf16 v[36:39], v[216:219], v[252:255], v[36:39]
	v_mfma_f32_16x16x32_bf16 v[32:35], v[220:223], v[252:255], v[32:35]
	s_branch .LBB0_865

;     ...
;         for (int m = 0; m < MF; ++m)
; #pragma unroll
;             for (int n = 0; n < 4; ++n) acc[m][n] = (f32x4){0.f, 0.f, 0.f, 0.f};
.Lslow_P6:
	v_mov_b32_e32 v32, 0
	v_mov_b32_e32 v33, v32
	v_mov_b32_e32 v34, v32
	v_mov_b32_e32 v35, v32
	v_mov_b32_e32 v36, v32
	v_mov_b32_e32 v37, v32
	v_mov_b32_e32 v38, v32
	v_mov_b32_e32 v39, v32
	v_mov_b32_e32 v40, v32
	v_mov_b32_e32 v41, v32
	v_mov_b32_e32 v42, v32
	v_mov_b32_e32 v43, v32
	v_mov_b32_e32 v44, v32
	v_mov_b32_e32 v45, v32
	v_mov_b32_e32 v46, v32
	v_mov_b32_e32 v47, v32
	v_mov_b32_e32 v48, v32
	v_mov_b32_e32 v49, v32
	v_mov_b32_e32 v50, v32
	v_mov_b32_e32 v51, v32
	v_mov_b32_e32 v52, v32
	v_mov_b32_e32 v53, v32
	v_mov_b32_e32 v54, v32
	v_mov_b32_e32 v55, v32
	v_mov_b32_e32 v56, v32
	v_mov_b32_e32 v57, v32
	v_mov_b32_e32 v58, v32
	v_mov_b32_e32 v59, v32
	v_mov_b32_e32 v68, v32
	v_mov_b32_e32 v69, v32
	v_mov_b32_e32 v70, v32
	v_mov_b32_e32 v71, v32
	v_mov_b32_e32 v76, v32
	v_mov_b32_e32 v77, v32
	v_mov_b32_e32 v78, v32
	v_mov_b32_e32 v79, v32
	v_mov_b32_e32 v60, v32
	v_mov_b32_e32 v61, v32
	v_mov_b32_e32 v62, v32
	v_mov_b32_e32 v63, v32
	v_mov_b32_e32 v64, v32
	v_mov_b32_e32 v65, v32
	v_mov_b32_e32 v66, v32
	v_mov_b32_e32 v67, v32
	v_mov_b32_e32 v72, v32
	v_mov_b32_e32 v73, v32
	v_mov_b32_e32 v74, v32
	v_mov_b32_e32 v75, v32
	v_mov_b32_e32 v80, v32
	v_mov_b32_e32 v81, v32
	v_mov_b32_e32 v82, v32
	v_mov_b32_e32 v83, v32
	v_mov_b32_e32 v84, v32
	v_mov_b32_e32 v85, v32
	v_mov_b32_e32 v86, v32
	v_mov_b32_e32 v87, v32
	v_mov_b32_e32 v96, v32
	v_mov_b32_e32 v97, v32
	v_mov_b32_e32 v98, v32
	v_mov_b32_e32 v99, v32
	v_mov_b32_e32 v104, v32
	v_mov_b32_e32 v105, v32
	v_mov_b32_e32 v106, v32
	v_mov_b32_e32 v107, v32
	v_mov_b32_e32 v108, v32
	v_mov_b32_e32 v109, v32
	v_mov_b32_e32 v110, v32
	v_mov_b32_e32 v111, v32
	v_mov_b32_e32 v88, v32
	v_mov_b32_e32 v89, v32
	v_mov_b32_e32 v90, v32
	v_mov_b32_e32 v91, v32
	v_mov_b32_e32 v92, v32
	v_mov_b32_e32 v93, v32
	v_mov_b32_e32 v94, v32
	v_mov_b32_e32 v95, v32
	v_mov_b32_e32 v100, v32
	v_mov_b32_e32 v101, v32
	v_mov_b32_e32 v102, v32
	v_mov_b32_e32 v103, v32
	v_mov_b32_e32 v112, v32
	v_mov_b32_e32 v113, v32
	v_mov_b32_e32 v114, v32
	v_mov_b32_e32 v115, v32
	v_mov_b32_e32 v116, v32
	v_mov_b32_e32 v117, v32
	v_mov_b32_e32 v118, v32
	v_mov_b32_e32 v119, v32
	v_mov_b32_e32 v128, v32
	v_mov_b32_e32 v129, v32
	v_mov_b32_e32 v130, v32
	v_mov_b32_e32 v131, v32
	v_mov_b32_e32 v136, v32
	v_mov_b32_e32 v137, v32
	v_mov_b32_e32 v138, v32
	v_mov_b32_e32 v139, v32
	v_mov_b32_e32 v140, v32
	v_mov_b32_e32 v141, v32
	v_mov_b32_e32 v142, v32
	v_mov_b32_e32 v143, v32
	v_mov_b32_e32 v120, v32
	v_mov_b32_e32 v121, v32
	v_mov_b32_e32 v122, v32
	v_mov_b32_e32 v123, v32
	v_mov_b32_e32 v124, v32
	v_mov_b32_e32 v125, v32
	v_mov_b32_e32 v126, v32
	v_mov_b32_e32 v127, v32
	v_mov_b32_e32 v132, v32
	v_mov_b32_e32 v133, v32
	v_mov_b32_e32 v134, v32
	v_mov_b32_e32 v135, v32
	v_mov_b32_e32 v144, v32
	v_mov_b32_e32 v145, v32
	v_mov_b32_e32 v146, v32
	v_mov_b32_e32 v147, v32
	v_mov_b32_e32 v148, v32
	v_mov_b32_e32 v149, v32
	v_mov_b32_e32 v150, v32
	v_mov_b32_e32 v151, v32
	v_mov_b32_e32 v152, v32
	v_mov_b32_e32 v153, v32
	v_mov_b32_e32 v154, v32
	v_mov_b32_e32 v155, v32
	v_mov_b32_e32 v156, v32
	v_mov_b32_e32 v157, v32
	v_mov_b32_e32 v158, v32
	v_mov_b32_e32 v159, v32
	v_mov_b32_e32 v160, v32
	v_mov_b32_e32 v161, v32
	v_mov_b32_e32 v162, v32
	v_mov_b32_e32 v163, v32
	v_mov_b32_e32 v164, v32
	v_mov_b32_e32 v165, v32
	v_mov_b32_e32 v166, v32
	v_mov_b32_e32 v167, v32
	v_mov_b32_e32 v168, v32
	v_mov_b32_e32 v169, v32
	v_mov_b32_e32 v170, v32
	v_mov_b32_e32 v171, v32
	v_mov_b32_e32 v172, v32
	v_mov_b32_e32 v173, v32
	v_mov_b32_e32 v174, v32
	v_mov_b32_e32 v175, v32
	v_mov_b32_e32 v216, 0
	v_mov_b32_e32 v217, 0
	v_mov_b32_e32 v218, 0
	v_mov_b32_e32 v219, 0
	v_mov_b32_e32 v220, 0
	v_mov_b32_e32 v221, 0
	v_mov_b32_e32 v222, 0
	v_mov_b32_e32 v223, 0
	v_mov_b32_e32 v244, 0
	v_mov_b32_e32 v245, 0
	v_mov_b32_e32 v246, 0
	v_mov_b32_e32 v247, 0
	v_mov_b32_e32 v248, 0
	v_mov_b32_e32 v249, 0
	v_mov_b32_e32 v250, 0
	v_mov_b32_e32 v251, 0
	v_mov_b32_e32 v252, 0
	v_mov_b32_e32 v253, 0
	v_mov_b32_e32 v254, 0
	v_mov_b32_e32 v255, 0
	s_branch .Lchk6_loop

; #define G_DMA_A(kt, AO) do { G_DMA1(kt, AO, 0); G_DMA1(kt, AO, 1); G_DMA1(kt, AO, 2); G_DMA1(kt, AO, 3); if (MF == 9) G_DMA5(kt, AO); } while (0)
; #define G_ISSUE_B(kt) do { const unsigned _sb = (unsigned)(kt) * 4u * kstepB; \
;         _Pragma("unroll") for (int _i = 0; _i < 8; ++_i) sb[_i] = bload16(_i < 4 ? rsB0 : rsB1, vob, _sb + (_i & 3) * kstepB); } while (0)
; #define G_WRITE_B(BO) do { \
;         _Pragma("unroll") for (int _i = 0; _i < 8; ++_i) *(LAS u32x2*)(b_wr + (BO) + (_i & 3) * (16 * G_BSTRIDE) + (_i >> 2) * SLAB1) = pack4(__builtin_bit_cast(f32x4, sb[_i])); } while (0)
; #define G_ENDTILE(VM) do { asm volatile("s_waitcnt vmcnt(" #VM ")" ::: "memory"); \
;         asm volatile("s_waitcnt lgkmcnt(0)" ::: "memory"); __builtin_amdgcn_s_barrier(); asm volatile("" ::: "memory"); } while (0)
;     ...
;     __builtin_amdgcn_s_barrier();
;     G_DMA_A(0, G_A0); G_ISSUE_B(0); G_WRITE_B(G_B0);
;     __builtin_amdgcn_sched_barrier(0);
;     G_ISSUE_B(1);
;     __builtin_amdgcn_sched_barrier(0);
;     G_ENDTILE(8);
;     for (int ui = 0;; ++ui) {
; #pragma unroll
;         for (int m = 0; m < MF; ++m)
; #pragma unroll
;             for (int n = 0; n < 4; ++n) acc[m][n] = (f32x4){0.f, 0.f, 0.f, 0.f};
;         for (int t = 0; t < nt - 2; t += 2) {
;             G_TILE(G_A0, G_B0, true, G_B1, G_A1, t + 1, true, t + 2, (void)0);
.LBB0_897:
	s_andn2_b64 vcc, exec, s[28:29]
	v_mov_b32_e32 v159, 0
	s_cbranch_vccnz .LBB0_900
	s_mov_b32 s12, 0
	s_mov_b32 s13, 0x1e0000
	s_movk_i32 s45, 0x100
	s_waitcnt lgkmcnt(0)
	s_mov_b32 m0, s64
	s_add_i32 s69, s45, 0xffffff80
	ds_read_b64_tr_b16 v[170:171], v166
	ds_read_b64_tr_b16 v[172:173], v167
	ds_read_b64_tr_b16 v[176:177], v167 offset:32
	ds_read_b128 v[178:181], v162
	ds_read_b64_tr_b16 v[174:175], v166 offset:32
	ds_read_b64_tr_b16 v[182:183], v166 offset:64
	ds_read_b64_tr_b16 v[186:187], v166 offset:96
	ds_read_b64_tr_b16 v[184:185], v167 offset:64
	ds_read_b64_tr_b16 v[188:189], v167 offset:96
	ds_read_b128 v[190:193], v162 offset:2048
	ds_read_b128 v[198:201], v162 offset:4096
	buffer_load_dwordx4 v163, s[20:23], s69 offen lds
	s_mov_b32 m0, s63
	s_waitcnt lgkmcnt(7)
	v_mfma_f32_16x16x32_bf16 v[156:159], v[170:173], v[178:181], 0
	buffer_load_dwordx4 v165, s[20:23], s69 offen lds
	s_waitcnt lgkmcnt(6)
	v_mfma_f32_16x16x32_bf16 v[152:155], v[174:177], v[178:181], 0
	s_waitcnt lgkmcnt(3)
	v_mfma_f32_16x16x32_bf16 v[148:151], v[182:185], v[178:181], 0
	s_waitcnt lgkmcnt(2)
	v_mfma_f32_16x16x32_bf16 v[144:147], v[186:189], v[178:181], 0
	s_waitcnt lgkmcnt(1)
	v_mfma_f32_16x16x32_bf16 v[140:143], v[170:173], v[190:193], 0
	s_mov_b32 m0, s62
	s_nop 0
	buffer_load_dwordx4 v164, s[20:23], s69 offen lds
	ds_read_b128 v[178:181], v162 offset:6144
	s_waitcnt vmcnt(10)
	v_cvt_pk_bf16_f32 v15, v14, v15
	v_cvt_pk_bf16_f32 v14, v12, v13
	v_mfma_f32_16x16x32_bf16 v[136:139], v[174:177], v[190:193], 0
	ds_write_b64 v161, v[14:15] offset:34816
	v_mfma_f32_16x16x32_bf16 v[132:135], v[182:185], v[190:193], 0
	s_mov_b32 m0, s31
	s_nop 0
	buffer_load_dwordx4 v168, s[20:23], s69 offen lds
	s_add_i32 s69, s13, 0xfff20000
	v_mfma_f32_16x16x32_bf16 v[128:131], v[186:189], v[190:193], 0
	s_waitcnt lgkmcnt(2)
	v_mfma_f32_16x16x32_bf16 v[124:127], v[170:173], v[198:201], 0
	ds_read_b128 v[190:193], v162 offset:8192
	v_mfma_f32_16x16x32_bf16 v[120:123], v[174:177], v[198:201], 0
	v_mfma_f32_16x16x32_bf16 v[116:119], v[182:185], v[198:201], 0
	v_mfma_f32_16x16x32_bf16 v[112:115], v[186:189], v[198:201], 0
	s_waitcnt lgkmcnt(2)
	v_mfma_f32_16x16x32_bf16 v[108:111], v[170:173], v[178:181], 0
	ds_read_b128 v[198:201], v162 offset:10240
	buffer_load_dwordx4 v[12:15], v160, s[24:27], s69 offen
	s_waitcnt vmcnt(11)
	v_cvt_pk_bf16_f32 v3, v2, v3
	v_cvt_pk_bf16_f32 v2, v0, v1
	v_mfma_f32_16x16x32_bf16 v[104:107], v[174:177], v[178:181], 0
	ds_write_b64 v161, v[2:3] offset:43520
	v_mfma_f32_16x16x32_bf16 v[100:103], v[182:185], v[178:181], 0
	v_mfma_f32_16x16x32_bf16 v[96:99], v[186:189], v[178:181], 0
	s_add_i32 s74, s13, 0xfff40000
	s_waitcnt lgkmcnt(2)
	v_mfma_f32_16x16x32_bf16 v[92:95], v[170:173], v[190:193], 0
	ds_read_b128 v[178:181], v162 offset:12288
	v_mfma_f32_16x16x32_bf16 v[88:91], v[174:177], v[190:193], 0
	v_mfma_f32_16x16x32_bf16 v[84:87], v[182:185], v[190:193], 0
	v_mfma_f32_16x16x32_bf16 v[80:83], v[186:189], v[190:193], 0
	s_waitcnt lgkmcnt(2)
	v_mfma_f32_16x16x32_bf16 v[76:79], v[170:173], v[198:201], 0
	ds_read_b128 v[190:193], v162 offset:14336
	buffer_load_dwordx4 v[0:3], v160, s[24:27], s74 offen
	s_waitcnt vmcnt(11)
	v_cvt_pk_bf16_f32 v31, v30, v31
	v_cvt_pk_bf16_f32 v30, v28, v29
	v_mfma_f32_16x16x32_bf16 v[72:75], v[174:177], v[198:201], 0
	ds_write_b64 v161, v[30:31] offset:52224
	v_mfma_f32_16x16x32_bf16 v[68:71], v[182:185], v[198:201], 0
	v_mfma_f32_16x16x32_bf16 v[64:67], v[186:189], v[198:201], 0
	s_add_i32 s75, s13, 0xfff60000
	s_waitcnt lgkmcnt(2)
	v_mfma_f32_16x16x32_bf16 v[60:63], v[170:173], v[178:181], 0
	ds_read_b128 v[198:201], v162 offset:1024
	v_mfma_f32_16x16x32_bf16 v[56:59], v[174:177], v[178:181], 0
	v_mfma_f32_16x16x32_bf16 v[52:55], v[182:185], v[178:181], 0
	v_mfma_f32_16x16x32_bf16 v[48:51], v[186:189], v[178:181], 0
	s_waitcnt lgkmcnt(2)
	v_mfma_f32_16x16x32_bf16 v[44:47], v[170:173], v[190:193], 0
	ds_read_b128 v[170:173], v162 offset:3072
	buffer_load_dwordx4 v[28:31], v160, s[24:27], s75 offen
	s_waitcnt vmcnt(11)
	v_cvt_pk_bf16_f32 v27, v26, v27
	v_cvt_pk_bf16_f32 v26, v24, v25
	v_mfma_f32_16x16x32_bf16 v[40:43], v[174:177], v[190:193], 0
	ds_read_b64_tr_b16 v[244:245], v166 offset:17408
	ds_read_b64_tr_b16 v[248:249], v166 offset:17440
	ds_read_b64_tr_b16 v[202:203], v166 offset:17472
	ds_read_b64_tr_b16 v[206:207], v166 offset:17504
	ds_read_b64_tr_b16 v[246:247], v167 offset:17408
	ds_read_b64_tr_b16 v[250:251], v167 offset:17440
	ds_read_b64_tr_b16 v[204:205], v167 offset:17472
	ds_read_b64_tr_b16 v[208:209], v167 offset:17504
	ds_write_b64 v161, v[26:27] offset:60928
	v_mfma_f32_16x16x32_bf16 v[36:39], v[182:185], v[190:193], 0
	v_mfma_f32_16x16x32_bf16 v[32:35], v[186:189], v[190:193], 0
	s_add_i32 s76, s13, 0xfff80000
	s_waitcnt lgkmcnt(4)
	v_mfma_f32_16x16x32_bf16 v[156:159], v[244:247], v[198:201], v[156:159]
	ds_read_b128 v[182:185], v162 offset:5120
	s_waitcnt lgkmcnt(4)
	v_mfma_f32_16x16x32_bf16 v[152:155], v[248:251], v[198:201], v[152:155]
	s_waitcnt lgkmcnt(3)
	v_mfma_f32_16x16x32_bf16 v[148:151], v[202:205], v[198:201], v[148:151]
	s_waitcnt lgkmcnt(2)
	v_mfma_f32_16x16x32_bf16 v[144:147], v[206:209], v[198:201], v[144:147]
	v_mfma_f32_16x16x32_bf16 v[140:143], v[244:247], v[170:173], v[140:143]
	ds_read_b128 v[186:189], v162 offset:7168
	buffer_load_dwordx4 v[24:27], v160, s[24:27], s76 offen
	s_waitcnt vmcnt(11)
	v_cvt_pk_bf16_f32 v23, v22, v23
	v_cvt_pk_bf16_f32 v22, v20, v21
	v_mfma_f32_16x16x32_bf16 v[136:139], v[248:251], v[170:173], v[136:139]
	ds_write_b64 v161, v[22:23] offset:35072
	v_mfma_f32_16x16x32_bf16 v[132:135], v[202:205], v[170:173], v[132:135]
	v_mfma_f32_16x16x32_bf16 v[128:131], v[206:209], v[170:173], v[128:131]
	s_waitcnt lgkmcnt(2)
; #define G_DMA_A(kt, AO) do { G_DMA1(kt, AO, 0); G_DMA1(kt, AO, 1); G_DMA1(kt, AO, 2); G_DMA1(kt, AO, 3); if (MF == 9) G_DMA5(kt, AO); } while (0)
; #define G_ISSUE_B(kt) do { const unsigned _sb = (unsigned)(kt) * 4u * kstepB; \
;         _Pragma("unroll") for (int _i = 0; _i < 8; ++_i) sb[_i] = bload16(_i < 4 ? rsB0 : rsB1, vob, _sb + (_i & 3) * kstepB); } while (0)
; #define G_WRITE_B(BO) do { \
;         _Pragma("unroll") for (int _i = 0; _i < 8; ++_i) *(LAS u32x2*)(b_wr + (BO) + (_i & 3) * (16 * G_BSTRIDE) + (_i >> 2) * SLAB1) = pack4(__builtin_bit_cast(f32x4, sb[_i])); } while (0)
; #define G_ENDTILE(VM) do { asm volatile("s_waitcnt vmcnt(" #VM ")" ::: "memory"); \
;         asm volatile("s_waitcnt lgkmcnt(0)" ::: "memory"); __builtin_amdgcn_s_barrier(); asm volatile("" ::: "memory"); } while (0)
;     ...
;     __builtin_amdgcn_s_barrier();
;     G_DMA_A(0, G_A0); G_ISSUE_B(0); G_WRITE_B(G_B0);
;     __builtin_amdgcn_sched_barrier(0);
;     G_ISSUE_B(1);
;     __builtin_amdgcn_sched_barrier(0);
;     G_ENDTILE(8);
;     for (int ui = 0;; ++ui) {
; #pragma unroll
;         for (int m = 0; m < MF; ++m)
; #pragma unroll
;             for (int n = 0; n < 4; ++n) acc[m][n] = (f32x4){0.f, 0.f, 0.f, 0.f};
;         for (int t = 0; t < nt - 2; t += 2) {
;             G_TILE(G_A0, G_B0, true, G_B1, G_A1, t + 1, true, t + 2, (void)0);
;             G_ENDTILE(8);
;             G_TILE(G_A1, G_B1, true, G_B0, G_A0, t + 2, true, t + 3, (void)0);
	v_mfma_f32_16x16x32_bf16 v[124:127], v[244:247], v[182:185], v[124:127]
	ds_read_b128 v[170:173], v162 offset:9216
	v_mfma_f32_16x16x32_bf16 v[120:123], v[248:251], v[182:185], v[120:123]
	v_mfma_f32_16x16x32_bf16 v[116:119], v[202:205], v[182:185], v[116:119]
	v_mfma_f32_16x16x32_bf16 v[112:115], v[206:209], v[182:185], v[112:115]
	s_waitcnt lgkmcnt(2)
	v_mfma_f32_16x16x32_bf16 v[108:111], v[244:247], v[186:189], v[108:111]
	ds_read_b128 v[182:185], v162 offset:11264
	buffer_load_dwordx4 v[20:23], v160, s[16:19], s69 offen
	s_waitcnt vmcnt(11)
	v_cvt_pk_bf16_f32 v7, v6, v7
	v_cvt_pk_bf16_f32 v6, v4, v5
	v_mfma_f32_16x16x32_bf16 v[104:107], v[248:251], v[186:189], v[104:107]
	ds_write_b64 v161, v[6:7] offset:43776
	v_mfma_f32_16x16x32_bf16 v[100:103], v[202:205], v[186:189], v[100:103]
	v_mfma_f32_16x16x32_bf16 v[96:99], v[206:209], v[186:189], v[96:99]
	s_waitcnt lgkmcnt(2)
	v_mfma_f32_16x16x32_bf16 v[92:95], v[244:247], v[170:173], v[92:95]
	ds_read_b128 v[186:189], v162 offset:13312
	v_mfma_f32_16x16x32_bf16 v[88:91], v[248:251], v[170:173], v[88:91]
	v_mfma_f32_16x16x32_bf16 v[84:87], v[202:205], v[170:173], v[84:87]
	v_mfma_f32_16x16x32_bf16 v[80:83], v[206:209], v[170:173], v[80:83]
	s_waitcnt lgkmcnt(2)
	v_mfma_f32_16x16x32_bf16 v[76:79], v[244:247], v[182:185], v[76:79]
	ds_read_b128 v[252:255], v162 offset:15360
	buffer_load_dwordx4 v[4:7], v160, s[16:19], s74 offen
	s_waitcnt vmcnt(11)
	v_cvt_pk_bf16_f32 v11, v10, v11
	v_cvt_pk_bf16_f32 v10, v8, v9
	v_mfma_f32_16x16x32_bf16 v[72:75], v[248:251], v[182:185], v[72:75]
	ds_write_b64 v161, v[10:11] offset:52480
	v_mfma_f32_16x16x32_bf16 v[68:71], v[202:205], v[182:185], v[68:71]
	v_mfma_f32_16x16x32_bf16 v[64:67], v[206:209], v[182:185], v[64:67]
	s_waitcnt lgkmcnt(2)
	v_mfma_f32_16x16x32_bf16 v[60:63], v[244:247], v[186:189], v[60:63]
	buffer_load_dwordx4 v[8:11], v160, s[16:19], s75 offen
	s_waitcnt vmcnt(11)
	v_cvt_pk_bf16_f32 v19, v18, v19
	v_cvt_pk_bf16_f32 v18, v16, v17
	v_mfma_f32_16x16x32_bf16 v[56:59], v[248:251], v[186:189], v[56:59]
	ds_write_b64 v161, v[18:19] offset:61184
	v_mfma_f32_16x16x32_bf16 v[52:55], v[202:205], v[186:189], v[52:55]
	buffer_load_dwordx4 v[16:19], v160, s[16:19], s76 offen
	v_mfma_f32_16x16x32_bf16 v[48:51], v[206:209], v[186:189], v[48:51]
	s_waitcnt vmcnt(8)
	s_mov_b32 m0, s56
	s_waitcnt lgkmcnt(0)
	s_barrier
	ds_read_b64_tr_b16 v[170:171], v166 offset:34816
	ds_read_b64_tr_b16 v[172:173], v167 offset:34816
	ds_read_b64_tr_b16 v[176:177], v167 offset:34848
	ds_read_b128 v[178:181], v162 offset:32768
	ds_read_b64_tr_b16 v[174:175], v166 offset:34848
	ds_read_b64_tr_b16 v[182:183], v166 offset:34880
	ds_read_b64_tr_b16 v[186:187], v166 offset:34912
	ds_read_b64_tr_b16 v[184:185], v167 offset:34880
	ds_read_b64_tr_b16 v[188:189], v167 offset:34912
	ds_read_b128 v[190:193], v162 offset:34816
	ds_read_b128 v[198:201], v162 offset:36864
	buffer_load_dwordx4 v163, s[20:23], s45 offen lds
	s_mov_b32 m0, s57
	v_mfma_f32_16x16x32_bf16 v[44:47], v[244:247], v[252:255], v[44:47]
	v_mfma_f32_16x16x32_bf16 v[40:43], v[248:251], v[252:255], v[40:43]
	v_mfma_f32_16x16x32_bf16 v[36:39], v[202:205], v[252:255], v[36:39]
	v_mfma_f32_16x16x32_bf16 v[32:35], v[206:209], v[252:255], v[32:35]
	s_waitcnt lgkmcnt(7)
	v_mfma_f32_16x16x32_bf16 v[156:159], v[170:173], v[178:181], v[156:159]
	buffer_load_dwordx4 v165, s[20:23], s45 offen lds
	s_add_i32 s69, s13, 0xfffa0000
	s_waitcnt lgkmcnt(6)
	v_mfma_f32_16x16x32_bf16 v[152:155], v[174:177], v[178:181], v[152:155]
	s_waitcnt lgkmcnt(3)
	v_mfma_f32_16x16x32_bf16 v[148:151], v[182:185], v[178:181], v[148:151]
	s_waitcnt lgkmcnt(2)
	v_mfma_f32_16x16x32_bf16 v[144:147], v[186:189], v[178:181], v[144:147]
	s_waitcnt lgkmcnt(1)
	v_mfma_f32_16x16x32_bf16 v[140:143], v[170:173], v[190:193], v[140:143]
	s_mov_b32 m0, s58
	s_nop 0
	buffer_load_dwordx4 v164, s[20:23], s45 offen lds
	ds_read_b128 v[178:181], v162 offset:38912
	s_waitcnt vmcnt(10)
	v_cvt_pk_bf16_f32 v15, v14, v15
	v_cvt_pk_bf16_f32 v14, v12, v13
	v_mfma_f32_16x16x32_bf16 v[136:139], v[174:177], v[190:193], v[136:139]
	ds_write_b64 v161, v[14:15]
	v_mfma_f32_16x16x32_bf16 v[132:135], v[182:185], v[190:193], v[132:135]
	s_mov_b32 m0, s59
	s_nop 0
	buffer_load_dwordx4 v168, s[20:23], s45 offen lds
	v_mfma_f32_16x16x32_bf16 v[128:131], v[186:189], v[190:193], v[128:131]
	s_waitcnt lgkmcnt(2)
	v_mfma_f32_16x16x32_bf16 v[124:127], v[170:173], v[198:201], v[124:127]
	ds_read_b128 v[190:193], v162 offset:40960
	v_mfma_f32_16x16x32_bf16 v[120:123], v[174:177], v[198:201], v[120:123]
	v_mfma_f32_16x16x32_bf16 v[116:119], v[182:185], v[198:201], v[116:119]
	v_mfma_f32_16x16x32_bf16 v[112:115], v[186:189], v[198:201], v[112:115]
	s_waitcnt lgkmcnt(2)
	v_mfma_f32_16x16x32_bf16 v[108:111], v[170:173], v[178:181], v[108:111]
	ds_read_b128 v[198:201], v162 offset:43008
	buffer_load_dwordx4 v[12:15], v160, s[24:27], s69 offen
	s_waitcnt vmcnt(11)
	v_cvt_pk_bf16_f32 v3, v2, v3
	v_cvt_pk_bf16_f32 v2, v0, v1
	v_mfma_f32_16x16x32_bf16 v[104:107], v[174:177], v[178:181], v[104:107]
	ds_write_b64 v161, v[2:3] offset:8704
	v_mfma_f32_16x16x32_bf16 v[100:103], v[182:185], v[178:181], v[100:103]
	v_mfma_f32_16x16x32_bf16 v[96:99], v[186:189], v[178:181], v[96:99]
	s_add_i32 s74, s13, 0xfffc0000
	s_waitcnt lgkmcnt(2)
; #define G_DMA_A(kt, AO) do { G_DMA1(kt, AO, 0); G_DMA1(kt, AO, 1); G_DMA1(kt, AO, 2); G_DMA1(kt, AO, 3); if (MF == 9) G_DMA5(kt, AO); } while (0)
; #define G_ISSUE_B(kt) do { const unsigned _sb = (unsigned)(kt) * 4u * kstepB; \
;         _Pragma("unroll") for (int _i = 0; _i < 8; ++_i) sb[_i] = bload16(_i < 4 ? rsB0 : rsB1, vob, _sb + (_i & 3) * kstepB); } while (0)
; #define G_WRITE_B(BO) do { \
;         _Pragma("unroll") for (int _i = 0; _i < 8; ++_i) *(LAS u32x2*)(b_wr + (BO) + (_i & 3) * (16 * G_BSTRIDE) + (_i >> 2) * SLAB1) = pack4(__builtin_bit_cast(f32x4, sb[_i])); } while (0)
; #define G_ENDTILE(VM) do { asm volatile("s_waitcnt vmcnt(" #VM ")" ::: "memory"); \
;         asm volatile("s_waitcnt lgkmcnt(0)" ::: "memory"); __builtin_amdgcn_s_barrier(); asm volatile("" ::: "memory"); } while (0)
;     ...
;     __builtin_amdgcn_s_barrier();
;     G_DMA_A(0, G_A0); G_ISSUE_B(0); G_WRITE_B(G_B0);
;     __builtin_amdgcn_sched_barrier(0);
;     G_ISSUE_B(1);
;     __builtin_amdgcn_sched_barrier(0);
;     G_ENDTILE(8);
;     for (int ui = 0;; ++ui) {
; #pragma unroll
;         for (int m = 0; m < MF; ++m)
; #pragma unroll
;             for (int n = 0; n < 4; ++n) acc[m][n] = (f32x4){0.f, 0.f, 0.f, 0.f};
;         for (int t = 0; t < nt - 2; t += 2) {
;             G_TILE(G_A0, G_B0, true, G_B1, G_A1, t + 1, true, t + 2, (void)0);
;             G_ENDTILE(8);
;             G_TILE(G_A1, G_B1, true, G_B0, G_A0, t + 2, true, t + 3, (void)0);
;             G_ENDTILE(8);
;         }
	v_mfma_f32_16x16x32_bf16 v[92:95], v[170:173], v[190:193], v[92:95]
	ds_read_b128 v[178:181], v162 offset:45056
	v_mfma_f32_16x16x32_bf16 v[88:91], v[174:177], v[190:193], v[88:91]
	v_mfma_f32_16x16x32_bf16 v[84:87], v[182:185], v[190:193], v[84:87]
	v_mfma_f32_16x16x32_bf16 v[80:83], v[186:189], v[190:193], v[80:83]
	s_waitcnt lgkmcnt(2)
	v_mfma_f32_16x16x32_bf16 v[76:79], v[170:173], v[198:201], v[76:79]
	ds_read_b128 v[190:193], v162 offset:47104
	buffer_load_dwordx4 v[0:3], v160, s[24:27], s74 offen
	s_waitcnt vmcnt(11)
	v_cvt_pk_bf16_f32 v31, v30, v31
	v_cvt_pk_bf16_f32 v30, v28, v29
	v_mfma_f32_16x16x32_bf16 v[72:75], v[174:177], v[198:201], v[72:75]
	ds_write_b64 v161, v[30:31] offset:17408
	v_mfma_f32_16x16x32_bf16 v[68:71], v[182:185], v[198:201], v[68:71]
	v_mfma_f32_16x16x32_bf16 v[64:67], v[186:189], v[198:201], v[64:67]
	s_add_i32 s75, s13, 0xfffe0000
	s_waitcnt lgkmcnt(2)
	v_mfma_f32_16x16x32_bf16 v[60:63], v[170:173], v[178:181], v[60:63]
	ds_read_b128 v[198:201], v162 offset:33792
	v_mfma_f32_16x16x32_bf16 v[56:59], v[174:177], v[178:181], v[56:59]
	v_mfma_f32_16x16x32_bf16 v[52:55], v[182:185], v[178:181], v[52:55]
	v_mfma_f32_16x16x32_bf16 v[48:51], v[186:189], v[178:181], v[48:51]
	s_waitcnt lgkmcnt(2)
	v_mfma_f32_16x16x32_bf16 v[44:47], v[170:173], v[190:193], v[44:47]
	ds_read_b128 v[170:173], v162 offset:35840
	buffer_load_dwordx4 v[28:31], v160, s[24:27], s75 offen
	s_waitcnt vmcnt(11)
	v_cvt_pk_bf16_f32 v27, v26, v27
	v_cvt_pk_bf16_f32 v26, v24, v25
	v_mfma_f32_16x16x32_bf16 v[40:43], v[174:177], v[190:193], v[40:43]
	ds_read_b64_tr_b16 v[244:245], v166 offset:52224
	ds_read_b64_tr_b16 v[248:249], v166 offset:52256
	ds_read_b64_tr_b16 v[202:203], v166 offset:52288
	ds_read_b64_tr_b16 v[206:207], v166 offset:52320
	ds_read_b64_tr_b16 v[246:247], v167 offset:52224
	ds_read_b64_tr_b16 v[250:251], v167 offset:52256
	ds_read_b64_tr_b16 v[204:205], v167 offset:52288
	ds_read_b64_tr_b16 v[208:209], v167 offset:52320
	ds_write_b64 v161, v[26:27] offset:26112
	v_mfma_f32_16x16x32_bf16 v[36:39], v[182:185], v[190:193], v[36:39]
	v_mfma_f32_16x16x32_bf16 v[32:35], v[186:189], v[190:193], v[32:35]
	s_waitcnt lgkmcnt(4)
	v_mfma_f32_16x16x32_bf16 v[156:159], v[244:247], v[198:201], v[156:159]
	ds_read_b128 v[182:185], v162 offset:37888
	s_waitcnt lgkmcnt(4)
	v_mfma_f32_16x16x32_bf16 v[152:155], v[248:251], v[198:201], v[152:155]
	s_waitcnt lgkmcnt(3)
	v_mfma_f32_16x16x32_bf16 v[148:151], v[202:205], v[198:201], v[148:151]
	s_waitcnt lgkmcnt(2)
	v_mfma_f32_16x16x32_bf16 v[144:147], v[206:209], v[198:201], v[144:147]
	v_mfma_f32_16x16x32_bf16 v[140:143], v[244:247], v[170:173], v[140:143]
	ds_read_b128 v[186:189], v162 offset:39936
	buffer_load_dwordx4 v[24:27], v160, s[24:27], s13 offen
	s_waitcnt vmcnt(11)
	v_cvt_pk_bf16_f32 v23, v22, v23
	v_cvt_pk_bf16_f32 v22, v20, v21
	v_mfma_f32_16x16x32_bf16 v[136:139], v[248:251], v[170:173], v[136:139]
	ds_write_b64 v161, v[22:23] offset:256
	v_mfma_f32_16x16x32_bf16 v[132:135], v[202:205], v[170:173], v[132:135]
	v_mfma_f32_16x16x32_bf16 v[128:131], v[206:209], v[170:173], v[128:131]
	s_waitcnt lgkmcnt(2)
	v_mfma_f32_16x16x32_bf16 v[124:127], v[244:247], v[182:185], v[124:127]
	ds_read_b128 v[170:173], v162 offset:41984
	v_mfma_f32_16x16x32_bf16 v[120:123], v[248:251], v[182:185], v[120:123]
	v_mfma_f32_16x16x32_bf16 v[116:119], v[202:205], v[182:185], v[116:119]
	v_mfma_f32_16x16x32_bf16 v[112:115], v[206:209], v[182:185], v[112:115]
	s_waitcnt lgkmcnt(2)
	v_mfma_f32_16x16x32_bf16 v[108:111], v[244:247], v[186:189], v[108:111]
	ds_read_b128 v[182:185], v162 offset:44032
	buffer_load_dwordx4 v[20:23], v160, s[16:19], s69 offen
	s_waitcnt vmcnt(11)
	v_cvt_pk_bf16_f32 v7, v6, v7
	v_cvt_pk_bf16_f32 v6, v4, v5
	v_mfma_f32_16x16x32_bf16 v[104:107], v[248:251], v[186:189], v[104:107]
	ds_write_b64 v161, v[6:7] offset:8960
	v_mfma_f32_16x16x32_bf16 v[100:103], v[202:205], v[186:189], v[100:103]
	v_mfma_f32_16x16x32_bf16 v[96:99], v[206:209], v[186:189], v[96:99]
	s_waitcnt lgkmcnt(2)
	v_mfma_f32_16x16x32_bf16 v[92:95], v[244:247], v[170:173], v[92:95]
	ds_read_b128 v[186:189], v162 offset:46080
	v_mfma_f32_16x16x32_bf16 v[88:91], v[248:251], v[170:173], v[88:91]
	v_mfma_f32_16x16x32_bf16 v[84:87], v[202:205], v[170:173], v[84:87]
	v_mfma_f32_16x16x32_bf16 v[80:83], v[206:209], v[170:173], v[80:83]
	s_waitcnt lgkmcnt(2)
	v_mfma_f32_16x16x32_bf16 v[76:79], v[244:247], v[182:185], v[76:79]
	ds_read_b128 v[252:255], v162 offset:48128
	buffer_load_dwordx4 v[4:7], v160, s[16:19], s74 offen
	s_waitcnt vmcnt(11)
	v_cvt_pk_bf16_f32 v11, v10, v11
	v_cvt_pk_bf16_f32 v10, v8, v9
	v_mfma_f32_16x16x32_bf16 v[72:75], v[248:251], v[182:185], v[72:75]
	ds_write_b64 v161, v[10:11] offset:17664
	v_mfma_f32_16x16x32_bf16 v[68:71], v[202:205], v[182:185], v[68:71]
	v_mfma_f32_16x16x32_bf16 v[64:67], v[206:209], v[182:185], v[64:67]
	s_waitcnt lgkmcnt(2)
	v_mfma_f32_16x16x32_bf16 v[60:63], v[244:247], v[186:189], v[60:63]
	buffer_load_dwordx4 v[8:11], v160, s[16:19], s75 offen
	s_waitcnt vmcnt(11)
	v_cvt_pk_bf16_f32 v19, v18, v19
	v_cvt_pk_bf16_f32 v18, v16, v17
	v_mfma_f32_16x16x32_bf16 v[56:59], v[248:251], v[186:189], v[56:59]
	ds_write_b64 v161, v[18:19] offset:26368
	v_mfma_f32_16x16x32_bf16 v[52:55], v[202:205], v[186:189], v[52:55]
	buffer_load_dwordx4 v[16:19], v160, s[16:19], s13 offen
	v_mfma_f32_16x16x32_bf16 v[48:51], v[206:209], v[186:189], v[48:51]
	s_waitcnt vmcnt(8)
	s_waitcnt lgkmcnt(0)
	s_barrier
	s_add_i32 s12, s12, 2
	s_add_i32 s13, s13, 0x100000
	s_addk_i32 s45, 0x100
	s_cmp_ge_i32 s12, s30
	s_cbranch_scc1 .Lflush_PLE

; #define G_DMA_A(kt, AO) do { G_DMA1(kt, AO, 0); G_DMA1(kt, AO, 1); G_DMA1(kt, AO, 2); G_DMA1(kt, AO, 3); if (MF == 9) G_DMA5(kt, AO); } while (0)
; #define G_ISSUE_B(kt) do { const unsigned _sb = (unsigned)(kt) * 4u * kstepB; \
;         _Pragma("unroll") for (int _i = 0; _i < 8; ++_i) sb[_i] = bload16(_i < 4 ? rsB0 : rsB1, vob, _sb + (_i & 3) * kstepB); } while (0)
; #define G_WRITE_B(BO) do { \
;         _Pragma("unroll") for (int _i = 0; _i < 8; ++_i) *(LAS u32x2*)(b_wr + (BO) + (_i & 3) * (16 * G_BSTRIDE) + (_i >> 2) * SLAB1) = pack4(__builtin_bit_cast(f32x4, sb[_i])); } while (0)
; #define G_ENDTILE(VM) do { asm volatile("s_waitcnt vmcnt(" #VM ")" ::: "memory"); \
;         asm volatile("s_waitcnt lgkmcnt(0)" ::: "memory"); __builtin_amdgcn_s_barrier(); asm volatile("" ::: "memory"); } while (0)
;     ...
;     __builtin_amdgcn_s_barrier();
;     G_DMA_A(0, G_A0); G_ISSUE_B(0); G_WRITE_B(G_B0);
;     __builtin_amdgcn_sched_barrier(0);
;     G_ISSUE_B(1);
;     __builtin_amdgcn_sched_barrier(0);
;     G_ENDTILE(8);
;     for (int ui = 0;; ++ui) {
; #pragma unroll
;         for (int m = 0; m < MF; ++m)
; #pragma unroll
;             for (int n = 0; n < 4; ++n) acc[m][n] = (f32x4){0.f, 0.f, 0.f, 0.f};
;         for (int t = 0; t < nt - 2; t += 2) {
;             G_TILE(G_A0, G_B0, true, G_B1, G_A1, t + 1, true, t + 2, (void)0);
.LBB0_1036:
	s_andn2_b64 vcc, exec, s[26:27]
	v_mov_b32_e32 v159, 0
	s_cbranch_vccnz .LBB0_1039
	s_mov_b32 s0, 0
	s_mov_b32 s1, 0x1e0000
	s_movk_i32 s4, 0x100
	s_mov_b32 m0, s64
	s_add_i32 s5, s4, 0xffffff80
	ds_read_b64_tr_b16 v[160:161], v178
	ds_read_b64_tr_b16 v[162:163], v179
	ds_read_b64_tr_b16 v[166:167], v179 offset:32
	ds_read_b128 v[168:171], v175
	ds_read_b64_tr_b16 v[164:165], v178 offset:32
	ds_read_b64_tr_b16 v[182:183], v178 offset:64
	ds_read_b64_tr_b16 v[186:187], v178 offset:96
	ds_read_b64_tr_b16 v[184:185], v179 offset:64
	ds_read_b64_tr_b16 v[188:189], v179 offset:96
	ds_read_b128 v[190:193], v175 offset:2048
	ds_read_b128 v[194:197], v175 offset:4096
	buffer_load_dwordx4 v176, s[16:19], s5 offen lds
	s_mov_b32 m0, s63
	s_waitcnt lgkmcnt(7)
	v_mfma_f32_16x16x32_bf16 v[156:159], v[160:163], v[168:171], 0
	buffer_load_dwordx4 v177, s[16:19], s5 offen lds
	s_waitcnt lgkmcnt(6)
	v_mfma_f32_16x16x32_bf16 v[152:155], v[164:167], v[168:171], 0
	s_waitcnt lgkmcnt(3)
	v_mfma_f32_16x16x32_bf16 v[148:151], v[182:185], v[168:171], 0
	s_waitcnt lgkmcnt(2)
	v_mfma_f32_16x16x32_bf16 v[144:147], v[186:189], v[168:171], 0
	s_waitcnt lgkmcnt(1)
	v_mfma_f32_16x16x32_bf16 v[140:143], v[160:163], v[190:193], 0
	s_mov_b32 m0, s62
	s_nop 0
	buffer_load_dwordx4 v180, s[16:19], s5 offen lds
	ds_read_b128 v[168:171], v175 offset:6144
	s_waitcnt vmcnt(10)
	v_cvt_pk_bf16_f32 v15, v14, v15
	v_cvt_pk_bf16_f32 v14, v12, v13
	v_mfma_f32_16x16x32_bf16 v[136:139], v[164:167], v[190:193], 0
	ds_write_b64 v174, v[14:15] offset:34816
	v_mfma_f32_16x16x32_bf16 v[132:135], v[182:185], v[190:193], 0
	s_mov_b32 m0, s61
	s_nop 0
	buffer_load_dwordx4 v181, s[16:19], s5 offen lds
	s_add_i32 s5, s1, 0xfff20000
	v_mfma_f32_16x16x32_bf16 v[128:131], v[186:189], v[190:193], 0
	s_waitcnt lgkmcnt(2)
	v_mfma_f32_16x16x32_bf16 v[124:127], v[160:163], v[194:197], 0
	ds_read_b128 v[190:193], v175 offset:8192
	v_mfma_f32_16x16x32_bf16 v[120:123], v[164:167], v[194:197], 0
	v_mfma_f32_16x16x32_bf16 v[116:119], v[182:185], v[194:197], 0
	v_mfma_f32_16x16x32_bf16 v[112:115], v[186:189], v[194:197], 0
	s_waitcnt lgkmcnt(2)
	v_mfma_f32_16x16x32_bf16 v[108:111], v[160:163], v[168:171], 0
	ds_read_b128 v[194:197], v175 offset:10240
	buffer_load_dwordx4 v[12:15], v173, s[8:11], s5 offen
	s_waitcnt vmcnt(10)
	v_cvt_pk_bf16_f32 v31, v30, v31
	v_cvt_pk_bf16_f32 v30, v28, v29
	v_mfma_f32_16x16x32_bf16 v[104:107], v[164:167], v[168:171], 0
	ds_write_b64 v174, v[30:31] offset:43520
	v_mfma_f32_16x16x32_bf16 v[100:103], v[182:185], v[168:171], 0
	v_mfma_f32_16x16x32_bf16 v[96:99], v[186:189], v[168:171], 0
	s_add_i32 s20, s1, 0xfff40000
	s_waitcnt lgkmcnt(2)
	v_mfma_f32_16x16x32_bf16 v[92:95], v[160:163], v[190:193], 0
	ds_read_b128 v[168:171], v175 offset:12288
	v_mfma_f32_16x16x32_bf16 v[88:91], v[164:167], v[190:193], 0
	v_mfma_f32_16x16x32_bf16 v[84:87], v[182:185], v[190:193], 0
	v_mfma_f32_16x16x32_bf16 v[80:83], v[186:189], v[190:193], 0
	s_waitcnt lgkmcnt(2)
	v_mfma_f32_16x16x32_bf16 v[76:79], v[160:163], v[194:197], 0
	ds_read_b128 v[190:193], v175 offset:14336
	v_cvt_pk_bf16_f32 v7, v6, v7
	v_cvt_pk_bf16_f32 v6, v4, v5
	v_mfma_f32_16x16x32_bf16 v[72:75], v[164:167], v[194:197], 0
	ds_write_b64 v174, v[6:7] offset:52224
	v_mfma_f32_16x16x32_bf16 v[68:71], v[182:185], v[194:197], 0
	v_mfma_f32_16x16x32_bf16 v[64:67], v[186:189], v[194:197], 0
	s_add_i32 s21, s1, 0xfff60000
	buffer_load_dwordx4 v[28:31], v173, s[8:11], s20 offen
	s_waitcnt lgkmcnt(2)
	v_mfma_f32_16x16x32_bf16 v[60:63], v[160:163], v[168:171], 0
	ds_read_b128 v[194:197], v175 offset:1024
	v_mfma_f32_16x16x32_bf16 v[56:59], v[164:167], v[168:171], 0
	v_mfma_f32_16x16x32_bf16 v[52:55], v[182:185], v[168:171], 0
	v_mfma_f32_16x16x32_bf16 v[48:51], v[186:189], v[168:171], 0
	s_waitcnt lgkmcnt(2)
	v_mfma_f32_16x16x32_bf16 v[44:47], v[160:163], v[190:193], 0
	ds_read_b128 v[160:163], v175 offset:3072
	buffer_load_dwordx4 v[4:7], v173, s[8:11], s21 offen
	s_waitcnt vmcnt(11)
	v_cvt_pk_bf16_f32 v27, v26, v27
	v_cvt_pk_bf16_f32 v26, v24, v25
	v_mfma_f32_16x16x32_bf16 v[40:43], v[164:167], v[190:193], 0
	ds_read_b64_tr_b16 v[244:245], v178 offset:17408
	ds_read_b64_tr_b16 v[248:249], v178 offset:17440
	ds_read_b64_tr_b16 v[198:199], v178 offset:17472
	ds_read_b64_tr_b16 v[202:203], v178 offset:17504
	ds_read_b64_tr_b16 v[246:247], v179 offset:17408
	ds_read_b64_tr_b16 v[250:251], v179 offset:17440
	ds_read_b64_tr_b16 v[200:201], v179 offset:17472
	ds_read_b64_tr_b16 v[204:205], v179 offset:17504
	ds_write_b64 v174, v[26:27] offset:60928
	v_mfma_f32_16x16x32_bf16 v[36:39], v[182:185], v[190:193], 0
	v_mfma_f32_16x16x32_bf16 v[32:35], v[186:189], v[190:193], 0
	s_add_i32 s22, s1, 0xfff80000
	s_waitcnt lgkmcnt(4)
	v_mfma_f32_16x16x32_bf16 v[156:159], v[244:247], v[194:197], v[156:159]
	ds_read_b128 v[182:185], v175 offset:5120
	s_waitcnt lgkmcnt(4)
	v_mfma_f32_16x16x32_bf16 v[152:155], v[248:251], v[194:197], v[152:155]
	s_waitcnt lgkmcnt(3)
	v_mfma_f32_16x16x32_bf16 v[148:151], v[198:201], v[194:197], v[148:151]
	s_waitcnt lgkmcnt(2)
	v_mfma_f32_16x16x32_bf16 v[144:147], v[202:205], v[194:197], v[144:147]
	v_mfma_f32_16x16x32_bf16 v[140:143], v[244:247], v[160:163], v[140:143]
	ds_read_b128 v[186:189], v175 offset:7168
	buffer_load_dwordx4 v[24:27], v173, s[8:11], s22 offen
	s_waitcnt vmcnt(11)
	v_cvt_pk_bf16_f32 v23, v22, v23
	v_cvt_pk_bf16_f32 v22, v20, v21
	v_mfma_f32_16x16x32_bf16 v[136:139], v[248:251], v[160:163], v[136:139]
	ds_write_b64 v174, v[22:23] offset:35072
	v_mfma_f32_16x16x32_bf16 v[132:135], v[198:201], v[160:163], v[132:135]
	v_mfma_f32_16x16x32_bf16 v[128:131], v[202:205], v[160:163], v[128:131]
	s_waitcnt lgkmcnt(2)
; #define G_DMA_A(kt, AO) do { G_DMA1(kt, AO, 0); G_DMA1(kt, AO, 1); G_DMA1(kt, AO, 2); G_DMA1(kt, AO, 3); if (MF == 9) G_DMA5(kt, AO); } while (0)
; #define G_ISSUE_B(kt) do { const unsigned _sb = (unsigned)(kt) * 4u * kstepB; \
;         _Pragma("unroll") for (int _i = 0; _i < 8; ++_i) sb[_i] = bload16(_i < 4 ? rsB0 : rsB1, vob, _sb + (_i & 3) * kstepB); } while (0)
; #define G_WRITE_B(BO) do { \
;         _Pragma("unroll") for (int _i = 0; _i < 8; ++_i) *(LAS u32x2*)(b_wr + (BO) + (_i & 3) * (16 * G_BSTRIDE) + (_i >> 2) * SLAB1) = pack4(__builtin_bit_cast(f32x4, sb[_i])); } while (0)
; #define G_ENDTILE(VM) do { asm volatile("s_waitcnt vmcnt(" #VM ")" ::: "memory"); \
;         asm volatile("s_waitcnt lgkmcnt(0)" ::: "memory"); __builtin_amdgcn_s_barrier(); asm volatile("" ::: "memory"); } while (0)
;     ...
;     __builtin_amdgcn_s_barrier();
;     G_DMA_A(0, G_A0); G_ISSUE_B(0); G_WRITE_B(G_B0);
;     __builtin_amdgcn_sched_barrier(0);
;     G_ISSUE_B(1);
;     __builtin_amdgcn_sched_barrier(0);
;     G_ENDTILE(8);
;     for (int ui = 0;; ++ui) {
; #pragma unroll
;         for (int m = 0; m < MF; ++m)
; #pragma unroll
;             for (int n = 0; n < 4; ++n) acc[m][n] = (f32x4){0.f, 0.f, 0.f, 0.f};
;         for (int t = 0; t < nt - 2; t += 2) {
;             G_TILE(G_A0, G_B0, true, G_B1, G_A1, t + 1, true, t + 2, (void)0);
;             G_ENDTILE(8);
;             G_TILE(G_A1, G_B1, true, G_B0, G_A0, t + 2, true, t + 3, (void)0);
	v_mfma_f32_16x16x32_bf16 v[124:127], v[244:247], v[182:185], v[124:127]
	ds_read_b128 v[160:163], v175 offset:9216
	v_mfma_f32_16x16x32_bf16 v[120:123], v[248:251], v[182:185], v[120:123]
	v_mfma_f32_16x16x32_bf16 v[116:119], v[198:201], v[182:185], v[116:119]
	v_mfma_f32_16x16x32_bf16 v[112:115], v[202:205], v[182:185], v[112:115]
	s_waitcnt lgkmcnt(2)
	v_mfma_f32_16x16x32_bf16 v[108:111], v[244:247], v[186:189], v[108:111]
	ds_read_b128 v[182:185], v175 offset:11264
	buffer_load_dwordx4 v[20:23], v173, s[12:15], s5 offen
	s_waitcnt vmcnt(10)
	v_cvt_pk_bf16_f32 v11, v10, v11
	v_cvt_pk_bf16_f32 v10, v8, v9
	v_mfma_f32_16x16x32_bf16 v[104:107], v[248:251], v[186:189], v[104:107]
	ds_write_b64 v174, v[10:11] offset:43776
	v_mfma_f32_16x16x32_bf16 v[100:103], v[198:201], v[186:189], v[100:103]
	v_mfma_f32_16x16x32_bf16 v[96:99], v[202:205], v[186:189], v[96:99]
	s_waitcnt lgkmcnt(2)
	v_mfma_f32_16x16x32_bf16 v[92:95], v[244:247], v[160:163], v[92:95]
	ds_read_b128 v[186:189], v175 offset:13312
	v_mfma_f32_16x16x32_bf16 v[88:91], v[248:251], v[160:163], v[88:91]
	v_mfma_f32_16x16x32_bf16 v[84:87], v[198:201], v[160:163], v[84:87]
	v_mfma_f32_16x16x32_bf16 v[80:83], v[202:205], v[160:163], v[80:83]
	s_waitcnt lgkmcnt(2)
	v_mfma_f32_16x16x32_bf16 v[76:79], v[244:247], v[182:185], v[76:79]
	ds_read_b128 v[252:255], v175 offset:15360
	v_cvt_pk_bf16_f32 v3, v2, v3
	v_cvt_pk_bf16_f32 v2, v0, v1
	v_mfma_f32_16x16x32_bf16 v[72:75], v[248:251], v[182:185], v[72:75]
	ds_write_b64 v174, v[2:3] offset:52480
	v_mfma_f32_16x16x32_bf16 v[68:71], v[198:201], v[182:185], v[68:71]
	v_mfma_f32_16x16x32_bf16 v[64:67], v[202:205], v[182:185], v[64:67]
	buffer_load_dwordx4 v[8:11], v173, s[12:15], s20 offen
	s_waitcnt lgkmcnt(2)
	v_mfma_f32_16x16x32_bf16 v[60:63], v[244:247], v[186:189], v[60:63]
	buffer_load_dwordx4 v[0:3], v173, s[12:15], s21 offen
	s_waitcnt vmcnt(11)
	v_cvt_pk_bf16_f32 v19, v18, v19
	v_cvt_pk_bf16_f32 v18, v16, v17
	v_mfma_f32_16x16x32_bf16 v[56:59], v[248:251], v[186:189], v[56:59]
	ds_write_b64 v174, v[18:19] offset:61184
	v_mfma_f32_16x16x32_bf16 v[52:55], v[198:201], v[186:189], v[52:55]
	buffer_load_dwordx4 v[16:19], v173, s[12:15], s22 offen
	v_mfma_f32_16x16x32_bf16 v[48:51], v[202:205], v[186:189], v[48:51]
	s_waitcnt vmcnt(8)
	s_mov_b32 m0, s45
	s_waitcnt lgkmcnt(0)
	s_barrier
	ds_read_b64_tr_b16 v[160:161], v178 offset:34816
	ds_read_b64_tr_b16 v[162:163], v179 offset:34816
	ds_read_b64_tr_b16 v[166:167], v179 offset:34848
	ds_read_b128 v[168:171], v175 offset:32768
	ds_read_b64_tr_b16 v[164:165], v178 offset:34848
	ds_read_b64_tr_b16 v[182:183], v178 offset:34880
	ds_read_b64_tr_b16 v[186:187], v178 offset:34912
	ds_read_b64_tr_b16 v[184:185], v179 offset:34880
	ds_read_b64_tr_b16 v[188:189], v179 offset:34912
	ds_read_b128 v[190:193], v175 offset:34816
	ds_read_b128 v[194:197], v175 offset:36864
	buffer_load_dwordx4 v176, s[16:19], s4 offen lds
	s_mov_b32 m0, s53
	v_mfma_f32_16x16x32_bf16 v[44:47], v[244:247], v[252:255], v[44:47]
	v_mfma_f32_16x16x32_bf16 v[40:43], v[248:251], v[252:255], v[40:43]
	v_mfma_f32_16x16x32_bf16 v[36:39], v[198:201], v[252:255], v[36:39]
	v_mfma_f32_16x16x32_bf16 v[32:35], v[202:205], v[252:255], v[32:35]
	s_waitcnt lgkmcnt(7)
	v_mfma_f32_16x16x32_bf16 v[156:159], v[160:163], v[168:171], v[156:159]
	buffer_load_dwordx4 v177, s[16:19], s4 offen lds
	s_add_i32 s5, s1, 0xfffa0000
	s_waitcnt lgkmcnt(6)
	v_mfma_f32_16x16x32_bf16 v[152:155], v[164:167], v[168:171], v[152:155]
	s_waitcnt lgkmcnt(3)
	v_mfma_f32_16x16x32_bf16 v[148:151], v[182:185], v[168:171], v[148:151]
	s_waitcnt lgkmcnt(2)
	v_mfma_f32_16x16x32_bf16 v[144:147], v[186:189], v[168:171], v[144:147]
	s_waitcnt lgkmcnt(1)
	v_mfma_f32_16x16x32_bf16 v[140:143], v[160:163], v[190:193], v[140:143]
	s_mov_b32 m0, s54
	s_nop 0
	buffer_load_dwordx4 v180, s[16:19], s4 offen lds
	ds_read_b128 v[168:171], v175 offset:38912
	s_waitcnt vmcnt(10)
	v_cvt_pk_bf16_f32 v15, v14, v15
	v_cvt_pk_bf16_f32 v14, v12, v13
	v_mfma_f32_16x16x32_bf16 v[136:139], v[164:167], v[190:193], v[136:139]
	ds_write_b64 v174, v[14:15]
	v_mfma_f32_16x16x32_bf16 v[132:135], v[182:185], v[190:193], v[132:135]
	s_mov_b32 m0, s55
	s_nop 0
	buffer_load_dwordx4 v181, s[16:19], s4 offen lds
	v_mfma_f32_16x16x32_bf16 v[128:131], v[186:189], v[190:193], v[128:131]
	s_waitcnt lgkmcnt(2)
	v_mfma_f32_16x16x32_bf16 v[124:127], v[160:163], v[194:197], v[124:127]
	ds_read_b128 v[190:193], v175 offset:40960
	v_mfma_f32_16x16x32_bf16 v[120:123], v[164:167], v[194:197], v[120:123]
	v_mfma_f32_16x16x32_bf16 v[116:119], v[182:185], v[194:197], v[116:119]
	v_mfma_f32_16x16x32_bf16 v[112:115], v[186:189], v[194:197], v[112:115]
	s_waitcnt lgkmcnt(2)
	v_mfma_f32_16x16x32_bf16 v[108:111], v[160:163], v[168:171], v[108:111]
	ds_read_b128 v[194:197], v175 offset:43008
	buffer_load_dwordx4 v[12:15], v173, s[8:11], s5 offen
	s_waitcnt vmcnt(11)
	v_cvt_pk_bf16_f32 v31, v30, v31
	v_cvt_pk_bf16_f32 v30, v28, v29
	v_mfma_f32_16x16x32_bf16 v[104:107], v[164:167], v[168:171], v[104:107]
	ds_write_b64 v174, v[30:31] offset:8704
	v_mfma_f32_16x16x32_bf16 v[100:103], v[182:185], v[168:171], v[100:103]
	v_mfma_f32_16x16x32_bf16 v[96:99], v[186:189], v[168:171], v[96:99]
	s_add_i32 s20, s1, 0xfffc0000
	s_waitcnt lgkmcnt(2)
; #define G_DMA_A(kt, AO) do { G_DMA1(kt, AO, 0); G_DMA1(kt, AO, 1); G_DMA1(kt, AO, 2); G_DMA1(kt, AO, 3); if (MF == 9) G_DMA5(kt, AO); } while (0)
; #define G_ISSUE_B(kt) do { const unsigned _sb = (unsigned)(kt) * 4u * kstepB; \
;         _Pragma("unroll") for (int _i = 0; _i < 8; ++_i) sb[_i] = bload16(_i < 4 ? rsB0 : rsB1, vob, _sb + (_i & 3) * kstepB); } while (0)
; #define G_WRITE_B(BO) do { \
;         _Pragma("unroll") for (int _i = 0; _i < 8; ++_i) *(LAS u32x2*)(b_wr + (BO) + (_i & 3) * (16 * G_BSTRIDE) + (_i >> 2) * SLAB1) = pack4(__builtin_bit_cast(f32x4, sb[_i])); } while (0)
; #define G_ENDTILE(VM) do { asm volatile("s_waitcnt vmcnt(" #VM ")" ::: "memory"); \
;         asm volatile("s_waitcnt lgkmcnt(0)" ::: "memory"); __builtin_amdgcn_s_barrier(); asm volatile("" ::: "memory"); } while (0)
;     ...
;     __builtin_amdgcn_s_barrier();
;     G_DMA_A(0, G_A0); G_ISSUE_B(0); G_WRITE_B(G_B0);
;     __builtin_amdgcn_sched_barrier(0);
;     G_ISSUE_B(1);
;     __builtin_amdgcn_sched_barrier(0);
;     G_ENDTILE(8);
;     for (int ui = 0;; ++ui) {
; #pragma unroll
;         for (int m = 0; m < MF; ++m)
; #pragma unroll
;             for (int n = 0; n < 4; ++n) acc[m][n] = (f32x4){0.f, 0.f, 0.f, 0.f};
;         for (int t = 0; t < nt - 2; t += 2) {
;             G_TILE(G_A0, G_B0, true, G_B1, G_A1, t + 1, true, t + 2, (void)0);
;             G_ENDTILE(8);
;             G_TILE(G_A1, G_B1, true, G_B0, G_A0, t + 2, true, t + 3, (void)0);
;             G_ENDTILE(8);
;         }
	v_mfma_f32_16x16x32_bf16 v[92:95], v[160:163], v[190:193], v[92:95]
	ds_read_b128 v[168:171], v175 offset:45056
	v_mfma_f32_16x16x32_bf16 v[88:91], v[164:167], v[190:193], v[88:91]
	v_mfma_f32_16x16x32_bf16 v[84:87], v[182:185], v[190:193], v[84:87]
	v_mfma_f32_16x16x32_bf16 v[80:83], v[186:189], v[190:193], v[80:83]
	s_waitcnt lgkmcnt(2)
	v_mfma_f32_16x16x32_bf16 v[76:79], v[160:163], v[194:197], v[76:79]
	ds_read_b128 v[190:193], v175 offset:47104
	buffer_load_dwordx4 v[28:31], v173, s[8:11], s20 offen
	s_waitcnt vmcnt(11)
	v_cvt_pk_bf16_f32 v7, v6, v7
	v_cvt_pk_bf16_f32 v6, v4, v5
	v_mfma_f32_16x16x32_bf16 v[72:75], v[164:167], v[194:197], v[72:75]
	ds_write_b64 v174, v[6:7] offset:17408
	v_mfma_f32_16x16x32_bf16 v[68:71], v[182:185], v[194:197], v[68:71]
	v_mfma_f32_16x16x32_bf16 v[64:67], v[186:189], v[194:197], v[64:67]
	s_add_i32 s21, s1, 0xfffe0000
	s_waitcnt lgkmcnt(2)
	v_mfma_f32_16x16x32_bf16 v[60:63], v[160:163], v[168:171], v[60:63]
	ds_read_b128 v[194:197], v175 offset:33792
	v_mfma_f32_16x16x32_bf16 v[56:59], v[164:167], v[168:171], v[56:59]
	v_mfma_f32_16x16x32_bf16 v[52:55], v[182:185], v[168:171], v[52:55]
	v_mfma_f32_16x16x32_bf16 v[48:51], v[186:189], v[168:171], v[48:51]
	s_waitcnt lgkmcnt(2)
	v_mfma_f32_16x16x32_bf16 v[44:47], v[160:163], v[190:193], v[44:47]
	ds_read_b128 v[160:163], v175 offset:35840
	buffer_load_dwordx4 v[4:7], v173, s[8:11], s21 offen
	s_waitcnt vmcnt(11)
	v_cvt_pk_bf16_f32 v27, v26, v27
	v_cvt_pk_bf16_f32 v26, v24, v25
	v_mfma_f32_16x16x32_bf16 v[40:43], v[164:167], v[190:193], v[40:43]
	ds_read_b64_tr_b16 v[244:245], v178 offset:52224
	ds_read_b64_tr_b16 v[248:249], v178 offset:52256
	ds_read_b64_tr_b16 v[198:199], v178 offset:52288
	ds_read_b64_tr_b16 v[202:203], v178 offset:52320
	ds_read_b64_tr_b16 v[246:247], v179 offset:52224
	ds_read_b64_tr_b16 v[250:251], v179 offset:52256
	ds_read_b64_tr_b16 v[200:201], v179 offset:52288
	ds_read_b64_tr_b16 v[204:205], v179 offset:52320
	ds_write_b64 v174, v[26:27] offset:26112
	v_mfma_f32_16x16x32_bf16 v[36:39], v[182:185], v[190:193], v[36:39]
	v_mfma_f32_16x16x32_bf16 v[32:35], v[186:189], v[190:193], v[32:35]
	s_waitcnt lgkmcnt(4)
	v_mfma_f32_16x16x32_bf16 v[156:159], v[244:247], v[194:197], v[156:159]
	ds_read_b128 v[182:185], v175 offset:37888
	s_waitcnt lgkmcnt(4)
	v_mfma_f32_16x16x32_bf16 v[152:155], v[248:251], v[194:197], v[152:155]
	s_waitcnt lgkmcnt(3)
	v_mfma_f32_16x16x32_bf16 v[148:151], v[198:201], v[194:197], v[148:151]
	s_waitcnt lgkmcnt(2)
	v_mfma_f32_16x16x32_bf16 v[144:147], v[202:205], v[194:197], v[144:147]
	v_mfma_f32_16x16x32_bf16 v[140:143], v[244:247], v[160:163], v[140:143]
	ds_read_b128 v[186:189], v175 offset:39936
	buffer_load_dwordx4 v[24:27], v173, s[8:11], s1 offen
	s_waitcnt vmcnt(11)
	v_cvt_pk_bf16_f32 v23, v22, v23
	v_cvt_pk_bf16_f32 v22, v20, v21
	v_mfma_f32_16x16x32_bf16 v[136:139], v[248:251], v[160:163], v[136:139]
	ds_write_b64 v174, v[22:23] offset:256
	v_mfma_f32_16x16x32_bf16 v[132:135], v[198:201], v[160:163], v[132:135]
	v_mfma_f32_16x16x32_bf16 v[128:131], v[202:205], v[160:163], v[128:131]
	s_waitcnt lgkmcnt(2)
	v_mfma_f32_16x16x32_bf16 v[124:127], v[244:247], v[182:185], v[124:127]
	ds_read_b128 v[160:163], v175 offset:41984
	v_mfma_f32_16x16x32_bf16 v[120:123], v[248:251], v[182:185], v[120:123]
	v_mfma_f32_16x16x32_bf16 v[116:119], v[198:201], v[182:185], v[116:119]
	v_mfma_f32_16x16x32_bf16 v[112:115], v[202:205], v[182:185], v[112:115]
	s_waitcnt lgkmcnt(2)
	v_mfma_f32_16x16x32_bf16 v[108:111], v[244:247], v[186:189], v[108:111]
	ds_read_b128 v[182:185], v175 offset:44032
	buffer_load_dwordx4 v[20:23], v173, s[12:15], s5 offen
	s_waitcnt vmcnt(11)
	v_cvt_pk_bf16_f32 v11, v10, v11
	v_cvt_pk_bf16_f32 v10, v8, v9
	v_mfma_f32_16x16x32_bf16 v[104:107], v[248:251], v[186:189], v[104:107]
	ds_write_b64 v174, v[10:11] offset:8960
	v_mfma_f32_16x16x32_bf16 v[100:103], v[198:201], v[186:189], v[100:103]
	v_mfma_f32_16x16x32_bf16 v[96:99], v[202:205], v[186:189], v[96:99]
	s_waitcnt lgkmcnt(2)
	v_mfma_f32_16x16x32_bf16 v[92:95], v[244:247], v[160:163], v[92:95]
	ds_read_b128 v[186:189], v175 offset:46080
	v_mfma_f32_16x16x32_bf16 v[88:91], v[248:251], v[160:163], v[88:91]
	v_mfma_f32_16x16x32_bf16 v[84:87], v[198:201], v[160:163], v[84:87]
	v_mfma_f32_16x16x32_bf16 v[80:83], v[202:205], v[160:163], v[80:83]
	s_waitcnt lgkmcnt(2)
	v_mfma_f32_16x16x32_bf16 v[76:79], v[244:247], v[182:185], v[76:79]
	ds_read_b128 v[252:255], v175 offset:48128
	buffer_load_dwordx4 v[8:11], v173, s[12:15], s20 offen
	s_waitcnt vmcnt(11)
	v_cvt_pk_bf16_f32 v3, v2, v3
	v_cvt_pk_bf16_f32 v2, v0, v1
	v_mfma_f32_16x16x32_bf16 v[72:75], v[248:251], v[182:185], v[72:75]
	ds_write_b64 v174, v[2:3] offset:17664
	v_mfma_f32_16x16x32_bf16 v[68:71], v[198:201], v[182:185], v[68:71]
	v_mfma_f32_16x16x32_bf16 v[64:67], v[202:205], v[182:185], v[64:67]
	s_waitcnt lgkmcnt(2)
	v_mfma_f32_16x16x32_bf16 v[60:63], v[244:247], v[186:189], v[60:63]
	buffer_load_dwordx4 v[0:3], v173, s[12:15], s21 offen
	s_waitcnt vmcnt(11)
	v_cvt_pk_bf16_f32 v19, v18, v19
	v_cvt_pk_bf16_f32 v18, v16, v17
	v_mfma_f32_16x16x32_bf16 v[56:59], v[248:251], v[186:189], v[56:59]
	ds_write_b64 v174, v[18:19] offset:26368
	v_mfma_f32_16x16x32_bf16 v[52:55], v[198:201], v[186:189], v[52:55]
	buffer_load_dwordx4 v[16:19], v173, s[12:15], s1 offen
	v_mfma_f32_16x16x32_bf16 v[48:51], v[202:205], v[186:189], v[48:51]
	s_waitcnt vmcnt(8)
	s_waitcnt lgkmcnt(0)
	s_barrier
	s_add_i32 s0, s0, 2
	s_add_i32 s1, s1, 0x100000
	s_addk_i32 s4, 0x100
	s_cmp_ge_i32 s0, s60
	s_cbranch_scc1 .Lflush_P8
